# GEMM epilogue stores (P1 P3 P4 P7 P8) issued with sc1 (write-through, not kept in L2)
# baseline (speedup 1.0000x reference)
.LBB0_148:
	s_lshl_b32 s2, s52, 8
	s_and_b32 s52, s2, 0x300
	s_and_b64 s[50:51], s[28:29], exec
	s_cselect_b32 s50, s52, s2
	s_mov_b64 s[40:41], -1
	s_add_i32 s50, s50, s79
	s_andn2_b64 vcc, exec, s[46:47]
	s_ashr_i32 s46, s7, 31
	s_cbranch_vccz .LBB0_155
	s_xor_b64 s[42:43], s[42:43], -1
	s_and_b64 vcc, exec, s[42:43]
	s_cbranch_vccz .LBB0_151
	s_lshl_b32 s2, s38, 2
	v_mul_f32_e32 v6, 0xbd38aa3b, v191
	s_ashr_i32 s40, s50, 4
	s_add_i32 s42, s88, s2
	v_and_b32_e32 v3, 1, v50
	v_exp_f32_e32 v6, v6
	s_ashr_i32 s41, s40, 31
	s_ashr_i32 s43, s42, 31
	v_cmp_eq_u32_e32 vcc, 0, v3
	v_lshlrev_b32_e32 v3, 3, v50
	s_lshl_b64 s[40:41], s[40:41], 15
	s_lshl_b64 s[42:43], s[42:43], 10
	v_add_u32_e32 v4, 24, v3
	v_cndmask_b32_e32 v3, v4, v3, vcc
	s_add_u32 s2, s22, s40
	v_ashrrev_i32_e32 v4, 4, v3
	s_addc_u32 s38, s23, s41
	v_add_f32_e32 v6, 1.0, v6
	v_ashrrev_i32_e32 v5, 31, v4
	s_add_u32 s40, s2, s42
	v_rcp_f32_e32 v7, v6
	v_mul_f32_e32 v6, 0xbd38aa3b, v192
	v_lshlrev_b64 v[4:5], 8, v[4:5]
	s_addc_u32 s41, s38, s43
	v_exp_f32_e32 v6, v6
	v_ashrrev_i32_e32 v3, 31, v2
	v_lshl_add_u64 v[4:5], s[40:41], 0, v[4:5]
	v_lshl_add_u64 v[4:5], v[2:3], 4, v[4:5]
	v_mul_f32_e32 v3, 0xbd38aa3b, v190
	v_exp_f32_e32 v3, v3
	v_add_f32_e32 v6, 1.0, v6
	v_rcp_f32_e32 v8, v6
	v_mul_f32_e32 v6, 0xbd38aa3b, v193
	v_exp_f32_e32 v6, v6
	v_add_f32_e32 v3, 1.0, v3
	v_rcp_f32_e32 v3, v3
	s_mov_b32 s2, 0x8000
	v_add_f32_e32 v6, 1.0, v6
	v_rcp_f32_e32 v9, v6
	v_mov_b32_e32 v6, v199
	v_cvt_pk_fp8_f32 v6, v3, v7
	v_mul_f32_e32 v7, 0xbd38aa3b, v187
	v_exp_f32_e32 v7, v7
	v_mul_f32_e32 v3, 0xbd38aa3b, v186
	v_cvt_pk_fp8_f32 v6, v8, v9 op_sel:[0,0,1]
	v_exp_f32_e32 v3, v3
	v_add_f32_e32 v7, 1.0, v7
	v_rcp_f32_e32 v8, v7
	v_mul_f32_e32 v7, 0xbd38aa3b, v188
	v_exp_f32_e32 v7, v7
	v_add_f32_e32 v3, 1.0, v3
	v_rcp_f32_e32 v3, v3
	s_mov_b64 s[40:41], 0
	v_add_f32_e32 v7, 1.0, v7
	v_rcp_f32_e32 v9, v7
	v_mul_f32_e32 v7, 0xbd38aa3b, v189
	v_exp_f32_e32 v7, v7
	s_nop 0
	v_add_f32_e32 v7, 1.0, v7
	v_rcp_f32_e32 v10, v7
	v_mov_b32_e32 v7, v199
	v_cvt_pk_fp8_f32 v7, v3, v8
	v_mul_f32_e32 v8, 0xbd38aa3b, v183
	v_exp_f32_e32 v8, v8
	v_mul_f32_e32 v3, 0xbd38aa3b, v182
	v_cvt_pk_fp8_f32 v7, v9, v10 op_sel:[0,0,1]
	v_exp_f32_e32 v3, v3
	v_add_f32_e32 v8, 1.0, v8
	v_rcp_f32_e32 v9, v8
	v_mul_f32_e32 v8, 0xbd38aa3b, v184
	v_exp_f32_e32 v8, v8
	v_add_f32_e32 v3, 1.0, v3
	v_rcp_f32_e32 v3, v3
	v_add_f32_e32 v8, 1.0, v8
	v_rcp_f32_e32 v10, v8
	v_mul_f32_e32 v8, 0xbd38aa3b, v185
	v_exp_f32_e32 v8, v8
	s_nop 0
	v_add_f32_e32 v8, 1.0, v8
	v_rcp_f32_e32 v11, v8
	v_mov_b32_e32 v8, v199
	v_cvt_pk_fp8_f32 v8, v3, v9
	v_mul_f32_e32 v9, 0xbd38aa3b, v179
	v_exp_f32_e32 v9, v9
	v_mul_f32_e32 v3, 0xbd38aa3b, v178
	v_cvt_pk_fp8_f32 v8, v10, v11 op_sel:[0,0,1]
	v_exp_f32_e32 v3, v3
	v_add_f32_e32 v9, 1.0, v9
	v_rcp_f32_e32 v10, v9
	v_mul_f32_e32 v9, 0xbd38aa3b, v180
	v_exp_f32_e32 v9, v9
	v_add_f32_e32 v3, 1.0, v3
	v_rcp_f32_e32 v3, v3
	v_permlane16_swap_b32_e32 v6, v8
	v_add_f32_e32 v9, 1.0, v9
	v_rcp_f32_e32 v11, v9
	v_mul_f32_e32 v9, 0xbd38aa3b, v181
	v_exp_f32_e32 v9, v9
	s_nop 0
	v_add_f32_e32 v9, 1.0, v9
	v_rcp_f32_e32 v12, v9
	v_mov_b32_e32 v9, v199
	v_cvt_pk_fp8_f32 v9, v3, v10
	v_mul_f32_e32 v3, 0xbd38aa3b, v174
	v_exp_f32_e32 v3, v3
	v_cvt_pk_fp8_f32 v9, v11, v12 op_sel:[0,0,1]
	v_add_f32_e32 v3, 1.0, v3
	v_rcp_f32_e32 v3, v3
	v_permlane16_swap_b32_e32 v7, v9
	global_store_dwordx4 v[4:5], v[6:9], off sc1
	s_nop 1
	v_mul_f32_e32 v6, 0xbd38aa3b, v175
	v_exp_f32_e32 v6, v6
	s_nop 0
	v_add_f32_e32 v6, 1.0, v6
	v_rcp_f32_e32 v7, v6
	v_mul_f32_e32 v6, 0xbd38aa3b, v176
	v_exp_f32_e32 v6, v6
	s_nop 0
	v_add_f32_e32 v6, 1.0, v6
	v_rcp_f32_e32 v8, v6
	v_mul_f32_e32 v6, 0xbd38aa3b, v177
	v_exp_f32_e32 v6, v6
	s_nop 0
	v_add_f32_e32 v6, 1.0, v6
	v_rcp_f32_e32 v9, v6
	v_mov_b32_e32 v6, v199
	v_cvt_pk_fp8_f32 v6, v3, v7
	v_mul_f32_e32 v7, 0xbd38aa3b, v171
	v_exp_f32_e32 v7, v7
	v_mul_f32_e32 v3, 0xbd38aa3b, v170
	v_cvt_pk_fp8_f32 v6, v8, v9 op_sel:[0,0,1]
	v_exp_f32_e32 v3, v3
	v_add_f32_e32 v7, 1.0, v7
	v_rcp_f32_e32 v8, v7
	v_mul_f32_e32 v7, 0xbd38aa3b, v172
	v_exp_f32_e32 v7, v7
	v_add_f32_e32 v3, 1.0, v3
	v_rcp_f32_e32 v3, v3
	v_add_f32_e32 v7, 1.0, v7
	v_rcp_f32_e32 v9, v7
	v_mul_f32_e32 v7, 0xbd38aa3b, v173
	v_exp_f32_e32 v7, v7
	s_nop 0
	v_add_f32_e32 v7, 1.0, v7
	v_rcp_f32_e32 v10, v7
	v_mov_b32_e32 v7, v199
	v_cvt_pk_fp8_f32 v7, v3, v8
	v_mul_f32_e32 v8, 0xbd38aa3b, v167
	v_exp_f32_e32 v8, v8
	v_mul_f32_e32 v3, 0xbd38aa3b, v166
	v_cvt_pk_fp8_f32 v7, v9, v10 op_sel:[0,0,1]
	v_exp_f32_e32 v3, v3
	v_add_f32_e32 v8, 1.0, v8
	v_rcp_f32_e32 v9, v8
	v_mul_f32_e32 v8, 0xbd38aa3b, v168
	v_exp_f32_e32 v8, v8
	v_add_f32_e32 v3, 1.0, v3
	v_rcp_f32_e32 v3, v3
	v_add_f32_e32 v8, 1.0, v8
	v_rcp_f32_e32 v10, v8
	v_mul_f32_e32 v8, 0xbd38aa3b, v169
	v_exp_f32_e32 v8, v8
	s_nop 0
	v_add_f32_e32 v8, 1.0, v8
	v_rcp_f32_e32 v11, v8
	v_mov_b32_e32 v8, v199
	v_cvt_pk_fp8_f32 v8, v3, v9
	v_mul_f32_e32 v9, 0xbd38aa3b, v163
	v_exp_f32_e32 v9, v9
	v_mul_f32_e32 v3, 0xbd38aa3b, v162
	v_cvt_pk_fp8_f32 v8, v10, v11 op_sel:[0,0,1]
	v_exp_f32_e32 v3, v3
	v_add_f32_e32 v9, 1.0, v9
	v_rcp_f32_e32 v10, v9
	v_mul_f32_e32 v9, 0xbd38aa3b, v164
	v_exp_f32_e32 v9, v9
	v_add_f32_e32 v3, 1.0, v3
	v_rcp_f32_e32 v3, v3
	v_permlane16_swap_b32_e32 v6, v8
	v_add_f32_e32 v9, 1.0, v9
	v_rcp_f32_e32 v11, v9
	v_mul_f32_e32 v9, 0xbd38aa3b, v165
	v_exp_f32_e32 v9, v9
	s_nop 0
	v_add_f32_e32 v9, 1.0, v9
	v_rcp_f32_e32 v12, v9
	v_mov_b32_e32 v9, v199
	v_cvt_pk_fp8_f32 v9, v3, v10
	v_add_co_u32_e32 v10, vcc, s2, v4
	v_mul_f32_e32 v3, 0xbd38aa3b, v158
	v_cvt_pk_fp8_f32 v9, v11, v12 op_sel:[0,0,1]
	v_addc_co_u32_e32 v11, vcc, 0, v5, vcc
	v_exp_f32_e32 v3, v3
	v_permlane16_swap_b32_e32 v7, v9
	global_store_dwordx4 v[10:11], v[6:9], off sc1
	v_add_f32_e32 v3, 1.0, v3
	v_rcp_f32_e32 v3, v3
	v_mul_f32_e32 v6, 0xbd38aa3b, v159
	v_exp_f32_e32 v6, v6
	s_mov_b32 s2, 0x10000
	v_add_f32_e32 v6, 1.0, v6
	v_rcp_f32_e32 v7, v6
	v_mul_f32_e32 v6, 0xbd38aa3b, v160
	v_exp_f32_e32 v6, v6
	s_nop 0
	v_add_f32_e32 v6, 1.0, v6
	v_rcp_f32_e32 v8, v6
	v_mul_f32_e32 v6, 0xbd38aa3b, v161
	v_exp_f32_e32 v6, v6
	s_nop 0
	v_add_f32_e32 v6, 1.0, v6
	v_rcp_f32_e32 v9, v6
	v_mov_b32_e32 v6, v199
	v_cvt_pk_fp8_f32 v6, v3, v7
	v_mul_f32_e32 v7, 0xbd38aa3b, v155
	v_exp_f32_e32 v7, v7
	v_mul_f32_e32 v3, 0xbd38aa3b, v154
	v_cvt_pk_fp8_f32 v6, v8, v9 op_sel:[0,0,1]
	v_exp_f32_e32 v3, v3
	v_add_f32_e32 v7, 1.0, v7
	v_rcp_f32_e32 v8, v7
	v_mul_f32_e32 v7, 0xbd38aa3b, v156
	v_exp_f32_e32 v7, v7
	v_add_f32_e32 v3, 1.0, v3
	v_rcp_f32_e32 v3, v3
	v_add_f32_e32 v7, 1.0, v7
	v_rcp_f32_e32 v9, v7
	v_mul_f32_e32 v7, 0xbd38aa3b, v157
	v_exp_f32_e32 v7, v7
	s_nop 0
	v_add_f32_e32 v7, 1.0, v7
	v_rcp_f32_e32 v10, v7
	v_mov_b32_e32 v7, v199
	v_cvt_pk_fp8_f32 v7, v3, v8
	v_mul_f32_e32 v8, 0xbd38aa3b, v151
	v_exp_f32_e32 v8, v8
	v_mul_f32_e32 v3, 0xbd38aa3b, v150
	v_cvt_pk_fp8_f32 v7, v9, v10 op_sel:[0,0,1]
	v_exp_f32_e32 v3, v3
	v_add_f32_e32 v8, 1.0, v8
	v_rcp_f32_e32 v9, v8
	v_mul_f32_e32 v8, 0xbd38aa3b, v152
	v_exp_f32_e32 v8, v8
	v_add_f32_e32 v3, 1.0, v3
	v_rcp_f32_e32 v3, v3
	v_add_f32_e32 v8, 1.0, v8
	v_rcp_f32_e32 v10, v8
	v_mul_f32_e32 v8, 0xbd38aa3b, v153
	v_exp_f32_e32 v8, v8
	s_nop 0
	v_add_f32_e32 v8, 1.0, v8
	v_rcp_f32_e32 v11, v8
	v_mov_b32_e32 v8, v199
	v_cvt_pk_fp8_f32 v8, v3, v9
	v_mul_f32_e32 v9, 0xbd38aa3b, v147
	v_exp_f32_e32 v9, v9
	v_mul_f32_e32 v3, 0xbd38aa3b, v146
	v_cvt_pk_fp8_f32 v8, v10, v11 op_sel:[0,0,1]
	v_exp_f32_e32 v3, v3
	v_add_f32_e32 v9, 1.0, v9
	v_rcp_f32_e32 v10, v9
	v_mul_f32_e32 v9, 0xbd38aa3b, v148
	v_exp_f32_e32 v9, v9
	v_add_f32_e32 v3, 1.0, v3
	v_rcp_f32_e32 v3, v3
	v_permlane16_swap_b32_e32 v6, v8
	v_add_f32_e32 v9, 1.0, v9
	v_rcp_f32_e32 v11, v9
	v_mul_f32_e32 v9, 0xbd38aa3b, v149
	v_exp_f32_e32 v9, v9
	s_nop 0
	v_add_f32_e32 v9, 1.0, v9
	v_rcp_f32_e32 v12, v9
	v_mov_b32_e32 v9, v199
	v_cvt_pk_fp8_f32 v9, v3, v10
	v_add_co_u32_e32 v10, vcc, s2, v4
	v_mul_f32_e32 v3, 0xbd38aa3b, v142
	v_cvt_pk_fp8_f32 v9, v11, v12 op_sel:[0,0,1]
	v_addc_co_u32_e32 v11, vcc, 0, v5, vcc
	v_exp_f32_e32 v3, v3
	v_permlane16_swap_b32_e32 v7, v9
	global_store_dwordx4 v[10:11], v[6:9], off sc1
	v_add_f32_e32 v3, 1.0, v3
	v_rcp_f32_e32 v3, v3
	v_mul_f32_e32 v6, 0xbd38aa3b, v143
	v_exp_f32_e32 v6, v6
	s_mov_b32 s2, 0x18000
	v_add_f32_e32 v6, 1.0, v6
	v_rcp_f32_e32 v7, v6
	v_mul_f32_e32 v6, 0xbd38aa3b, v144
	v_exp_f32_e32 v6, v6
	s_nop 0
	v_add_f32_e32 v6, 1.0, v6
	v_rcp_f32_e32 v8, v6
	v_mul_f32_e32 v6, 0xbd38aa3b, v145
	v_exp_f32_e32 v6, v6
	s_nop 0
	v_add_f32_e32 v6, 1.0, v6
	v_rcp_f32_e32 v9, v6
	v_mov_b32_e32 v6, v199
	v_cvt_pk_fp8_f32 v6, v3, v7
	v_mul_f32_e32 v7, 0xbd38aa3b, v139
	v_exp_f32_e32 v7, v7
	v_mul_f32_e32 v3, 0xbd38aa3b, v138
	v_cvt_pk_fp8_f32 v6, v8, v9 op_sel:[0,0,1]
	v_exp_f32_e32 v3, v3
	v_add_f32_e32 v7, 1.0, v7
	v_rcp_f32_e32 v8, v7
	v_mul_f32_e32 v7, 0xbd38aa3b, v140
	v_exp_f32_e32 v7, v7
	v_add_f32_e32 v3, 1.0, v3
	v_rcp_f32_e32 v3, v3
	v_add_f32_e32 v7, 1.0, v7
	v_rcp_f32_e32 v9, v7
	v_mul_f32_e32 v7, 0xbd38aa3b, v141
	v_exp_f32_e32 v7, v7
	s_nop 0
	v_add_f32_e32 v7, 1.0, v7
	v_rcp_f32_e32 v10, v7
	v_mov_b32_e32 v7, v199
	v_cvt_pk_fp8_f32 v7, v3, v8
	v_mul_f32_e32 v8, 0xbd38aa3b, v135
	v_exp_f32_e32 v8, v8
	v_mul_f32_e32 v3, 0xbd38aa3b, v134
	v_cvt_pk_fp8_f32 v7, v9, v10 op_sel:[0,0,1]
	v_exp_f32_e32 v3, v3
	v_add_f32_e32 v8, 1.0, v8
	v_rcp_f32_e32 v9, v8
	v_mul_f32_e32 v8, 0xbd38aa3b, v136
	v_exp_f32_e32 v8, v8
	v_add_f32_e32 v3, 1.0, v3
	v_rcp_f32_e32 v3, v3
	v_add_f32_e32 v8, 1.0, v8
	v_rcp_f32_e32 v10, v8
	v_mul_f32_e32 v8, 0xbd38aa3b, v137
	v_exp_f32_e32 v8, v8
	s_nop 0
	v_add_f32_e32 v8, 1.0, v8
	v_rcp_f32_e32 v11, v8
	v_mov_b32_e32 v8, v199
	v_cvt_pk_fp8_f32 v8, v3, v9
	v_mul_f32_e32 v9, 0xbd38aa3b, v131
	v_exp_f32_e32 v9, v9
	v_mul_f32_e32 v3, 0xbd38aa3b, v130
	v_cvt_pk_fp8_f32 v8, v10, v11 op_sel:[0,0,1]
	v_exp_f32_e32 v3, v3
	v_add_f32_e32 v9, 1.0, v9
	v_rcp_f32_e32 v10, v9
	v_mul_f32_e32 v9, 0xbd38aa3b, v132
	v_exp_f32_e32 v9, v9
	v_add_f32_e32 v3, 1.0, v3
	v_rcp_f32_e32 v3, v3
	v_permlane16_swap_b32_e32 v6, v8
	v_add_f32_e32 v9, 1.0, v9
	v_rcp_f32_e32 v11, v9
	v_mul_f32_e32 v9, 0xbd38aa3b, v133
	v_exp_f32_e32 v9, v9
	s_nop 0
	v_add_f32_e32 v9, 1.0, v9
	v_rcp_f32_e32 v12, v9
	v_mov_b32_e32 v9, v199
	v_cvt_pk_fp8_f32 v9, v3, v10
	v_add_co_u32_e32 v10, vcc, s2, v4
	v_mul_f32_e32 v3, 0xbd38aa3b, v126
	v_cvt_pk_fp8_f32 v9, v11, v12 op_sel:[0,0,1]
	v_addc_co_u32_e32 v11, vcc, 0, v5, vcc
	v_exp_f32_e32 v3, v3
	v_permlane16_swap_b32_e32 v7, v9
	global_store_dwordx4 v[10:11], v[6:9], off sc1
	v_add_f32_e32 v3, 1.0, v3
	v_rcp_f32_e32 v3, v3
	v_mul_f32_e32 v6, 0xbd38aa3b, v127
	v_exp_f32_e32 v6, v6
	s_mov_b32 s2, 0x40000
	v_add_f32_e32 v6, 1.0, v6
	v_rcp_f32_e32 v7, v6
	v_mul_f32_e32 v6, 0xbd38aa3b, v128
	v_exp_f32_e32 v6, v6
	s_nop 0
	v_add_f32_e32 v6, 1.0, v6
	v_rcp_f32_e32 v8, v6
	v_mul_f32_e32 v6, 0xbd38aa3b, v129
	v_exp_f32_e32 v6, v6
	s_nop 0
	v_add_f32_e32 v6, 1.0, v6
	v_rcp_f32_e32 v9, v6
	v_mov_b32_e32 v6, v199
	v_cvt_pk_fp8_f32 v6, v3, v7
	v_mul_f32_e32 v7, 0xbd38aa3b, v123
	v_exp_f32_e32 v7, v7
	v_mul_f32_e32 v3, 0xbd38aa3b, v122
	v_cvt_pk_fp8_f32 v6, v8, v9 op_sel:[0,0,1]
	v_exp_f32_e32 v3, v3
	v_add_f32_e32 v7, 1.0, v7
	v_rcp_f32_e32 v8, v7
	v_mul_f32_e32 v7, 0xbd38aa3b, v124
	v_exp_f32_e32 v7, v7
	v_add_f32_e32 v3, 1.0, v3
	v_rcp_f32_e32 v3, v3
	v_add_f32_e32 v7, 1.0, v7
	v_rcp_f32_e32 v9, v7
	v_mul_f32_e32 v7, 0xbd38aa3b, v125
	v_exp_f32_e32 v7, v7
	s_nop 0
	v_add_f32_e32 v7, 1.0, v7
	v_rcp_f32_e32 v10, v7
	v_mov_b32_e32 v7, v199
	v_cvt_pk_fp8_f32 v7, v3, v8
	v_mul_f32_e32 v8, 0xbd38aa3b, v119
	v_exp_f32_e32 v8, v8
	v_mul_f32_e32 v3, 0xbd38aa3b, v118
	v_cvt_pk_fp8_f32 v7, v9, v10 op_sel:[0,0,1]
	v_exp_f32_e32 v3, v3
	v_add_f32_e32 v8, 1.0, v8
	v_rcp_f32_e32 v9, v8
	v_mul_f32_e32 v8, 0xbd38aa3b, v120
	v_exp_f32_e32 v8, v8
	v_add_f32_e32 v3, 1.0, v3
	v_rcp_f32_e32 v3, v3
	v_add_f32_e32 v8, 1.0, v8
	v_rcp_f32_e32 v10, v8
	v_mul_f32_e32 v8, 0xbd38aa3b, v121
	v_exp_f32_e32 v8, v8
	s_nop 0
	v_add_f32_e32 v8, 1.0, v8
	v_rcp_f32_e32 v11, v8
	v_mov_b32_e32 v8, v199
	v_cvt_pk_fp8_f32 v8, v3, v9
	v_mul_f32_e32 v9, 0xbd38aa3b, v115
	v_exp_f32_e32 v9, v9
	v_mul_f32_e32 v3, 0xbd38aa3b, v114
	v_cvt_pk_fp8_f32 v8, v10, v11 op_sel:[0,0,1]
	v_exp_f32_e32 v3, v3
	v_add_f32_e32 v9, 1.0, v9
	v_rcp_f32_e32 v10, v9
	v_mul_f32_e32 v9, 0xbd38aa3b, v116
	v_exp_f32_e32 v9, v9
	v_add_f32_e32 v3, 1.0, v3
	v_rcp_f32_e32 v3, v3
	v_permlane16_swap_b32_e32 v6, v8
	v_add_f32_e32 v9, 1.0, v9
	v_rcp_f32_e32 v11, v9
	v_mul_f32_e32 v9, 0xbd38aa3b, v117
	v_exp_f32_e32 v9, v9
	s_nop 0
	v_add_f32_e32 v9, 1.0, v9
	v_rcp_f32_e32 v12, v9
	v_mov_b32_e32 v9, v199
	v_cvt_pk_fp8_f32 v9, v3, v10
	v_add_co_u32_e32 v10, vcc, s2, v4
	v_mul_f32_e32 v3, 0xbd38aa3b, v110
	v_cvt_pk_fp8_f32 v9, v11, v12 op_sel:[0,0,1]
	v_addc_co_u32_e32 v11, vcc, 0, v5, vcc
	v_exp_f32_e32 v3, v3
	v_permlane16_swap_b32_e32 v7, v9
	global_store_dwordx4 v[10:11], v[6:9], off sc1
	v_add_f32_e32 v3, 1.0, v3
	v_rcp_f32_e32 v3, v3
	v_mul_f32_e32 v6, 0xbd38aa3b, v111
	v_exp_f32_e32 v6, v6
	s_mov_b32 s2, 0x48000
	v_add_f32_e32 v6, 1.0, v6
	v_rcp_f32_e32 v7, v6
	v_mul_f32_e32 v6, 0xbd38aa3b, v112
	v_exp_f32_e32 v6, v6
	s_nop 0
	v_add_f32_e32 v6, 1.0, v6
	v_rcp_f32_e32 v8, v6
	v_mul_f32_e32 v6, 0xbd38aa3b, v113
	v_exp_f32_e32 v6, v6
	s_nop 0
	v_add_f32_e32 v6, 1.0, v6
	v_rcp_f32_e32 v9, v6
	v_mov_b32_e32 v6, v199
	v_cvt_pk_fp8_f32 v6, v3, v7
	v_mul_f32_e32 v7, 0xbd38aa3b, v107
	v_exp_f32_e32 v7, v7
	v_mul_f32_e32 v3, 0xbd38aa3b, v106
	v_cvt_pk_fp8_f32 v6, v8, v9 op_sel:[0,0,1]
	v_exp_f32_e32 v3, v3
	v_add_f32_e32 v7, 1.0, v7
	v_rcp_f32_e32 v8, v7
	v_mul_f32_e32 v7, 0xbd38aa3b, v108
	v_exp_f32_e32 v7, v7
	v_add_f32_e32 v3, 1.0, v3
	v_rcp_f32_e32 v3, v3
	v_add_f32_e32 v7, 1.0, v7
	v_rcp_f32_e32 v9, v7
	v_mul_f32_e32 v7, 0xbd38aa3b, v109
	v_exp_f32_e32 v7, v7
	s_nop 0
	v_add_f32_e32 v7, 1.0, v7
	v_rcp_f32_e32 v10, v7
	v_mov_b32_e32 v7, v199
	v_cvt_pk_fp8_f32 v7, v3, v8
	v_mul_f32_e32 v8, 0xbd38aa3b, v95
	v_exp_f32_e32 v8, v8
	v_mul_f32_e32 v3, 0xbd38aa3b, v94
	v_cvt_pk_fp8_f32 v7, v9, v10 op_sel:[0,0,1]
	v_exp_f32_e32 v3, v3
	v_add_f32_e32 v8, 1.0, v8
	v_rcp_f32_e32 v9, v8
	v_mul_f32_e32 v8, 0xbd38aa3b, v96
	v_exp_f32_e32 v8, v8
	v_add_f32_e32 v3, 1.0, v3
	v_rcp_f32_e32 v3, v3
	v_add_f32_e32 v8, 1.0, v8
	v_rcp_f32_e32 v10, v8
	v_mul_f32_e32 v8, 0xbd38aa3b, v97
	v_exp_f32_e32 v8, v8
	s_nop 0
	v_add_f32_e32 v8, 1.0, v8
	v_rcp_f32_e32 v11, v8
	v_mov_b32_e32 v8, v199
	v_cvt_pk_fp8_f32 v8, v3, v9
	v_mul_f32_e32 v9, 0xbd38aa3b, v91
	v_exp_f32_e32 v9, v9
	v_mul_f32_e32 v3, 0xbd38aa3b, v90
	v_cvt_pk_fp8_f32 v8, v10, v11 op_sel:[0,0,1]
	v_exp_f32_e32 v3, v3
	v_add_f32_e32 v9, 1.0, v9
	v_rcp_f32_e32 v10, v9
	v_mul_f32_e32 v9, 0xbd38aa3b, v92
	v_exp_f32_e32 v9, v9
	v_add_f32_e32 v3, 1.0, v3
	v_rcp_f32_e32 v3, v3
	v_permlane16_swap_b32_e32 v6, v8
	v_add_f32_e32 v9, 1.0, v9
	v_rcp_f32_e32 v11, v9
	v_mul_f32_e32 v9, 0xbd38aa3b, v93
	v_exp_f32_e32 v9, v9
	s_nop 0
	v_add_f32_e32 v9, 1.0, v9
	v_rcp_f32_e32 v12, v9
	v_mov_b32_e32 v9, v199
	v_cvt_pk_fp8_f32 v9, v3, v10
	v_add_co_u32_e32 v10, vcc, s2, v4
	v_mul_f32_e32 v3, 0xbd38aa3b, v78
	v_cvt_pk_fp8_f32 v9, v11, v12 op_sel:[0,0,1]
	v_addc_co_u32_e32 v11, vcc, 0, v5, vcc
	v_exp_f32_e32 v3, v3
	v_permlane16_swap_b32_e32 v7, v9
	global_store_dwordx4 v[10:11], v[6:9], off sc1
	v_add_f32_e32 v3, 1.0, v3
	v_rcp_f32_e32 v3, v3
	v_mul_f32_e32 v6, 0xbd38aa3b, v79
	v_exp_f32_e32 v6, v6
	s_mov_b32 s2, 0x50000
	v_add_f32_e32 v6, 1.0, v6
	v_rcp_f32_e32 v7, v6
	v_mul_f32_e32 v6, 0xbd38aa3b, v80
	v_exp_f32_e32 v6, v6
	s_nop 0
	v_add_f32_e32 v6, 1.0, v6
	v_rcp_f32_e32 v8, v6
	v_mul_f32_e32 v6, 0xbd38aa3b, v81
	v_exp_f32_e32 v6, v6
	s_nop 0
	v_add_f32_e32 v6, 1.0, v6
	v_rcp_f32_e32 v9, v6
	v_mov_b32_e32 v6, v199
	v_cvt_pk_fp8_f32 v6, v3, v7
	v_mul_f32_e32 v7, 0xbd38aa3b, v75
	v_exp_f32_e32 v7, v7
	v_mul_f32_e32 v3, 0xbd38aa3b, v74
	v_cvt_pk_fp8_f32 v6, v8, v9 op_sel:[0,0,1]
	v_exp_f32_e32 v3, v3
	v_add_f32_e32 v7, 1.0, v7
	v_rcp_f32_e32 v8, v7
	v_mul_f32_e32 v7, 0xbd38aa3b, v76
	v_exp_f32_e32 v7, v7
	v_add_f32_e32 v3, 1.0, v3
	v_rcp_f32_e32 v3, v3
	v_add_f32_e32 v7, 1.0, v7
	v_rcp_f32_e32 v9, v7
	v_mul_f32_e32 v7, 0xbd38aa3b, v77
	v_exp_f32_e32 v7, v7
	s_nop 0
	v_add_f32_e32 v7, 1.0, v7
	v_rcp_f32_e32 v10, v7
	v_mov_b32_e32 v7, v199
	v_cvt_pk_fp8_f32 v7, v3, v8
	v_mul_f32_e32 v8, 0xbd38aa3b, v99
	v_exp_f32_e32 v8, v8
	v_mul_f32_e32 v3, 0xbd38aa3b, v98
	v_cvt_pk_fp8_f32 v7, v9, v10 op_sel:[0,0,1]
	v_exp_f32_e32 v3, v3
	v_add_f32_e32 v8, 1.0, v8
	v_rcp_f32_e32 v9, v8
	v_mul_f32_e32 v8, 0xbd38aa3b, v100
	v_exp_f32_e32 v8, v8
	v_add_f32_e32 v3, 1.0, v3
	v_rcp_f32_e32 v3, v3
	v_add_f32_e32 v8, 1.0, v8
	v_rcp_f32_e32 v10, v8
	v_mul_f32_e32 v8, 0xbd38aa3b, v101
	v_exp_f32_e32 v8, v8
	s_nop 0
	v_add_f32_e32 v8, 1.0, v8
	v_rcp_f32_e32 v11, v8
	v_mov_b32_e32 v8, v199
	v_cvt_pk_fp8_f32 v8, v3, v9
	v_mul_f32_e32 v9, 0xbd38aa3b, v103
	v_exp_f32_e32 v9, v9
	v_mul_f32_e32 v3, 0xbd38aa3b, v102
	v_cvt_pk_fp8_f32 v8, v10, v11 op_sel:[0,0,1]
	v_exp_f32_e32 v3, v3
	v_add_f32_e32 v9, 1.0, v9
	v_rcp_f32_e32 v10, v9
	v_mul_f32_e32 v9, 0xbd38aa3b, v104
	v_exp_f32_e32 v9, v9
	v_add_f32_e32 v3, 1.0, v3
	v_rcp_f32_e32 v3, v3
	v_permlane16_swap_b32_e32 v6, v8
	v_add_f32_e32 v9, 1.0, v9
	v_rcp_f32_e32 v11, v9
	v_mul_f32_e32 v9, 0xbd38aa3b, v105
	v_exp_f32_e32 v9, v9
	s_nop 0
	v_add_f32_e32 v9, 1.0, v9
	v_rcp_f32_e32 v12, v9
	v_mov_b32_e32 v9, v199
	v_cvt_pk_fp8_f32 v9, v3, v10
	v_add_co_u32_e32 v10, vcc, s2, v4
	v_mul_f32_e32 v3, 0xbd38aa3b, v70
	v_cvt_pk_fp8_f32 v9, v11, v12 op_sel:[0,0,1]
	v_addc_co_u32_e32 v11, vcc, 0, v5, vcc
	v_exp_f32_e32 v3, v3
	v_permlane16_swap_b32_e32 v7, v9
	global_store_dwordx4 v[10:11], v[6:9], off sc1
	v_add_f32_e32 v3, 1.0, v3
	v_rcp_f32_e32 v3, v3
	v_mul_f32_e32 v6, 0xbd38aa3b, v71
	v_exp_f32_e32 v6, v6
	v_add_co_u32_e32 v4, vcc, 0x58000, v4
	v_add_f32_e32 v6, 1.0, v6
	v_rcp_f32_e32 v7, v6
	v_mul_f32_e32 v6, 0xbd38aa3b, v72
	v_exp_f32_e32 v6, v6
	v_addc_co_u32_e32 v5, vcc, 0, v5, vcc
	v_add_f32_e32 v6, 1.0, v6
	v_rcp_f32_e32 v8, v6
	v_mul_f32_e32 v6, 0xbd38aa3b, v73
	v_exp_f32_e32 v6, v6
	s_nop 0
	v_add_f32_e32 v6, 1.0, v6
	v_rcp_f32_e32 v9, v6
	v_mov_b32_e32 v6, v199
	v_cvt_pk_fp8_f32 v6, v3, v7
	v_mul_f32_e32 v7, 0xbd38aa3b, v67
	v_exp_f32_e32 v7, v7
	v_mul_f32_e32 v3, 0xbd38aa3b, v66
	v_cvt_pk_fp8_f32 v6, v8, v9 op_sel:[0,0,1]
	v_exp_f32_e32 v3, v3
	v_add_f32_e32 v7, 1.0, v7
	v_rcp_f32_e32 v8, v7
	v_mul_f32_e32 v7, 0xbd38aa3b, v68
	v_exp_f32_e32 v7, v7
	v_add_f32_e32 v3, 1.0, v3
	v_rcp_f32_e32 v3, v3
	v_add_f32_e32 v7, 1.0, v7
	v_rcp_f32_e32 v9, v7
	v_mul_f32_e32 v7, 0xbd38aa3b, v69
	v_exp_f32_e32 v7, v7
	s_nop 0
	v_add_f32_e32 v7, 1.0, v7
	v_rcp_f32_e32 v10, v7
	v_mov_b32_e32 v7, v199
	v_cvt_pk_fp8_f32 v7, v3, v8
	v_mul_f32_e32 v8, 0xbd38aa3b, v83
	v_exp_f32_e32 v8, v8
	v_mul_f32_e32 v3, 0xbd38aa3b, v82
	v_cvt_pk_fp8_f32 v7, v9, v10 op_sel:[0,0,1]
	v_exp_f32_e32 v3, v3
	v_add_f32_e32 v8, 1.0, v8
	v_rcp_f32_e32 v9, v8
	v_mul_f32_e32 v8, 0xbd38aa3b, v84
	v_exp_f32_e32 v8, v8
	v_add_f32_e32 v3, 1.0, v3
	v_rcp_f32_e32 v3, v3
	v_add_f32_e32 v8, 1.0, v8
	v_rcp_f32_e32 v10, v8
	v_mul_f32_e32 v8, 0xbd38aa3b, v85
	v_exp_f32_e32 v8, v8
	s_nop 0
	v_add_f32_e32 v8, 1.0, v8
	v_rcp_f32_e32 v11, v8
	v_mov_b32_e32 v8, v199
	v_cvt_pk_fp8_f32 v8, v3, v9
	v_mul_f32_e32 v9, 0xbd38aa3b, v87
	v_exp_f32_e32 v9, v9
	v_mul_f32_e32 v3, 0xbd38aa3b, v86
	v_cvt_pk_fp8_f32 v8, v10, v11 op_sel:[0,0,1]
	v_exp_f32_e32 v3, v3
	v_add_f32_e32 v9, 1.0, v9
	v_rcp_f32_e32 v10, v9
	v_mul_f32_e32 v9, 0xbd38aa3b, v88
	v_exp_f32_e32 v9, v9
	v_add_f32_e32 v3, 1.0, v3
	v_rcp_f32_e32 v3, v3
	v_permlane16_swap_b32_e32 v6, v8
	v_add_f32_e32 v9, 1.0, v9
	v_rcp_f32_e32 v11, v9
	v_mul_f32_e32 v9, 0xbd38aa3b, v89
	v_exp_f32_e32 v9, v9
	s_nop 0
	v_add_f32_e32 v9, 1.0, v9
	v_rcp_f32_e32 v12, v9
	v_mov_b32_e32 v9, v199
	v_cvt_pk_fp8_f32 v9, v3, v10
	v_cvt_pk_fp8_f32 v9, v11, v12 op_sel:[0,0,1]
	s_nop 1
	v_permlane16_swap_b32_e32 v7, v9
	global_store_dwordx4 v[4:5], v[6:9], off sc1
.LBB0_151:
	s_andn2_b64 vcc, exec, s[40:41]
	s_cbranch_vccnz .LBB0_153
	v_pk_mul_f32 v[8:9], v[190:191], s[36:37] op_sel_hi:[1,0]
	v_pk_mul_f32 v[10:11], v[186:187], s[36:37] op_sel_hi:[1,0]
	v_mov_b32_e32 v6, v199
	v_mov_b32_e32 v7, v199
	v_cvt_pk_fp8_f32 v6, v8, v9
	v_cvt_pk_fp8_f32 v7, v10, v11
	v_pk_mul_f32 v[8:9], v[192:193], s[36:37] op_sel_hi:[1,0]
	v_pk_mul_f32 v[10:11], v[188:189], s[36:37] op_sel_hi:[1,0]
	v_cvt_pk_fp8_f32 v6, v8, v9 op_sel:[0,0,1]
	v_cvt_pk_fp8_f32 v7, v10, v11 op_sel:[0,0,1]
	v_pk_mul_f32 v[10:11], v[182:183], s[36:37] op_sel_hi:[1,0]
	v_pk_mul_f32 v[12:13], v[178:179], s[36:37] op_sel_hi:[1,0]
	v_mov_b32_e32 v8, v199
	v_mov_b32_e32 v9, v199
	v_cvt_pk_fp8_f32 v8, v10, v11
	v_cvt_pk_fp8_f32 v9, v12, v13
	s_add_u32 s2, s62, s7
	v_and_b32_e32 v3, 1, v50
	v_lshlrev_b32_e32 v4, 3, v50
	s_addc_u32 s38, s63, s46
	v_add_u32_e32 v5, 24, v4
	v_cmp_eq_u32_e32 vcc, 0, v3
	v_pk_mul_f32 v[10:11], v[184:185], s[36:37] op_sel_hi:[1,0]
	v_pk_mul_f32 v[12:13], v[180:181], s[36:37] op_sel_hi:[1,0]
	s_add_u32 s40, s2, s89
	v_cndmask_b32_e32 v4, v5, v4, vcc
	v_cvt_pk_fp8_f32 v8, v10, v11 op_sel:[0,0,1]
	v_cvt_pk_fp8_f32 v9, v12, v13 op_sel:[0,0,1]
	s_addc_u32 s41, s38, 0
	v_ashrrev_i32_e32 v5, 31, v4
	v_add_u32_e32 v3, s50, v2
	v_lshl_add_u64 v[4:5], s[40:41], 0, v[4:5]
	v_ashrrev_i32_e32 v14, 31, v3
	v_mad_u64_u32 v[10:11], s[40:41], s58, v3, v[4:5]
	v_mul_lo_u32 v12, s58, v14
	v_mul_lo_u32 v13, s59, v3
	v_add3_u32 v11, v13, v11, v12
	v_permlane16_swap_b32_e32 v6, v8
	v_permlane16_swap_b32_e32 v7, v9
	global_store_dwordx4 v[10:11], v[6:9], off sc1
	v_pk_mul_f32 v[10:11], v[170:171], s[36:37] op_sel_hi:[1,0]
	v_pk_mul_f32 v[12:13], v[162:163], s[36:37] op_sel_hi:[1,0]
	v_pk_mul_f32 v[8:9], v[174:175], s[36:37] op_sel_hi:[1,0]
	v_mov_b32_e32 v6, v199
	v_mov_b32_e32 v7, v199
	v_cvt_pk_fp8_f32 v6, v8, v9
	v_cvt_pk_fp8_f32 v7, v10, v11
	v_pk_mul_f32 v[8:9], v[176:177], s[36:37] op_sel_hi:[1,0]
	v_pk_mul_f32 v[10:11], v[172:173], s[36:37] op_sel_hi:[1,0]
	v_cvt_pk_fp8_f32 v6, v8, v9 op_sel:[0,0,1]
	v_cvt_pk_fp8_f32 v7, v10, v11 op_sel:[0,0,1]
	v_pk_mul_f32 v[10:11], v[166:167], s[36:37] op_sel_hi:[1,0]
	v_mov_b32_e32 v8, v199
	v_mov_b32_e32 v9, v199
	v_cvt_pk_fp8_f32 v8, v10, v11
	v_cvt_pk_fp8_f32 v9, v12, v13
	v_pk_mul_f32 v[10:11], v[168:169], s[36:37] op_sel_hi:[1,0]
	v_pk_mul_f32 v[12:13], v[164:165], s[36:37] op_sel_hi:[1,0]
	v_cvt_pk_fp8_f32 v8, v10, v11 op_sel:[0,0,1]
	v_cvt_pk_fp8_f32 v9, v12, v13 op_sel:[0,0,1]
	v_add_u32_e32 v14, 16, v3
	v_ashrrev_i32_e32 v15, 31, v14
	v_mad_u64_u32 v[10:11], s[40:41], s58, v14, v[4:5]
	v_mul_lo_u32 v12, s58, v15
	v_mul_lo_u32 v13, s59, v14
	v_add3_u32 v11, v13, v11, v12
	v_permlane16_swap_b32_e32 v6, v8
	v_permlane16_swap_b32_e32 v7, v9
	global_store_dwordx4 v[10:11], v[6:9], off sc1
	v_pk_mul_f32 v[10:11], v[154:155], s[36:37] op_sel_hi:[1,0]
	v_pk_mul_f32 v[12:13], v[146:147], s[36:37] op_sel_hi:[1,0]
	v_pk_mul_f32 v[8:9], v[158:159], s[36:37] op_sel_hi:[1,0]
	v_mov_b32_e32 v6, v199
	v_mov_b32_e32 v7, v199
	v_cvt_pk_fp8_f32 v6, v8, v9
	v_cvt_pk_fp8_f32 v7, v10, v11
	v_pk_mul_f32 v[8:9], v[160:161], s[36:37] op_sel_hi:[1,0]
	v_pk_mul_f32 v[10:11], v[156:157], s[36:37] op_sel_hi:[1,0]
	v_cvt_pk_fp8_f32 v6, v8, v9 op_sel:[0,0,1]
	v_cvt_pk_fp8_f32 v7, v10, v11 op_sel:[0,0,1]
	v_pk_mul_f32 v[10:11], v[150:151], s[36:37] op_sel_hi:[1,0]
	v_mov_b32_e32 v8, v199
	v_mov_b32_e32 v9, v199
	v_cvt_pk_fp8_f32 v8, v10, v11
	v_cvt_pk_fp8_f32 v9, v12, v13
	v_pk_mul_f32 v[10:11], v[152:153], s[36:37] op_sel_hi:[1,0]
	v_pk_mul_f32 v[12:13], v[148:149], s[36:37] op_sel_hi:[1,0]
	v_cvt_pk_fp8_f32 v8, v10, v11 op_sel:[0,0,1]
	v_cvt_pk_fp8_f32 v9, v12, v13 op_sel:[0,0,1]
	v_add_u32_e32 v14, 32, v3
	v_ashrrev_i32_e32 v15, 31, v14
	v_mad_u64_u32 v[10:11], s[40:41], s58, v14, v[4:5]
	v_mul_lo_u32 v12, s58, v15
	v_mul_lo_u32 v13, s59, v14
	v_add3_u32 v11, v13, v11, v12
	v_permlane16_swap_b32_e32 v6, v8
	v_permlane16_swap_b32_e32 v7, v9
	global_store_dwordx4 v[10:11], v[6:9], off sc1
	v_pk_mul_f32 v[10:11], v[138:139], s[36:37] op_sel_hi:[1,0]
	v_pk_mul_f32 v[12:13], v[130:131], s[36:37] op_sel_hi:[1,0]
	v_pk_mul_f32 v[8:9], v[142:143], s[36:37] op_sel_hi:[1,0]
	v_mov_b32_e32 v6, v199
	v_mov_b32_e32 v7, v199
	v_cvt_pk_fp8_f32 v6, v8, v9
	v_cvt_pk_fp8_f32 v7, v10, v11
	v_pk_mul_f32 v[8:9], v[144:145], s[36:37] op_sel_hi:[1,0]
	v_pk_mul_f32 v[10:11], v[140:141], s[36:37] op_sel_hi:[1,0]
	v_cvt_pk_fp8_f32 v6, v8, v9 op_sel:[0,0,1]
	v_cvt_pk_fp8_f32 v7, v10, v11 op_sel:[0,0,1]
	v_pk_mul_f32 v[10:11], v[134:135], s[36:37] op_sel_hi:[1,0]
	v_mov_b32_e32 v8, v199
	v_mov_b32_e32 v9, v199
	v_cvt_pk_fp8_f32 v8, v10, v11
	v_cvt_pk_fp8_f32 v9, v12, v13
	v_pk_mul_f32 v[10:11], v[136:137], s[36:37] op_sel_hi:[1,0]
	v_pk_mul_f32 v[12:13], v[132:133], s[36:37] op_sel_hi:[1,0]
	v_cvt_pk_fp8_f32 v8, v10, v11 op_sel:[0,0,1]
	v_cvt_pk_fp8_f32 v9, v12, v13 op_sel:[0,0,1]
	v_add_u32_e32 v14, 48, v3
	v_ashrrev_i32_e32 v15, 31, v14
	v_mad_u64_u32 v[10:11], s[40:41], s58, v14, v[4:5]
	v_mul_lo_u32 v12, s58, v15
	v_mul_lo_u32 v13, s59, v14
	v_add3_u32 v11, v13, v11, v12
	v_permlane16_swap_b32_e32 v6, v8
	v_permlane16_swap_b32_e32 v7, v9
	global_store_dwordx4 v[10:11], v[6:9], off sc1
	v_pk_mul_f32 v[10:11], v[122:123], s[36:37] op_sel_hi:[1,0]
	v_pk_mul_f32 v[12:13], v[114:115], s[36:37] op_sel_hi:[1,0]
	v_pk_mul_f32 v[8:9], v[126:127], s[36:37] op_sel_hi:[1,0]
	v_mov_b32_e32 v6, v199
	v_mov_b32_e32 v7, v199
	v_cvt_pk_fp8_f32 v6, v8, v9
	v_cvt_pk_fp8_f32 v7, v10, v11
	v_pk_mul_f32 v[8:9], v[128:129], s[36:37] op_sel_hi:[1,0]
	v_pk_mul_f32 v[10:11], v[124:125], s[36:37] op_sel_hi:[1,0]
	v_cvt_pk_fp8_f32 v6, v8, v9 op_sel:[0,0,1]
	v_cvt_pk_fp8_f32 v7, v10, v11 op_sel:[0,0,1]
	v_pk_mul_f32 v[10:11], v[118:119], s[36:37] op_sel_hi:[1,0]
	v_mov_b32_e32 v8, v199
	v_mov_b32_e32 v9, v199
	v_cvt_pk_fp8_f32 v8, v10, v11
	v_cvt_pk_fp8_f32 v9, v12, v13
	v_pk_mul_f32 v[10:11], v[120:121], s[36:37] op_sel_hi:[1,0]
	v_pk_mul_f32 v[12:13], v[116:117], s[36:37] op_sel_hi:[1,0]
	v_cvt_pk_fp8_f32 v8, v10, v11 op_sel:[0,0,1]
	v_cvt_pk_fp8_f32 v9, v12, v13 op_sel:[0,0,1]
	v_add_u32_e32 v14, 0x80, v3
	v_ashrrev_i32_e32 v15, 31, v14
	v_mad_u64_u32 v[10:11], s[40:41], s58, v14, v[4:5]
	v_mul_lo_u32 v12, s58, v15
	v_mul_lo_u32 v13, s59, v14
	v_add3_u32 v11, v13, v11, v12
	v_permlane16_swap_b32_e32 v6, v8
	v_permlane16_swap_b32_e32 v7, v9
	global_store_dwordx4 v[10:11], v[6:9], off sc1
	v_pk_mul_f32 v[10:11], v[106:107], s[36:37] op_sel_hi:[1,0]
	v_pk_mul_f32 v[12:13], v[90:91], s[36:37] op_sel_hi:[1,0]
	v_pk_mul_f32 v[8:9], v[110:111], s[36:37] op_sel_hi:[1,0]
	v_mov_b32_e32 v6, v199
	v_mov_b32_e32 v7, v199
	v_cvt_pk_fp8_f32 v6, v8, v9
	v_cvt_pk_fp8_f32 v7, v10, v11
	v_pk_mul_f32 v[8:9], v[112:113], s[36:37] op_sel_hi:[1,0]
	v_pk_mul_f32 v[10:11], v[108:109], s[36:37] op_sel_hi:[1,0]
	v_cvt_pk_fp8_f32 v6, v8, v9 op_sel:[0,0,1]
	v_cvt_pk_fp8_f32 v7, v10, v11 op_sel:[0,0,1]
	v_pk_mul_f32 v[10:11], v[94:95], s[36:37] op_sel_hi:[1,0]
	v_mov_b32_e32 v8, v199
	v_mov_b32_e32 v9, v199
	v_cvt_pk_fp8_f32 v8, v10, v11
	v_cvt_pk_fp8_f32 v9, v12, v13
	v_pk_mul_f32 v[10:11], v[96:97], s[36:37] op_sel_hi:[1,0]
	v_pk_mul_f32 v[12:13], v[92:93], s[36:37] op_sel_hi:[1,0]
	v_cvt_pk_fp8_f32 v8, v10, v11 op_sel:[0,0,1]
	v_cvt_pk_fp8_f32 v9, v12, v13 op_sel:[0,0,1]
	v_add_u32_e32 v14, 0x90, v3
	v_ashrrev_i32_e32 v15, 31, v14
	v_mad_u64_u32 v[10:11], s[40:41], s58, v14, v[4:5]
	v_mul_lo_u32 v12, s58, v15
	v_mul_lo_u32 v13, s59, v14
	v_add3_u32 v11, v13, v11, v12
	v_permlane16_swap_b32_e32 v6, v8
	v_permlane16_swap_b32_e32 v7, v9
	global_store_dwordx4 v[10:11], v[6:9], off sc1
	v_pk_mul_f32 v[10:11], v[74:75], s[36:37] op_sel_hi:[1,0]
	v_pk_mul_f32 v[12:13], v[102:103], s[36:37] op_sel_hi:[1,0]
	v_pk_mul_f32 v[8:9], v[78:79], s[36:37] op_sel_hi:[1,0]
	v_mov_b32_e32 v6, v199
	v_mov_b32_e32 v7, v199
	v_cvt_pk_fp8_f32 v6, v8, v9
	v_cvt_pk_fp8_f32 v7, v10, v11
	v_pk_mul_f32 v[8:9], v[80:81], s[36:37] op_sel_hi:[1,0]
	v_pk_mul_f32 v[10:11], v[76:77], s[36:37] op_sel_hi:[1,0]
	v_cvt_pk_fp8_f32 v6, v8, v9 op_sel:[0,0,1]
	v_cvt_pk_fp8_f32 v7, v10, v11 op_sel:[0,0,1]
	v_pk_mul_f32 v[10:11], v[98:99], s[36:37] op_sel_hi:[1,0]
	v_mov_b32_e32 v8, v199
	v_mov_b32_e32 v9, v199
	v_cvt_pk_fp8_f32 v8, v10, v11
	v_cvt_pk_fp8_f32 v9, v12, v13
	v_pk_mul_f32 v[10:11], v[100:101], s[36:37] op_sel_hi:[1,0]
	v_pk_mul_f32 v[12:13], v[104:105], s[36:37] op_sel_hi:[1,0]
	v_cvt_pk_fp8_f32 v8, v10, v11 op_sel:[0,0,1]
	v_cvt_pk_fp8_f32 v9, v12, v13 op_sel:[0,0,1]
	v_add_u32_e32 v14, 0xa0, v3
	v_ashrrev_i32_e32 v15, 31, v14
	v_mad_u64_u32 v[10:11], s[40:41], s58, v14, v[4:5]
	v_mul_lo_u32 v12, s58, v15
	v_mul_lo_u32 v13, s59, v14
	v_add3_u32 v11, v13, v11, v12
	v_permlane16_swap_b32_e32 v6, v8
	v_permlane16_swap_b32_e32 v7, v9
	global_store_dwordx4 v[10:11], v[6:9], off sc1
	v_pk_mul_f32 v[10:11], v[66:67], s[36:37] op_sel_hi:[1,0]
	v_pk_mul_f32 v[12:13], v[86:87], s[36:37] op_sel_hi:[1,0]
	v_pk_mul_f32 v[8:9], v[70:71], s[36:37] op_sel_hi:[1,0]
	v_mov_b32_e32 v6, v199
	v_mov_b32_e32 v7, v199
	v_cvt_pk_fp8_f32 v6, v8, v9
	v_cvt_pk_fp8_f32 v7, v10, v11
	v_pk_mul_f32 v[8:9], v[72:73], s[36:37] op_sel_hi:[1,0]
	v_pk_mul_f32 v[10:11], v[68:69], s[36:37] op_sel_hi:[1,0]
	v_cvt_pk_fp8_f32 v6, v8, v9 op_sel:[0,0,1]
	v_cvt_pk_fp8_f32 v7, v10, v11 op_sel:[0,0,1]
	v_pk_mul_f32 v[10:11], v[82:83], s[36:37] op_sel_hi:[1,0]
	v_mov_b32_e32 v8, v199
	v_mov_b32_e32 v9, v199
	v_cvt_pk_fp8_f32 v8, v10, v11
	v_cvt_pk_fp8_f32 v9, v12, v13
	v_pk_mul_f32 v[10:11], v[84:85], s[36:37] op_sel_hi:[1,0]
	v_pk_mul_f32 v[12:13], v[88:89], s[36:37] op_sel_hi:[1,0]
	v_cvt_pk_fp8_f32 v8, v10, v11 op_sel:[0,0,1]
	v_cvt_pk_fp8_f32 v9, v12, v13 op_sel:[0,0,1]
	v_add_u32_e32 v3, 0xb0, v3
	v_ashrrev_i32_e32 v14, 31, v3
	v_mad_u64_u32 v[4:5], s[40:41], s58, v3, v[4:5]
	v_mul_lo_u32 v10, s58, v14
	v_mul_lo_u32 v3, s59, v3
	v_add3_u32 v5, v3, v5, v10
	v_permlane16_swap_b32_e32 v6, v8
	v_permlane16_swap_b32_e32 v7, v9
	global_store_dwordx4 v[4:5], v[6:9], off sc1

.LBB0_156:
	v_add_u32_e32 v201, s50, v2
	v_lshlrev_b32_e32 v2, 2, v2
	v_and_b32_e32 v6, 60, v2
	v_lshrrev_b32_e32 v2, 2, v201
	v_and_b32_e32 v2, 0x1fc, v2
	v_add_u32_e32 v2, v2, v50
	v_lshl_or_b32 v2, v2, 6, v6
	v_ashrrev_i32_e32 v3, 31, v2
	v_lshl_add_u64 v[2:3], v[2:3], 2, s[24:25]
	v_add_co_u32_e32 v4, vcc, 0x20000, v2
	v_add_u32_e32 v221, 16, v201
	s_nop 0
	v_addc_co_u32_e32 v5, vcc, 0, v3, vcc
	global_load_dwordx4 v[56:59], v[2:3], off
	global_load_dwordx4 v[60:63], v[4:5], off
	v_lshrrev_b32_e32 v2, 2, v221
	v_and_b32_e32 v2, 0x1fc, v2
	v_add_u32_e32 v2, v2, v50
	v_lshl_or_b32 v2, v2, 6, v6
	v_ashrrev_i32_e32 v3, 31, v2
	v_lshl_add_u64 v[2:3], v[2:3], 2, s[24:25]
	v_add_co_u32_e32 v4, vcc, s90, v2
	v_add_u32_e32 v236, 32, v201
	s_nop 0
	v_addc_co_u32_e32 v5, vcc, 0, v3, vcc
	global_load_dwordx4 v[204:207], v[2:3], off
	global_load_dwordx4 v[208:211], v[4:5], off
	v_lshrrev_b32_e32 v2, 2, v236
	v_and_b32_e32 v2, 0x1fc, v2
	v_add_u32_e32 v2, v2, v50
	v_lshl_or_b32 v2, v2, 6, v6
	v_ashrrev_i32_e32 v3, 31, v2
	v_lshl_add_u64 v[2:3], v[2:3], 2, s[24:25]
	v_add_co_u32_e32 v4, vcc, s90, v2
	v_add_u32_e32 v237, 48, v201
	s_nop 0
	v_addc_co_u32_e32 v5, vcc, 0, v3, vcc
	global_load_dwordx4 v[46:49], v[2:3], off
	global_load_dwordx4 v[42:45], v[4:5], off
	v_lshrrev_b32_e32 v2, 2, v237
	v_and_b32_e32 v2, 0x1fc, v2
	v_add_u32_e32 v2, v2, v50
	v_lshl_or_b32 v2, v2, 6, v6
	v_ashrrev_i32_e32 v3, 31, v2
	v_lshl_add_u64 v[2:3], v[2:3], 2, s[24:25]
	v_add_co_u32_e32 v4, vcc, s90, v2
	v_add_u32_e32 v55, 0x80, v201
	s_nop 0
	v_addc_co_u32_e32 v5, vcc, 0, v3, vcc
	global_load_dwordx4 v[38:41], v[2:3], off
	global_load_dwordx4 v[34:37], v[4:5], off
	v_lshrrev_b32_e32 v2, 2, v55
	v_and_b32_e32 v2, 0x1fc, v2
	v_add_u32_e32 v2, v2, v50
	v_lshl_or_b32 v2, v2, 6, v6
	v_ashrrev_i32_e32 v3, 31, v2
	v_lshl_add_u64 v[2:3], v[2:3], 2, s[24:25]
	v_add_co_u32_e32 v4, vcc, s90, v2
	v_add_u32_e32 v54, 0x90, v201
	s_nop 0
	v_addc_co_u32_e32 v5, vcc, 0, v3, vcc
	global_load_dwordx4 v[30:33], v[2:3], off
	global_load_dwordx4 v[26:29], v[4:5], off
	v_lshrrev_b32_e32 v2, 2, v54
	v_and_b32_e32 v2, 0x1fc, v2
	v_add_u32_e32 v2, v2, v50
	v_lshl_or_b32 v2, v2, 6, v6
	v_ashrrev_i32_e32 v3, 31, v2
	v_lshl_add_u64 v[2:3], v[2:3], 2, s[24:25]
	v_add_co_u32_e32 v4, vcc, s90, v2
	v_add_u32_e32 v53, 0xa0, v201
	s_nop 0
	v_addc_co_u32_e32 v5, vcc, 0, v3, vcc
	global_load_dwordx4 v[22:25], v[2:3], off
	global_load_dwordx4 v[18:21], v[4:5], off
	v_lshrrev_b32_e32 v2, 2, v53
	v_and_b32_e32 v2, 0x1fc, v2
	v_add_u32_e32 v2, v2, v50
	v_lshl_or_b32 v2, v2, 6, v6
	v_ashrrev_i32_e32 v3, 31, v2
	v_lshl_add_u64 v[2:3], v[2:3], 2, s[24:25]
	v_add_co_u32_e32 v4, vcc, s90, v2
	v_add_u32_e32 v52, 0xb0, v201
	s_nop 0
	v_addc_co_u32_e32 v5, vcc, 0, v3, vcc
	global_load_dwordx4 v[14:17], v[2:3], off
	global_load_dwordx4 v[10:13], v[4:5], off
	v_lshrrev_b32_e32 v2, 2, v52
	v_and_b32_e32 v2, 0x1fc, v2
	v_add_u32_e32 v2, v2, v50
	v_lshl_or_b32 v2, v2, 6, v6
	v_ashrrev_i32_e32 v3, 31, v2
	v_lshl_add_u64 v[2:3], v[2:3], 2, s[24:25]
	v_add_co_u32_e32 v4, vcc, s90, v2
	v_and_b32_e32 v51, 1, v50
	s_nop 0
	v_addc_co_u32_e32 v5, vcc, 0, v3, vcc
	v_lshlrev_b32_e32 v50, 3, v50
	v_add_u32_e32 v64, 24, v50
	v_cmp_eq_u32_e32 vcc, 0, v51
	s_add_u32 s2, s62, s7
	s_waitcnt vmcnt(0)
	v_lshlrev_b32_e32 v65, 16, v57
	v_cndmask_b32_e32 v50, v64, v50, vcc
	v_lshlrev_b32_e32 v64, 16, v56
	v_and_b32_e32 v56, 0xffff0000, v56
	v_and_b32_e32 v57, 0xffff0000, v57
	s_addc_u32 s7, s63, s46
	v_pk_mul_f32 v[228:229], v[182:183], v[56:57]
	s_add_u32 s40, s2, s89
	v_lshlrev_b32_e32 v224, 16, v60
	v_lshlrev_b32_e32 v225, 16, v61
	v_pk_fma_f32 v[228:229], v[190:191], v[64:65], v[228:229] neg_lo:[0,0,1] neg_hi:[0,0,1]
	v_pk_mul_f32 v[64:65], v[182:183], v[64:65]
	s_addc_u32 s41, s7, 0
	v_ashrrev_i32_e32 v51, 31, v50
	v_lshlrev_b32_e32 v222, 16, v58
	v_lshlrev_b32_e32 v223, 16, v59
	v_and_b32_e32 v60, 0xffff0000, v60
	v_and_b32_e32 v61, 0xffff0000, v61
	v_pk_fma_f32 v[64:65], v[190:191], v[56:57], v[64:65]
	v_pk_mul_f32 v[56:57], v[178:179], v[224:225]
	v_lshl_add_u64 v[50:51], s[40:41], 0, v[50:51]
	v_and_b32_e32 v58, 0xffff0000, v58
	v_and_b32_e32 v59, 0xffff0000, v59
	v_lshlrev_b32_e32 v226, 16, v62
	v_lshlrev_b32_e32 v227, 16, v63
	v_pk_mul_f32 v[232:233], v[178:179], v[60:61]
	v_pk_mul_f32 v[182:183], v[184:185], v[222:223]
	v_pk_fma_f32 v[60:61], v[186:187], v[60:61], v[56:57]
	v_ashrrev_i32_e32 v56, 31, v201
	v_and_b32_e32 v62, 0xffff0000, v62
	v_and_b32_e32 v63, 0xffff0000, v63
	v_pk_mul_f32 v[230:231], v[184:185], v[58:59]
	v_pk_fma_f32 v[182:183], v[192:193], v[58:59], v[182:183]
	v_pk_mul_f32 v[58:59], v[180:181], v[226:227]
	v_mad_u64_u32 v[178:179], s[40:41], s58, v201, v[50:51]
	v_mul_lo_u32 v56, s58, v56
	v_mul_lo_u32 v57, s59, v201
	v_pk_mul_f32 v[234:235], v[180:181], v[62:63]
	v_pk_fma_f32 v[232:233], v[186:187], v[224:225], v[232:233] neg_lo:[0,0,1] neg_hi:[0,0,1]
	v_pk_fma_f32 v[62:63], v[188:189], v[62:63], v[58:59]
	v_add3_u32 v179, v57, v179, v56
	v_mov_b32_e32 v56, v199
	v_mov_b32_e32 v57, v199
	v_mov_b32_e32 v58, v199
	v_mov_b32_e32 v59, v199
	v_cvt_pk_fp8_f32 v56, v228, v229
	v_cvt_pk_fp8_f32 v57, v232, v233
	v_cvt_pk_fp8_f32 v58, v64, v65
	v_cvt_pk_fp8_f32 v59, v60, v61
	v_pk_fma_f32 v[230:231], v[192:193], v[222:223], v[230:231] neg_lo:[0,0,1] neg_hi:[0,0,1]
	v_pk_fma_f32 v[234:235], v[188:189], v[226:227], v[234:235] neg_lo:[0,0,1] neg_hi:[0,0,1]
	v_cvt_pk_fp8_f32 v56, v230, v231 op_sel:[0,0,1]
	v_cvt_pk_fp8_f32 v58, v182, v183 op_sel:[0,0,1]
	v_cvt_pk_fp8_f32 v57, v234, v235 op_sel:[0,0,1]
	v_cvt_pk_fp8_f32 v59, v62, v63 op_sel:[0,0,1]
	v_and_b32_e32 v60, 0xffff0000, v204
	v_permlane16_swap_b32_e32 v56, v58
	v_permlane16_swap_b32_e32 v57, v59
	v_and_b32_e32 v61, 0xffff0000, v205
	global_load_dwordx4 v[6:9], v[2:3], off
	s_nop 0
	global_load_dwordx4 v[2:5], v[4:5], off
	global_store_dwordx4 v[178:179], v[56:59], off sc1
	v_pk_mul_f32 v[184:185], v[166:167], v[60:61]
	v_and_b32_e32 v62, 0xffff0000, v206
	v_lshlrev_b32_e32 v56, 16, v204
	v_lshlrev_b32_e32 v57, 16, v205
	v_and_b32_e32 v63, 0xffff0000, v207
	v_lshlrev_b32_e32 v64, 16, v208
	v_lshlrev_b32_e32 v65, 16, v209
	v_pk_fma_f32 v[184:185], v[174:175], v[56:57], v[184:185] neg_lo:[0,0,1] neg_hi:[0,0,1]
	v_pk_mul_f32 v[56:57], v[166:167], v[56:57]
	v_lshlrev_b32_e32 v58, 16, v206
	v_lshlrev_b32_e32 v59, 16, v207
	v_and_b32_e32 v180, 0xffff0000, v208
	v_and_b32_e32 v181, 0xffff0000, v209
	v_pk_mul_f32 v[186:187], v[168:169], v[62:63]
	v_pk_fma_f32 v[60:61], v[174:175], v[60:61], v[56:57]
	v_pk_mul_f32 v[56:57], v[162:163], v[64:65]
	v_lshlrev_b32_e32 v178, 16, v210
	v_lshlrev_b32_e32 v179, 16, v211
	v_and_b32_e32 v182, 0xffff0000, v210
	v_and_b32_e32 v183, 0xffff0000, v211
	v_pk_fma_f32 v[186:187], v[176:177], v[58:59], v[186:187] neg_lo:[0,0,1] neg_hi:[0,0,1]
	v_pk_mul_f32 v[188:189], v[162:163], v[180:181]
	v_pk_mul_f32 v[58:59], v[168:169], v[58:59]
	v_pk_fma_f32 v[162:163], v[170:171], v[180:181], v[56:57]
	v_ashrrev_i32_e32 v56, 31, v221
	v_pk_mul_f32 v[190:191], v[164:165], v[182:183]
	v_pk_fma_f32 v[62:63], v[176:177], v[62:63], v[58:59]
	v_pk_mul_f32 v[58:59], v[164:165], v[178:179]
	v_mad_u64_u32 v[164:165], s[40:41], s58, v221, v[50:51]
	v_mul_lo_u32 v56, s58, v56
	v_mul_lo_u32 v57, s59, v221
	v_pk_fma_f32 v[188:189], v[170:171], v[64:65], v[188:189] neg_lo:[0,0,1] neg_hi:[0,0,1]
	v_pk_fma_f32 v[64:65], v[172:173], v[182:183], v[58:59]
	v_add3_u32 v165, v57, v165, v56
	v_mov_b32_e32 v56, v199
	v_mov_b32_e32 v57, v199
	v_mov_b32_e32 v58, v199
	v_mov_b32_e32 v59, v199
	v_cvt_pk_fp8_f32 v56, v184, v185
	v_cvt_pk_fp8_f32 v57, v188, v189
	v_cvt_pk_fp8_f32 v58, v60, v61
	v_cvt_pk_fp8_f32 v59, v162, v163
	v_pk_fma_f32 v[190:191], v[172:173], v[178:179], v[190:191] neg_lo:[0,0,1] neg_hi:[0,0,1]
	v_cvt_pk_fp8_f32 v56, v186, v187 op_sel:[0,0,1]
	v_cvt_pk_fp8_f32 v58, v62, v63 op_sel:[0,0,1]
	v_cvt_pk_fp8_f32 v57, v190, v191 op_sel:[0,0,1]
	v_cvt_pk_fp8_f32 v59, v64, v65 op_sel:[0,0,1]
	v_lshlrev_b32_e32 v60, 16, v42
	v_permlane16_swap_b32_e32 v56, v58
	v_permlane16_swap_b32_e32 v57, v59
	global_store_dwordx4 v[164:165], v[56:59], off sc1
	v_lshlrev_b32_e32 v61, 16, v43
	v_and_b32_e32 v42, 0xffff0000, v42
	v_lshlrev_b32_e32 v56, 16, v46
	v_lshlrev_b32_e32 v57, 16, v47
	v_and_b32_e32 v46, 0xffff0000, v46
	v_and_b32_e32 v47, 0xffff0000, v47
	v_pk_mul_f32 v[64:65], v[150:151], v[46:47]
	v_lshlrev_b32_e32 v58, 16, v48
	v_lshlrev_b32_e32 v59, 16, v49
	v_and_b32_e32 v48, 0xffff0000, v48
	v_and_b32_e32 v49, 0xffff0000, v49
	v_pk_fma_f32 v[64:65], v[158:159], v[56:57], v[64:65] neg_lo:[0,0,1] neg_hi:[0,0,1]
	v_pk_mul_f32 v[56:57], v[150:151], v[56:57]
	v_and_b32_e32 v43, 0xffff0000, v43
	v_pk_mul_f32 v[162:163], v[152:153], v[48:49]
	v_pk_fma_f32 v[46:47], v[158:159], v[46:47], v[56:57]
	v_pk_mul_f32 v[56:57], v[146:147], v[60:61]
	v_lshlrev_b32_e32 v62, 16, v44
	v_lshlrev_b32_e32 v63, 16, v45
	v_pk_fma_f32 v[162:163], v[160:161], v[58:59], v[162:163] neg_lo:[0,0,1] neg_hi:[0,0,1]
	v_pk_mul_f32 v[164:165], v[146:147], v[42:43]
	v_pk_mul_f32 v[58:59], v[152:153], v[58:59]
	v_pk_fma_f32 v[56:57], v[154:155], v[42:43], v[56:57]
	v_ashrrev_i32_e32 v42, 31, v236
	v_and_b32_e32 v44, 0xffff0000, v44
	v_and_b32_e32 v45, 0xffff0000, v45
	v_pk_fma_f32 v[164:165], v[154:155], v[60:61], v[164:165] neg_lo:[0,0,1] neg_hi:[0,0,1]
	v_pk_fma_f32 v[48:49], v[160:161], v[48:49], v[58:59]
	v_pk_mul_f32 v[58:59], v[148:149], v[62:63]
	v_mad_u64_u32 v[60:61], s[40:41], s58, v236, v[50:51]
	v_mul_lo_u32 v42, s58, v42
	v_mul_lo_u32 v43, s59, v236
	v_pk_mul_f32 v[166:167], v[148:149], v[44:45]
	v_pk_fma_f32 v[58:59], v[156:157], v[44:45], v[58:59]
	v_add3_u32 v61, v43, v61, v42
	v_mov_b32_e32 v42, v199
	v_mov_b32_e32 v43, v199
	v_mov_b32_e32 v44, v199
	v_mov_b32_e32 v45, v199
	v_cvt_pk_fp8_f32 v42, v64, v65
	v_cvt_pk_fp8_f32 v43, v164, v165
	v_cvt_pk_fp8_f32 v44, v46, v47
	v_cvt_pk_fp8_f32 v45, v56, v57
	v_pk_fma_f32 v[166:167], v[156:157], v[62:63], v[166:167] neg_lo:[0,0,1] neg_hi:[0,0,1]
	v_cvt_pk_fp8_f32 v42, v162, v163 op_sel:[0,0,1]
	v_cvt_pk_fp8_f32 v44, v48, v49 op_sel:[0,0,1]
	v_cvt_pk_fp8_f32 v43, v166, v167 op_sel:[0,0,1]
	v_cvt_pk_fp8_f32 v45, v58, v59 op_sel:[0,0,1]
	v_lshlrev_b32_e32 v46, 16, v34
	v_permlane16_swap_b32_e32 v42, v44
	v_permlane16_swap_b32_e32 v43, v45
	global_store_dwordx4 v[60:61], v[42:45], off sc1
	v_lshlrev_b32_e32 v47, 16, v35
	v_and_b32_e32 v34, 0xffff0000, v34
	v_lshlrev_b32_e32 v42, 16, v38
	v_lshlrev_b32_e32 v43, 16, v39
	v_and_b32_e32 v38, 0xffff0000, v38
	v_and_b32_e32 v39, 0xffff0000, v39
	v_pk_mul_f32 v[56:57], v[134:135], v[38:39]
	v_lshlrev_b32_e32 v44, 16, v40
	v_lshlrev_b32_e32 v45, 16, v41
	v_and_b32_e32 v40, 0xffff0000, v40
	v_and_b32_e32 v41, 0xffff0000, v41
	v_pk_fma_f32 v[56:57], v[142:143], v[42:43], v[56:57] neg_lo:[0,0,1] neg_hi:[0,0,1]
	v_pk_mul_f32 v[42:43], v[134:135], v[42:43]
	v_and_b32_e32 v35, 0xffff0000, v35
	v_pk_mul_f32 v[58:59], v[136:137], v[40:41]
	v_pk_fma_f32 v[38:39], v[142:143], v[38:39], v[42:43]
	v_pk_mul_f32 v[42:43], v[130:131], v[46:47]
	v_lshlrev_b32_e32 v48, 16, v36
	v_lshlrev_b32_e32 v49, 16, v37
	v_pk_fma_f32 v[58:59], v[144:145], v[44:45], v[58:59] neg_lo:[0,0,1] neg_hi:[0,0,1]
	v_pk_mul_f32 v[60:61], v[130:131], v[34:35]
	v_pk_mul_f32 v[44:45], v[136:137], v[44:45]
	v_pk_fma_f32 v[42:43], v[138:139], v[34:35], v[42:43]
	v_ashrrev_i32_e32 v34, 31, v237
	v_and_b32_e32 v36, 0xffff0000, v36
	v_and_b32_e32 v37, 0xffff0000, v37
	v_pk_fma_f32 v[60:61], v[138:139], v[46:47], v[60:61] neg_lo:[0,0,1] neg_hi:[0,0,1]
	v_pk_fma_f32 v[40:41], v[144:145], v[40:41], v[44:45]
	v_pk_mul_f32 v[44:45], v[132:133], v[48:49]
	v_mad_u64_u32 v[46:47], s[40:41], s58, v237, v[50:51]
	v_mul_lo_u32 v34, s58, v34
	v_mul_lo_u32 v35, s59, v237
	v_pk_mul_f32 v[62:63], v[132:133], v[36:37]
	v_pk_fma_f32 v[44:45], v[140:141], v[36:37], v[44:45]
	v_add3_u32 v47, v35, v47, v34
	v_mov_b32_e32 v34, v199
	v_mov_b32_e32 v35, v199
	v_mov_b32_e32 v36, v199
	v_mov_b32_e32 v37, v199
	v_cvt_pk_fp8_f32 v34, v56, v57
	v_cvt_pk_fp8_f32 v35, v60, v61
	v_cvt_pk_fp8_f32 v36, v38, v39
	v_cvt_pk_fp8_f32 v37, v42, v43
	v_pk_fma_f32 v[62:63], v[140:141], v[48:49], v[62:63] neg_lo:[0,0,1] neg_hi:[0,0,1]
	v_cvt_pk_fp8_f32 v34, v58, v59 op_sel:[0,0,1]
	v_cvt_pk_fp8_f32 v36, v40, v41 op_sel:[0,0,1]
	v_cvt_pk_fp8_f32 v35, v62, v63 op_sel:[0,0,1]
	v_cvt_pk_fp8_f32 v37, v44, v45 op_sel:[0,0,1]
	v_lshlrev_b32_e32 v38, 16, v26
	v_permlane16_swap_b32_e32 v34, v36
	v_permlane16_swap_b32_e32 v35, v37
	global_store_dwordx4 v[46:47], v[34:37], off sc1
	v_lshlrev_b32_e32 v39, 16, v27
	v_and_b32_e32 v26, 0xffff0000, v26
	v_lshlrev_b32_e32 v34, 16, v30
	v_lshlrev_b32_e32 v35, 16, v31
	v_and_b32_e32 v30, 0xffff0000, v30
	v_and_b32_e32 v31, 0xffff0000, v31
	v_pk_mul_f32 v[42:43], v[118:119], v[30:31]
	v_lshlrev_b32_e32 v36, 16, v32
	v_lshlrev_b32_e32 v37, 16, v33
	v_and_b32_e32 v32, 0xffff0000, v32
	v_and_b32_e32 v33, 0xffff0000, v33
	v_pk_fma_f32 v[42:43], v[126:127], v[34:35], v[42:43] neg_lo:[0,0,1] neg_hi:[0,0,1]
	v_pk_mul_f32 v[34:35], v[118:119], v[34:35]
	v_and_b32_e32 v27, 0xffff0000, v27
	v_pk_mul_f32 v[44:45], v[120:121], v[32:33]
	v_pk_fma_f32 v[30:31], v[126:127], v[30:31], v[34:35]
	v_pk_mul_f32 v[34:35], v[114:115], v[38:39]
	v_lshlrev_b32_e32 v40, 16, v28
	v_lshlrev_b32_e32 v41, 16, v29
	v_pk_fma_f32 v[44:45], v[128:129], v[36:37], v[44:45] neg_lo:[0,0,1] neg_hi:[0,0,1]
	v_pk_mul_f32 v[46:47], v[114:115], v[26:27]
	v_pk_mul_f32 v[36:37], v[120:121], v[36:37]
	v_pk_fma_f32 v[34:35], v[122:123], v[26:27], v[34:35]
	v_ashrrev_i32_e32 v26, 31, v55
	v_and_b32_e32 v28, 0xffff0000, v28
	v_and_b32_e32 v29, 0xffff0000, v29
	v_pk_fma_f32 v[46:47], v[122:123], v[38:39], v[46:47] neg_lo:[0,0,1] neg_hi:[0,0,1]
	v_pk_fma_f32 v[32:33], v[128:129], v[32:33], v[36:37]
	v_pk_mul_f32 v[36:37], v[116:117], v[40:41]
	v_mad_u64_u32 v[38:39], s[40:41], s58, v55, v[50:51]
	v_mul_lo_u32 v26, s58, v26
	v_mul_lo_u32 v27, s59, v55
	v_pk_mul_f32 v[48:49], v[116:117], v[28:29]
	v_pk_fma_f32 v[36:37], v[124:125], v[28:29], v[36:37]
	v_add3_u32 v39, v27, v39, v26
	v_mov_b32_e32 v26, v199
	v_mov_b32_e32 v27, v199
	v_mov_b32_e32 v28, v199
	v_mov_b32_e32 v29, v199
	v_cvt_pk_fp8_f32 v26, v42, v43
	v_cvt_pk_fp8_f32 v27, v46, v47
	v_cvt_pk_fp8_f32 v28, v30, v31
	v_cvt_pk_fp8_f32 v29, v34, v35
	v_pk_fma_f32 v[48:49], v[124:125], v[40:41], v[48:49] neg_lo:[0,0,1] neg_hi:[0,0,1]
	v_cvt_pk_fp8_f32 v26, v44, v45 op_sel:[0,0,1]
	v_cvt_pk_fp8_f32 v28, v32, v33 op_sel:[0,0,1]
	v_cvt_pk_fp8_f32 v27, v48, v49 op_sel:[0,0,1]
	v_cvt_pk_fp8_f32 v29, v36, v37 op_sel:[0,0,1]
	v_lshlrev_b32_e32 v30, 16, v18
	v_permlane16_swap_b32_e32 v26, v28
	v_permlane16_swap_b32_e32 v27, v29
	global_store_dwordx4 v[38:39], v[26:29], off sc1
	v_lshlrev_b32_e32 v31, 16, v19
	v_and_b32_e32 v18, 0xffff0000, v18
	v_lshlrev_b32_e32 v26, 16, v22
	v_lshlrev_b32_e32 v27, 16, v23
	v_and_b32_e32 v22, 0xffff0000, v22
	v_and_b32_e32 v23, 0xffff0000, v23
	v_pk_mul_f32 v[34:35], v[94:95], v[22:23]
	v_lshlrev_b32_e32 v28, 16, v24
	v_lshlrev_b32_e32 v29, 16, v25
	v_and_b32_e32 v24, 0xffff0000, v24
	v_and_b32_e32 v25, 0xffff0000, v25
	v_pk_fma_f32 v[34:35], v[110:111], v[26:27], v[34:35] neg_lo:[0,0,1] neg_hi:[0,0,1]
	v_pk_mul_f32 v[26:27], v[94:95], v[26:27]
	v_and_b32_e32 v19, 0xffff0000, v19
	v_pk_mul_f32 v[36:37], v[96:97], v[24:25]
	v_pk_fma_f32 v[22:23], v[110:111], v[22:23], v[26:27]
	v_pk_mul_f32 v[26:27], v[90:91], v[30:31]
	v_lshlrev_b32_e32 v32, 16, v20
	v_lshlrev_b32_e32 v33, 16, v21
	v_pk_fma_f32 v[36:37], v[112:113], v[28:29], v[36:37] neg_lo:[0,0,1] neg_hi:[0,0,1]
	v_pk_mul_f32 v[38:39], v[90:91], v[18:19]
	v_pk_mul_f32 v[28:29], v[96:97], v[28:29]
	v_pk_fma_f32 v[26:27], v[106:107], v[18:19], v[26:27]
	v_ashrrev_i32_e32 v18, 31, v54
	v_and_b32_e32 v20, 0xffff0000, v20
	v_and_b32_e32 v21, 0xffff0000, v21
	v_pk_fma_f32 v[38:39], v[106:107], v[30:31], v[38:39] neg_lo:[0,0,1] neg_hi:[0,0,1]
	v_pk_fma_f32 v[24:25], v[112:113], v[24:25], v[28:29]
	v_pk_mul_f32 v[28:29], v[92:93], v[32:33]
	v_mad_u64_u32 v[30:31], s[40:41], s58, v54, v[50:51]
	v_mul_lo_u32 v18, s58, v18
	v_mul_lo_u32 v19, s59, v54
	v_pk_mul_f32 v[40:41], v[92:93], v[20:21]
	v_pk_fma_f32 v[28:29], v[108:109], v[20:21], v[28:29]
	v_add3_u32 v31, v19, v31, v18
	v_mov_b32_e32 v18, v199
	v_mov_b32_e32 v19, v199
	v_mov_b32_e32 v20, v199
	v_mov_b32_e32 v21, v199
	v_cvt_pk_fp8_f32 v18, v34, v35
	v_cvt_pk_fp8_f32 v19, v38, v39
	v_cvt_pk_fp8_f32 v20, v22, v23
	v_cvt_pk_fp8_f32 v21, v26, v27
	v_pk_fma_f32 v[40:41], v[108:109], v[32:33], v[40:41] neg_lo:[0,0,1] neg_hi:[0,0,1]
	v_cvt_pk_fp8_f32 v18, v36, v37 op_sel:[0,0,1]
	v_cvt_pk_fp8_f32 v20, v24, v25 op_sel:[0,0,1]
	v_cvt_pk_fp8_f32 v19, v40, v41 op_sel:[0,0,1]
	v_cvt_pk_fp8_f32 v21, v28, v29 op_sel:[0,0,1]
	v_lshlrev_b32_e32 v22, 16, v10
	v_permlane16_swap_b32_e32 v18, v20
	v_permlane16_swap_b32_e32 v19, v21
	global_store_dwordx4 v[30:31], v[18:21], off sc1
	v_lshlrev_b32_e32 v23, 16, v11
	v_and_b32_e32 v10, 0xffff0000, v10
	v_lshlrev_b32_e32 v18, 16, v14
	v_lshlrev_b32_e32 v19, 16, v15
	v_and_b32_e32 v14, 0xffff0000, v14
	v_and_b32_e32 v15, 0xffff0000, v15
	v_pk_mul_f32 v[26:27], v[98:99], v[14:15]
	v_lshlrev_b32_e32 v20, 16, v16
	v_lshlrev_b32_e32 v21, 16, v17
	v_and_b32_e32 v16, 0xffff0000, v16
	v_and_b32_e32 v17, 0xffff0000, v17
	v_pk_fma_f32 v[26:27], v[78:79], v[18:19], v[26:27] neg_lo:[0,0,1] neg_hi:[0,0,1]
	v_pk_mul_f32 v[18:19], v[98:99], v[18:19]
	v_and_b32_e32 v11, 0xffff0000, v11
	v_pk_mul_f32 v[28:29], v[100:101], v[16:17]
	v_pk_fma_f32 v[14:15], v[78:79], v[14:15], v[18:19]
	v_pk_mul_f32 v[18:19], v[102:103], v[22:23]
	v_lshlrev_b32_e32 v24, 16, v12
	v_lshlrev_b32_e32 v25, 16, v13
	v_pk_fma_f32 v[28:29], v[80:81], v[20:21], v[28:29] neg_lo:[0,0,1] neg_hi:[0,0,1]
	v_pk_mul_f32 v[30:31], v[102:103], v[10:11]
	v_pk_mul_f32 v[20:21], v[100:101], v[20:21]
	v_pk_fma_f32 v[18:19], v[74:75], v[10:11], v[18:19]
	v_ashrrev_i32_e32 v10, 31, v53
	v_and_b32_e32 v12, 0xffff0000, v12
	v_and_b32_e32 v13, 0xffff0000, v13
	v_pk_fma_f32 v[30:31], v[74:75], v[22:23], v[30:31] neg_lo:[0,0,1] neg_hi:[0,0,1]
	v_pk_fma_f32 v[16:17], v[80:81], v[16:17], v[20:21]
	v_pk_mul_f32 v[20:21], v[104:105], v[24:25]
	v_mad_u64_u32 v[22:23], s[40:41], s58, v53, v[50:51]
	v_mul_lo_u32 v10, s58, v10
	v_mul_lo_u32 v11, s59, v53
	v_pk_mul_f32 v[32:33], v[104:105], v[12:13]
	v_pk_fma_f32 v[20:21], v[76:77], v[12:13], v[20:21]
	v_add3_u32 v23, v11, v23, v10
	v_mov_b32_e32 v10, v199
	v_mov_b32_e32 v11, v199
	v_mov_b32_e32 v12, v199
	v_mov_b32_e32 v13, v199
	v_cvt_pk_fp8_f32 v10, v26, v27
	v_cvt_pk_fp8_f32 v11, v30, v31
	v_cvt_pk_fp8_f32 v12, v14, v15
	v_cvt_pk_fp8_f32 v13, v18, v19
	v_pk_fma_f32 v[32:33], v[76:77], v[24:25], v[32:33] neg_lo:[0,0,1] neg_hi:[0,0,1]
	v_cvt_pk_fp8_f32 v10, v28, v29 op_sel:[0,0,1]
	v_cvt_pk_fp8_f32 v12, v16, v17 op_sel:[0,0,1]
	v_cvt_pk_fp8_f32 v11, v32, v33 op_sel:[0,0,1]
	v_cvt_pk_fp8_f32 v13, v20, v21 op_sel:[0,0,1]
	s_waitcnt vmcnt(6)
	v_lshlrev_b32_e32 v14, 16, v2
	v_permlane16_swap_b32_e32 v10, v12
	v_permlane16_swap_b32_e32 v11, v13
	global_store_dwordx4 v[22:23], v[10:13], off sc1
	v_lshlrev_b32_e32 v15, 16, v3
	v_and_b32_e32 v2, 0xffff0000, v2
	v_lshlrev_b32_e32 v10, 16, v6
	v_lshlrev_b32_e32 v11, 16, v7
	v_and_b32_e32 v6, 0xffff0000, v6
	v_and_b32_e32 v7, 0xffff0000, v7
	v_pk_mul_f32 v[18:19], v[82:83], v[6:7]
	v_lshlrev_b32_e32 v12, 16, v8
	v_lshlrev_b32_e32 v13, 16, v9
	v_and_b32_e32 v8, 0xffff0000, v8
	v_and_b32_e32 v9, 0xffff0000, v9
	v_pk_fma_f32 v[18:19], v[70:71], v[10:11], v[18:19] neg_lo:[0,0,1] neg_hi:[0,0,1]
	v_pk_mul_f32 v[10:11], v[82:83], v[10:11]
	v_and_b32_e32 v3, 0xffff0000, v3
	v_pk_mul_f32 v[20:21], v[84:85], v[8:9]
	v_pk_fma_f32 v[6:7], v[70:71], v[6:7], v[10:11]
	v_pk_mul_f32 v[10:11], v[86:87], v[14:15]
	v_lshlrev_b32_e32 v16, 16, v4
	v_lshlrev_b32_e32 v17, 16, v5
	v_pk_fma_f32 v[20:21], v[72:73], v[12:13], v[20:21] neg_lo:[0,0,1] neg_hi:[0,0,1]
	v_pk_mul_f32 v[22:23], v[86:87], v[2:3]
	v_pk_mul_f32 v[12:13], v[84:85], v[12:13]
	v_pk_fma_f32 v[10:11], v[66:67], v[2:3], v[10:11]
	v_ashrrev_i32_e32 v2, 31, v52
	v_and_b32_e32 v4, 0xffff0000, v4
	v_and_b32_e32 v5, 0xffff0000, v5
	v_pk_fma_f32 v[22:23], v[66:67], v[14:15], v[22:23] neg_lo:[0,0,1] neg_hi:[0,0,1]
	v_pk_fma_f32 v[8:9], v[72:73], v[8:9], v[12:13]
	v_pk_mul_f32 v[12:13], v[88:89], v[16:17]
	v_mad_u64_u32 v[14:15], s[40:41], s58, v52, v[50:51]
	v_mul_lo_u32 v2, s58, v2
	v_mul_lo_u32 v3, s59, v52
	v_pk_mul_f32 v[24:25], v[88:89], v[4:5]
	v_pk_fma_f32 v[12:13], v[68:69], v[4:5], v[12:13]
	v_add3_u32 v15, v3, v15, v2
	v_mov_b32_e32 v2, v199
	v_mov_b32_e32 v3, v199
	v_mov_b32_e32 v4, v199
	v_mov_b32_e32 v5, v199
	v_cvt_pk_fp8_f32 v2, v18, v19
	v_cvt_pk_fp8_f32 v3, v22, v23
	v_cvt_pk_fp8_f32 v4, v6, v7
	v_cvt_pk_fp8_f32 v5, v10, v11
	v_pk_fma_f32 v[24:25], v[68:69], v[16:17], v[24:25] neg_lo:[0,0,1] neg_hi:[0,0,1]
	v_cvt_pk_fp8_f32 v2, v20, v21 op_sel:[0,0,1]
	v_cvt_pk_fp8_f32 v4, v8, v9 op_sel:[0,0,1]
	v_cvt_pk_fp8_f32 v3, v24, v25 op_sel:[0,0,1]
	v_cvt_pk_fp8_f32 v5, v12, v13 op_sel:[0,0,1]
	v_permlane16_swap_b32_e32 v2, v4
	s_nop 0
	v_permlane16_swap_b32_e32 v3, v5
	global_store_dwordx4 v[14:15], v[2:5], off sc1
	s_and_b64 vcc, exec, s[4:5]
	s_mov_b64 s[4:5], -1
	s_cbranch_vccnz .LBB0_118

.LBB0_493:
	s_lshl_b32 s2, s79, 8
	s_add_i32 s28, s2, s59
	s_add_i32 s26, s62, s52
	s_ashr_i32 s2, s28, 4
	s_ashr_i32 s27, s26, 31
	s_lshl_b64 s[26:27], s[26:27], 10
	s_ashr_i32 s3, s2, 31
	v_lshl_add_u64 v[2:3], v[202:203], 0, s[26:27]
	s_lshl_b64 s[26:27], s[2:3], 15
	v_lshl_add_u64 v[4:5], v[2:3], 0, s[26:27]
	s_or_b32 s26, s2, 1
	s_ashr_i32 s27, s26, 31
	s_lshl_b64 s[26:27], s[26:27], 15
	v_lshl_add_u64 v[6:7], v[2:3], 0, s[26:27]
	s_or_b32 s26, s2, 2
	s_or_b32 s2, s2, 3
	s_ashr_i32 s27, s26, 31
	s_ashr_i32 s3, s2, 31
	s_waitcnt vmcnt(0)
	s_lshl_b64 s[26:27], s[26:27], 15
	s_lshl_b64 s[2:3], s[2:3], 15
	global_load_dwordx4 v[22:25], v[4:5], off
	global_load_dwordx4 v[26:29], v[6:7], off
	v_lshl_add_u64 v[6:7], v[2:3], 0, s[26:27]
	v_lshl_add_u64 v[2:3], v[2:3], 0, s[2:3]
	global_load_dwordx4 v[30:33], v[6:7], off
	global_load_dwordx4 v[18:21], v[2:3], off
	v_add_co_u32_e32 v2, vcc, s1, v4
	s_waitcnt vmcnt(0)
	v_mov_b32_e32 v34, v24
	v_addc_co_u32_e32 v3, vcc, 0, v5, vcc
	v_add_co_u32_e32 v6, vcc, s64, v4
	v_mov_b32_e32 v36, v25
	s_nop 0
	v_addc_co_u32_e32 v7, vcc, 0, v5, vcc
	global_load_dwordx4 v[14:17], v[2:3], off
	global_load_dwordx4 v[10:13], v[6:7], off
	v_add_co_u32_e32 v2, vcc, s54, v4
	v_permlane16_swap_b32_e32 v22, v34
	s_nop 0
	v_addc_co_u32_e32 v3, vcc, 0, v5, vcc
	global_load_dwordx4 v[6:9], v[2:3], off
	v_add_co_u32_e32 v2, vcc, s65, v4
	v_permlane16_swap_b32_e32 v23, v36
	s_nop 0
	v_addc_co_u32_e32 v3, vcc, 0, v5, vcc
	global_load_dwordx4 v[2:5], v[2:3], off
	v_mov_b32_e32 v44, v20
	v_mov_b32_e32 v45, v21
	v_cvt_pk_f32_fp8_sdwa v[20:21], v22 src0_sel:WORD_1
	v_cvt_pk_f32_fp8_e32 v[24:25], v23
	v_mov_b32_e32 v40, v28
	v_mov_b32_e32 v41, v29
	v_pk_mul_f32 v[20:21], v[20:21], s[0:1] op_sel_hi:[1,0]
	v_mov_b32_e32 v42, v32
	v_pk_mul_f32 v[28:29], v[192:193], v[20:21]
	v_pk_mul_f32 v[20:21], v[24:25], s[0:1] op_sel_hi:[1,0]
	v_mov_b32_e32 v43, v33
	v_cvt_pk_f32_fp8_sdwa v[32:33], v34 src0_sel:WORD_1
	v_permlane16_swap_b32_e32 v26, v40
	v_pk_mul_f32 v[32:33], v[32:33], s[0:1] op_sel_hi:[1,0]
	v_permlane16_swap_b32_e32 v27, v41
	v_pk_mul_f32 v[32:33], v[184:185], v[32:33]
	v_permlane16_swap_b32_e32 v30, v42
	v_permlane16_swap_b32_e32 v31, v43
	v_permlane16_swap_b32_e32 v18, v44
	v_permlane16_swap_b32_e32 v19, v45
	s_and_b64 vcc, exec, s[4:5]
	s_mov_b64 s[4:5], -1
	s_waitcnt vmcnt(3)
	v_mov_b32_e32 v46, v16
	v_mov_b32_e32 v47, v17
	v_cvt_pk_f32_fp8_e32 v[16:17], v22
	v_cvt_pk_f32_fp8_sdwa v[22:23], v23 src0_sel:WORD_1
	s_waitcnt vmcnt(2)
	v_mov_b32_e32 v48, v12
	v_mov_b32_e32 v49, v13
	v_pk_mul_f32 v[16:17], v[16:17], s[0:1] op_sel_hi:[1,0]
	v_pk_mul_f32 v[22:23], v[22:23], s[0:1] op_sel_hi:[1,0]
	v_pk_mul_f32 v[16:17], v[190:191], v[16:17]
	v_pk_mul_f32 v[24:25], v[188:189], v[22:23]
	v_pk_mul_f32 v[22:23], v[186:187], v[20:21]
	v_cvt_pk_f32_fp8_e32 v[20:21], v34
	v_cvt_pk_f32_fp8_e32 v[34:35], v36
	v_cvt_pk_f32_fp8_sdwa v[36:37], v36 src0_sel:WORD_1
	s_waitcnt vmcnt(1)
	v_mov_b32_e32 v50, v8
	v_pk_mul_f32 v[20:21], v[20:21], s[0:1] op_sel_hi:[1,0]
	v_or_b32_e32 v8, s28, v217
	v_pk_mul_f32 v[38:39], v[182:183], v[20:21]
	v_pk_mul_f32 v[20:21], v[34:35], s[0:1] op_sel_hi:[1,0]
	v_pk_mul_f32 v[34:35], v[36:37], s[0:1] op_sel_hi:[1,0]
	v_pk_mul_f32 v[36:37], v[178:179], v[20:21]
	v_mov_b32_e32 v21, v199
	v_mov_b32_e32 v20, v199
	v_cvt_pk_fp8_f32 v21, v22, v23
	v_mov_b32_e32 v22, v199
	v_mov_b32_e32 v23, v199
	v_cvt_pk_fp8_f32 v20, v16, v17
	v_cvt_pk_fp8_f32 v22, v38, v39
	v_cvt_pk_fp8_f32 v23, v36, v37
	v_mov_b32_e32 v51, v9
	v_pk_mul_f32 v[34:35], v[180:181], v[34:35]
	v_ashrrev_i32_e32 v9, 31, v8
	s_waitcnt vmcnt(0)
	v_mov_b32_e32 v12, v4
	v_lshl_or_b32 v4, s78, 8, v221
	v_cvt_pk_fp8_f32 v20, v28, v29 op_sel:[0,0,1]
	v_cvt_pk_fp8_f32 v21, v24, v25 op_sel:[0,0,1]
	v_cvt_pk_fp8_f32 v22, v32, v33 op_sel:[0,0,1]
	v_cvt_pk_fp8_f32 v23, v34, v35 op_sel:[0,0,1]
	v_lshlrev_b64 v[16:17], 10, v[8:9]
	v_mov_b32_e32 v13, v5
	v_ashrrev_i32_e32 v5, 31, v4
	v_lshl_add_u64 v[16:17], s[14:15], 0, v[16:17]
	v_lshl_add_u64 v[16:17], v[16:17], 0, v[4:5]
	v_lshl_add_u64 v[16:17], v[16:17], 0, v[204:205]
	v_lshl_add_u64 v[16:17], v[16:17], 0, v[206:207]
	v_permlane16_swap_b32_e32 v20, v22
	v_permlane16_swap_b32_e32 v21, v23
	global_store_dwordx4 v[16:17], v[20:23], off sc1
	v_cvt_pk_f32_fp8_sdwa v[24:25], v27 src0_sel:WORD_1
	v_cvt_pk_f32_fp8_e32 v[16:17], v26
	v_cvt_pk_f32_fp8_sdwa v[20:21], v26 src0_sel:WORD_1
	v_cvt_pk_f32_fp8_e32 v[22:23], v27
	v_cvt_pk_f32_fp8_e32 v[32:33], v41
	v_cvt_pk_f32_fp8_sdwa v[34:35], v41 src0_sel:WORD_1
	v_pk_mul_f32 v[20:21], v[20:21], s[0:1] op_sel_hi:[1,0]
	v_pk_mul_f32 v[16:17], v[16:17], s[0:1] op_sel_hi:[1,0]
	v_pk_mul_f32 v[26:27], v[176:177], v[20:21]
	v_pk_mul_f32 v[20:21], v[22:23], s[0:1] op_sel_hi:[1,0]
	v_pk_mul_f32 v[22:23], v[24:25], s[0:1] op_sel_hi:[1,0]
	v_cvt_pk_f32_fp8_sdwa v[28:29], v40 src0_sel:WORD_1
	v_pk_mul_f32 v[24:25], v[172:173], v[22:23]
	v_pk_mul_f32 v[22:23], v[170:171], v[20:21]
	v_cvt_pk_f32_fp8_e32 v[20:21], v40
	v_pk_mul_f32 v[16:17], v[174:175], v[16:17]
	v_pk_mul_f32 v[28:29], v[28:29], s[0:1] op_sel_hi:[1,0]
	v_permlane16_swap_b32_e32 v14, v46
	v_pk_mul_f32 v[20:21], v[20:21], s[0:1] op_sel_hi:[1,0]
	v_pk_mul_f32 v[28:29], v[168:169], v[28:29]
	v_pk_mul_f32 v[36:37], v[166:167], v[20:21]
	v_pk_mul_f32 v[20:21], v[32:33], s[0:1] op_sel_hi:[1,0]
	v_pk_mul_f32 v[32:33], v[34:35], s[0:1] op_sel_hi:[1,0]
	v_pk_mul_f32 v[34:35], v[162:163], v[20:21]
	v_mov_b32_e32 v21, v199
	v_mov_b32_e32 v20, v199
	v_cvt_pk_fp8_f32 v21, v22, v23
	v_mov_b32_e32 v22, v199
	v_mov_b32_e32 v23, v199
	v_cvt_pk_fp8_f32 v20, v16, v17
	v_cvt_pk_fp8_f32 v22, v36, v37
	v_cvt_pk_fp8_f32 v23, v34, v35
	v_or_b32_e32 v16, 16, v8
	v_pk_mul_f32 v[32:33], v[164:165], v[32:33]
	v_ashrrev_i32_e32 v17, 31, v16
	v_cvt_pk_fp8_f32 v20, v26, v27 op_sel:[0,0,1]
	v_cvt_pk_fp8_f32 v21, v24, v25 op_sel:[0,0,1]
	v_cvt_pk_fp8_f32 v22, v28, v29 op_sel:[0,0,1]
	v_cvt_pk_fp8_f32 v23, v32, v33 op_sel:[0,0,1]
	v_lshlrev_b64 v[16:17], 10, v[16:17]
	v_lshl_add_u64 v[16:17], s[14:15], 0, v[16:17]
	v_lshl_add_u64 v[16:17], v[16:17], 0, v[4:5]
	v_lshl_add_u64 v[16:17], v[16:17], 0, v[204:205]
	v_lshl_add_u64 v[16:17], v[16:17], 0, v[206:207]
	v_permlane16_swap_b32_e32 v20, v22
	v_permlane16_swap_b32_e32 v21, v23
	global_store_dwordx4 v[16:17], v[20:23], off sc1
	v_cvt_pk_f32_fp8_sdwa v[24:25], v31 src0_sel:WORD_1
	v_cvt_pk_f32_fp8_e32 v[16:17], v30
	v_cvt_pk_f32_fp8_sdwa v[20:21], v30 src0_sel:WORD_1
	v_cvt_pk_f32_fp8_e32 v[22:23], v31
	v_cvt_pk_f32_fp8_e32 v[30:31], v43
	v_cvt_pk_f32_fp8_sdwa v[32:33], v43 src0_sel:WORD_1
	v_pk_mul_f32 v[20:21], v[20:21], s[0:1] op_sel_hi:[1,0]
	v_pk_mul_f32 v[16:17], v[16:17], s[0:1] op_sel_hi:[1,0]
	v_pk_mul_f32 v[26:27], v[160:161], v[20:21]
	v_pk_mul_f32 v[20:21], v[22:23], s[0:1] op_sel_hi:[1,0]
	v_pk_mul_f32 v[22:23], v[24:25], s[0:1] op_sel_hi:[1,0]
	v_cvt_pk_f32_fp8_sdwa v[28:29], v42 src0_sel:WORD_1
	v_pk_mul_f32 v[24:25], v[156:157], v[22:23]
	v_pk_mul_f32 v[22:23], v[154:155], v[20:21]
	v_cvt_pk_f32_fp8_e32 v[20:21], v42
	v_pk_mul_f32 v[16:17], v[158:159], v[16:17]
	v_pk_mul_f32 v[28:29], v[28:29], s[0:1] op_sel_hi:[1,0]
	v_permlane16_swap_b32_e32 v15, v47
	v_pk_mul_f32 v[20:21], v[20:21], s[0:1] op_sel_hi:[1,0]
	v_pk_mul_f32 v[28:29], v[152:153], v[28:29]
	v_pk_mul_f32 v[34:35], v[150:151], v[20:21]
	v_pk_mul_f32 v[20:21], v[30:31], s[0:1] op_sel_hi:[1,0]
	v_pk_mul_f32 v[30:31], v[32:33], s[0:1] op_sel_hi:[1,0]
	v_pk_mul_f32 v[32:33], v[146:147], v[20:21]
	v_mov_b32_e32 v21, v199
	v_mov_b32_e32 v20, v199
	v_cvt_pk_fp8_f32 v21, v22, v23
	v_mov_b32_e32 v22, v199
	v_mov_b32_e32 v23, v199
	v_cvt_pk_fp8_f32 v20, v16, v17
	v_cvt_pk_fp8_f32 v22, v34, v35
	v_cvt_pk_fp8_f32 v23, v32, v33
	v_or_b32_e32 v16, 32, v8
	v_pk_mul_f32 v[30:31], v[148:149], v[30:31]
	v_ashrrev_i32_e32 v17, 31, v16
	v_cvt_pk_fp8_f32 v20, v26, v27 op_sel:[0,0,1]
	v_cvt_pk_fp8_f32 v21, v24, v25 op_sel:[0,0,1]
	v_cvt_pk_fp8_f32 v22, v28, v29 op_sel:[0,0,1]
	v_cvt_pk_fp8_f32 v23, v30, v31 op_sel:[0,0,1]
	v_lshlrev_b64 v[16:17], 10, v[16:17]
	v_lshl_add_u64 v[16:17], s[14:15], 0, v[16:17]
	v_lshl_add_u64 v[16:17], v[16:17], 0, v[4:5]
	v_lshl_add_u64 v[16:17], v[16:17], 0, v[204:205]
	v_lshl_add_u64 v[16:17], v[16:17], 0, v[206:207]
	v_permlane16_swap_b32_e32 v20, v22
	v_permlane16_swap_b32_e32 v21, v23
	global_store_dwordx4 v[16:17], v[20:23], off sc1
	v_cvt_pk_f32_fp8_e32 v[16:17], v18
	v_cvt_pk_f32_fp8_e32 v[28:29], v45
	v_cvt_pk_f32_fp8_sdwa v[20:21], v18 src0_sel:WORD_1
	v_cvt_pk_f32_fp8_e32 v[22:23], v19
	v_cvt_pk_f32_fp8_sdwa v[18:19], v19 src0_sel:WORD_1
	v_pk_mul_f32 v[16:17], v[16:17], s[0:1] op_sel_hi:[1,0]
	v_cvt_pk_f32_fp8_sdwa v[30:31], v45 src0_sel:WORD_1
	v_pk_mul_f32 v[24:25], v[142:143], v[16:17]
	v_pk_mul_f32 v[16:17], v[22:23], s[0:1] op_sel_hi:[1,0]
	v_pk_mul_f32 v[18:19], v[18:19], s[0:1] op_sel_hi:[1,0]
	v_cvt_pk_f32_fp8_sdwa v[26:27], v44 src0_sel:WORD_1
	v_pk_mul_f32 v[22:23], v[140:141], v[18:19]
	v_pk_mul_f32 v[18:19], v[138:139], v[16:17]
	v_cvt_pk_f32_fp8_e32 v[16:17], v44
	v_pk_mul_f32 v[20:21], v[20:21], s[0:1] op_sel_hi:[1,0]
	v_pk_mul_f32 v[26:27], v[26:27], s[0:1] op_sel_hi:[1,0]
	v_pk_mul_f32 v[20:21], v[144:145], v[20:21]
	v_pk_mul_f32 v[16:17], v[16:17], s[0:1] op_sel_hi:[1,0]
	v_pk_mul_f32 v[26:27], v[136:137], v[26:27]
	v_pk_mul_f32 v[32:33], v[134:135], v[16:17]
	v_pk_mul_f32 v[16:17], v[28:29], s[0:1] op_sel_hi:[1,0]
	v_pk_mul_f32 v[28:29], v[30:31], s[0:1] op_sel_hi:[1,0]
	v_pk_mul_f32 v[30:31], v[130:131], v[16:17]
	v_mov_b32_e32 v16, v199
	v_cvt_pk_fp8_f32 v16, v24, v25
	v_mov_b32_e32 v17, v199
	v_cvt_pk_fp8_f32 v17, v18, v19
	v_mov_b32_e32 v18, v199
	v_mov_b32_e32 v19, v199
	v_cvt_pk_fp8_f32 v18, v32, v33
	v_cvt_pk_fp8_f32 v19, v30, v31
	v_cvt_pk_fp8_f32 v16, v20, v21 op_sel:[0,0,1]
	v_or_b32_e32 v20, 48, v8
	v_pk_mul_f32 v[28:29], v[132:133], v[28:29]
	v_ashrrev_i32_e32 v21, 31, v20
	v_cvt_pk_fp8_f32 v17, v22, v23 op_sel:[0,0,1]
	v_cvt_pk_fp8_f32 v18, v26, v27 op_sel:[0,0,1]
	v_cvt_pk_fp8_f32 v19, v28, v29 op_sel:[0,0,1]
	v_lshlrev_b64 v[20:21], 10, v[20:21]
	v_lshl_add_u64 v[20:21], s[14:15], 0, v[20:21]
	v_lshl_add_u64 v[20:21], v[20:21], 0, v[4:5]
	v_lshl_add_u64 v[20:21], v[20:21], 0, v[204:205]
	v_lshl_add_u64 v[20:21], v[20:21], 0, v[206:207]
	v_permlane16_swap_b32_e32 v16, v18
	v_permlane16_swap_b32_e32 v17, v19
	global_store_dwordx4 v[20:21], v[16:19], off sc1
	v_cvt_pk_f32_fp8_sdwa v[20:21], v14 src0_sel:WORD_1
	v_cvt_pk_f32_fp8_e32 v[22:23], v15
	v_cvt_pk_f32_fp8_e32 v[16:17], v14
	v_cvt_pk_f32_fp8_sdwa v[14:15], v15 src0_sel:WORD_1
	v_cvt_pk_f32_fp8_e32 v[28:29], v47
	v_cvt_pk_f32_fp8_sdwa v[30:31], v47 src0_sel:WORD_1
	v_pk_mul_f32 v[16:17], v[16:17], s[0:1] op_sel_hi:[1,0]
	v_pk_mul_f32 v[14:15], v[14:15], s[0:1] op_sel_hi:[1,0]
	v_pk_mul_f32 v[16:17], v[126:127], v[16:17]
	v_pk_mul_f32 v[24:25], v[124:125], v[14:15]
	v_cvt_pk_f32_fp8_e32 v[14:15], v46
	v_pk_mul_f32 v[22:23], v[22:23], s[0:1] op_sel_hi:[1,0]
	v_cvt_pk_f32_fp8_sdwa v[26:27], v46 src0_sel:WORD_1
	v_pk_mul_f32 v[22:23], v[122:123], v[22:23]
	v_pk_mul_f32 v[14:15], v[14:15], s[0:1] op_sel_hi:[1,0]
	v_add_u32_e32 v18, 0x80, v8
	v_pk_mul_f32 v[32:33], v[118:119], v[14:15]
	v_pk_mul_f32 v[14:15], v[28:29], s[0:1] op_sel_hi:[1,0]
	v_pk_mul_f32 v[28:29], v[30:31], s[0:1] op_sel_hi:[1,0]
	v_pk_mul_f32 v[30:31], v[114:115], v[14:15]
	v_mov_b32_e32 v14, v199
	v_cvt_pk_fp8_f32 v14, v16, v17
	v_mov_b32_e32 v15, v199
	v_mov_b32_e32 v16, v199
	v_mov_b32_e32 v17, v199
	v_cvt_pk_fp8_f32 v15, v22, v23
	v_cvt_pk_fp8_f32 v16, v32, v33
	v_cvt_pk_fp8_f32 v17, v30, v31
	v_pk_mul_f32 v[20:21], v[20:21], s[0:1] op_sel_hi:[1,0]
	v_pk_mul_f32 v[26:27], v[26:27], s[0:1] op_sel_hi:[1,0]
	v_pk_mul_f32 v[20:21], v[128:129], v[20:21]
	v_pk_mul_f32 v[26:27], v[120:121], v[26:27]
	v_pk_mul_f32 v[28:29], v[116:117], v[28:29]
	v_ashrrev_i32_e32 v19, 31, v18
	v_cvt_pk_fp8_f32 v14, v20, v21 op_sel:[0,0,1]
	v_cvt_pk_fp8_f32 v15, v24, v25 op_sel:[0,0,1]
	v_cvt_pk_fp8_f32 v16, v26, v27 op_sel:[0,0,1]
	v_cvt_pk_fp8_f32 v17, v28, v29 op_sel:[0,0,1]
	v_lshlrev_b64 v[18:19], 10, v[18:19]
	v_lshl_add_u64 v[18:19], s[14:15], 0, v[18:19]
	v_lshl_add_u64 v[18:19], v[18:19], 0, v[4:5]
	v_lshl_add_u64 v[18:19], v[18:19], 0, v[204:205]
	v_permlane16_swap_b32_e32 v10, v48
	v_lshl_add_u64 v[18:19], v[18:19], 0, v[206:207]
	v_permlane16_swap_b32_e32 v14, v16
	v_permlane16_swap_b32_e32 v15, v17
	v_permlane16_swap_b32_e32 v11, v49
	global_store_dwordx4 v[18:19], v[14:17], off sc1
	v_cvt_pk_f32_fp8_e32 v[18:19], v11
	v_cvt_pk_f32_fp8_e32 v[24:25], v49
	v_cvt_pk_f32_fp8_e32 v[14:15], v10
	v_cvt_pk_f32_fp8_sdwa v[16:17], v10 src0_sel:WORD_1
	v_cvt_pk_f32_fp8_sdwa v[26:27], v49 src0_sel:WORD_1
	v_cvt_pk_f32_fp8_sdwa v[10:11], v11 src0_sel:WORD_1
	v_pk_mul_f32 v[14:15], v[14:15], s[0:1] op_sel_hi:[1,0]
	v_pk_mul_f32 v[16:17], v[16:17], s[0:1] op_sel_hi:[1,0]
	v_cvt_pk_f32_fp8_sdwa v[22:23], v48 src0_sel:WORD_1
	v_pk_mul_f32 v[20:21], v[112:113], v[16:17]
	v_pk_mul_f32 v[16:17], v[110:111], v[14:15]
	v_pk_mul_f32 v[14:15], v[18:19], s[0:1] op_sel_hi:[1,0]
	v_pk_mul_f32 v[10:11], v[10:11], s[0:1] op_sel_hi:[1,0]
	v_pk_mul_f32 v[18:19], v[106:107], v[14:15]
	v_cvt_pk_f32_fp8_e32 v[14:15], v48
	v_pk_mul_f32 v[10:11], v[108:109], v[10:11]
	v_pk_mul_f32 v[22:23], v[22:23], s[0:1] op_sel_hi:[1,0]
	v_permlane16_swap_b32_e32 v6, v50
	v_pk_mul_f32 v[14:15], v[14:15], s[0:1] op_sel_hi:[1,0]
	v_pk_mul_f32 v[22:23], v[104:105], v[22:23]
	v_pk_mul_f32 v[28:29], v[102:103], v[14:15]
	v_pk_mul_f32 v[14:15], v[24:25], s[0:1] op_sel_hi:[1,0]
	v_pk_mul_f32 v[24:25], v[26:27], s[0:1] op_sel_hi:[1,0]
	v_pk_mul_f32 v[26:27], v[98:99], v[14:15]
	v_mov_b32_e32 v15, v199
	v_mov_b32_e32 v14, v199
	v_cvt_pk_fp8_f32 v15, v18, v19
	v_cvt_pk_fp8_f32 v14, v16, v17
	v_mov_b32_e32 v16, v199
	v_mov_b32_e32 v17, v199
	v_cvt_pk_fp8_f32 v16, v28, v29
	v_cvt_pk_fp8_f32 v17, v26, v27
	v_cvt_pk_fp8_f32 v15, v10, v11 op_sel:[0,0,1]
	v_add_u32_e32 v10, 0x90, v8
	v_pk_mul_f32 v[24:25], v[100:101], v[24:25]
	v_ashrrev_i32_e32 v11, 31, v10
	v_cvt_pk_fp8_f32 v14, v20, v21 op_sel:[0,0,1]
	v_cvt_pk_fp8_f32 v16, v22, v23 op_sel:[0,0,1]
	v_cvt_pk_fp8_f32 v17, v24, v25 op_sel:[0,0,1]
	v_lshlrev_b64 v[10:11], 10, v[10:11]
	v_lshl_add_u64 v[10:11], s[14:15], 0, v[10:11]
	v_lshl_add_u64 v[10:11], v[10:11], 0, v[4:5]
	v_lshl_add_u64 v[10:11], v[10:11], 0, v[204:205]
	v_lshl_add_u64 v[10:11], v[10:11], 0, v[206:207]
	v_permlane16_swap_b32_e32 v14, v16
	v_permlane16_swap_b32_e32 v15, v17
	v_permlane16_swap_b32_e32 v7, v51
	global_store_dwordx4 v[10:11], v[14:17], off sc1
	v_cvt_pk_f32_fp8_e32 v[22:23], v51
	v_cvt_pk_f32_fp8_sdwa v[24:25], v51 src0_sel:WORD_1
	v_cvt_pk_f32_fp8_sdwa v[14:15], v6 src0_sel:WORD_1
	v_cvt_pk_f32_fp8_e32 v[16:17], v7
	v_cvt_pk_f32_fp8_e32 v[10:11], v6
	v_cvt_pk_f32_fp8_sdwa v[6:7], v7 src0_sel:WORD_1
	v_pk_mul_f32 v[14:15], v[14:15], s[0:1] op_sel_hi:[1,0]
	v_cvt_pk_f32_fp8_sdwa v[20:21], v50 src0_sel:WORD_1
	v_pk_mul_f32 v[18:19], v[88:89], v[14:15]
	v_pk_mul_f32 v[14:15], v[16:17], s[0:1] op_sel_hi:[1,0]
	v_pk_mul_f32 v[10:11], v[10:11], s[0:1] op_sel_hi:[1,0]
	v_pk_mul_f32 v[16:17], v[82:83], v[14:15]
	v_cvt_pk_f32_fp8_e32 v[14:15], v50
	v_pk_mul_f32 v[10:11], v[86:87], v[10:11]
	v_pk_mul_f32 v[6:7], v[6:7], s[0:1] op_sel_hi:[1,0]
	v_pk_mul_f32 v[20:21], v[20:21], s[0:1] op_sel_hi:[1,0]
	v_pk_mul_f32 v[14:15], v[14:15], s[0:1] op_sel_hi:[1,0]
	v_pk_mul_f32 v[6:7], v[84:85], v[6:7]
	v_pk_mul_f32 v[26:27], v[94:95], v[14:15]
	v_pk_mul_f32 v[14:15], v[22:23], s[0:1] op_sel_hi:[1,0]
	v_pk_mul_f32 v[22:23], v[24:25], s[0:1] op_sel_hi:[1,0]
	v_pk_mul_f32 v[24:25], v[90:91], v[14:15]
	v_mov_b32_e32 v15, v199
	v_cvt_pk_fp8_f32 v15, v16, v17
	v_mov_b32_e32 v14, v199
	v_mov_b32_e32 v16, v199
	v_mov_b32_e32 v17, v199
	v_cvt_pk_fp8_f32 v14, v10, v11
	v_cvt_pk_fp8_f32 v16, v26, v27
	v_cvt_pk_fp8_f32 v17, v24, v25
	v_cvt_pk_fp8_f32 v15, v6, v7 op_sel:[0,0,1]
	v_add_u32_e32 v6, 0xa0, v8
	v_pk_mul_f32 v[20:21], v[96:97], v[20:21]
	v_pk_mul_f32 v[22:23], v[92:93], v[22:23]
	v_ashrrev_i32_e32 v7, 31, v6
	v_cvt_pk_fp8_f32 v14, v18, v19 op_sel:[0,0,1]
	v_cvt_pk_fp8_f32 v16, v20, v21 op_sel:[0,0,1]
	v_cvt_pk_fp8_f32 v17, v22, v23 op_sel:[0,0,1]
	v_lshlrev_b64 v[6:7], 10, v[6:7]
	v_lshl_add_u64 v[6:7], s[14:15], 0, v[6:7]
	v_lshl_add_u64 v[6:7], v[6:7], 0, v[4:5]
	v_permlane16_swap_b32_e32 v2, v12
	v_lshl_add_u64 v[6:7], v[6:7], 0, v[204:205]
	v_permlane16_swap_b32_e32 v3, v13
	v_lshl_add_u64 v[6:7], v[6:7], 0, v[206:207]
	v_permlane16_swap_b32_e32 v14, v16
	v_permlane16_swap_b32_e32 v15, v17
	v_cvt_pk_f32_fp8_sdwa v[10:11], v2 src0_sel:WORD_1
	global_store_dwordx4 v[6:7], v[14:17], off sc1
	v_cvt_pk_f32_fp8_e32 v[20:21], v13
	v_cvt_pk_f32_fp8_e32 v[6:7], v2
	v_cvt_pk_f32_fp8_e32 v[14:15], v3
	v_pk_mul_f32 v[10:11], v[10:11], s[0:1] op_sel_hi:[1,0]
	v_cvt_pk_f32_fp8_sdwa v[18:19], v12 src0_sel:WORD_1
	v_pk_mul_f32 v[16:17], v[72:73], v[10:11]
	v_pk_mul_f32 v[10:11], v[14:15], s[0:1] op_sel_hi:[1,0]
	v_cvt_pk_f32_fp8_sdwa v[2:3], v3 src0_sel:WORD_1
	v_pk_mul_f32 v[14:15], v[66:67], v[10:11]
	v_cvt_pk_f32_fp8_e32 v[10:11], v12
	v_cvt_pk_f32_fp8_sdwa v[12:13], v13 src0_sel:WORD_1
	v_pk_mul_f32 v[6:7], v[6:7], s[0:1] op_sel_hi:[1,0]
	v_pk_mul_f32 v[2:3], v[2:3], s[0:1] op_sel_hi:[1,0]
	v_pk_mul_f32 v[10:11], v[10:11], s[0:1] op_sel_hi:[1,0]
	v_pk_mul_f32 v[12:13], v[12:13], s[0:1] op_sel_hi:[1,0]
	v_pk_mul_f32 v[22:23], v[78:79], v[10:11]
	v_pk_mul_f32 v[10:11], v[20:21], s[0:1] op_sel_hi:[1,0]
	v_pk_mul_f32 v[6:7], v[70:71], v[6:7]
	v_pk_mul_f32 v[24:25], v[74:75], v[10:11]
	v_mov_b32_e32 v11, v199
	v_cvt_pk_fp8_f32 v11, v14, v15
	v_pk_mul_f32 v[20:21], v[76:77], v[12:13]
	v_mov_b32_e32 v10, v199
	v_mov_b32_e32 v12, v199
	v_mov_b32_e32 v13, v199
	v_cvt_pk_fp8_f32 v10, v6, v7
	v_cvt_pk_fp8_f32 v12, v22, v23
	v_cvt_pk_fp8_f32 v13, v24, v25
	v_pk_mul_f32 v[2:3], v[68:69], v[2:3]
	v_pk_mul_f32 v[18:19], v[18:19], s[0:1] op_sel_hi:[1,0]
	v_cvt_pk_fp8_f32 v11, v2, v3 op_sel:[0,0,1]
	v_add_u32_e32 v2, 0xb0, v8
	v_pk_mul_f32 v[18:19], v[80:81], v[18:19]
	v_ashrrev_i32_e32 v3, 31, v2
	v_cvt_pk_fp8_f32 v10, v16, v17 op_sel:[0,0,1]
	v_cvt_pk_fp8_f32 v12, v18, v19 op_sel:[0,0,1]
	v_cvt_pk_fp8_f32 v13, v20, v21 op_sel:[0,0,1]
	v_lshlrev_b64 v[2:3], 10, v[2:3]
	v_lshl_add_u64 v[2:3], s[14:15], 0, v[2:3]
	v_lshl_add_u64 v[2:3], v[2:3], 0, v[4:5]
	v_lshl_add_u64 v[2:3], v[2:3], 0, v[204:205]
	v_lshl_add_u64 v[2:3], v[2:3], 0, v[206:207]
	v_permlane16_swap_b32_e32 v10, v12
	v_permlane16_swap_b32_e32 v11, v13
	global_store_dwordx4 v[2:3], v[10:13], off sc1
	s_cbranch_vccnz .LBB0_470
	s_andn2_b64 vcc, exec, s[10:11]
	s_cbranch_vccnz .LBB0_469
	s_barrier
	s_branch .LBB0_469

.LBB0_579:
	s_lshl_b32 s2, s57, 8
	s_add_i32 s2, s2, s59
	s_lshl_b32 s36, s34, 8
	v_or_b32_e32 v2, s36, v222
	v_or_b32_e32 v212, s2, v219
	v_ashrrev_i32_e32 v3, 31, v2
	v_ashrrev_i32_e32 v213, 31, v212
	v_lshl_add_u64 v[214:215], v[2:3], 2, s[80:81]
	v_lshlrev_b64 v[2:3], 12, v[212:213]
	v_or_b32_e32 v210, 16, v212
	v_or_b32_e32 v208, 32, v212
	s_waitcnt vmcnt(0)
	v_lshl_add_u64 v[6:7], v[214:215], 0, v[2:3]
	v_or_b32_e32 v206, 48, v212
	v_ashrrev_i32_e32 v211, 31, v210
	v_ashrrev_i32_e32 v209, 31, v208
	global_load_dwordx4 v[2:5], v[6:7], off nt
	global_load_dwordx4 v[54:57], v[6:7], off offset:64 nt
	global_load_dwordx4 v[58:61], v[6:7], off offset:128 nt
	global_load_dwordx4 v[62:65], v[6:7], off offset:192 nt
	v_ashrrev_i32_e32 v207, 31, v206
	v_lshlrev_b64 v[6:7], 12, v[210:211]
	v_lshlrev_b64 v[8:9], 12, v[208:209]
	v_lshlrev_b64 v[10:11], 12, v[206:207]
	v_lshl_add_u64 v[6:7], v[214:215], 0, v[6:7]
	v_lshl_add_u64 v[8:9], v[214:215], 0, v[8:9]
	v_lshl_add_u64 v[226:227], v[214:215], 0, v[10:11]
	global_load_dwordx4 v[22:25], v[6:7], off nt
	global_load_dwordx4 v[50:53], v[6:7], off offset:64 nt
	global_load_dwordx4 v[46:49], v[6:7], off offset:128 nt
	global_load_dwordx4 v[42:45], v[6:7], off offset:192 nt
	global_load_dwordx4 v[38:41], v[8:9], off nt
	global_load_dwordx4 v[34:37], v[8:9], off offset:64 nt
	global_load_dwordx4 v[30:33], v[8:9], off offset:128 nt
	global_load_dwordx4 v[26:29], v[8:9], off offset:192 nt
	global_load_dwordx4 v[18:21], v[226:227], off nt
	global_load_dwordx4 v[14:17], v[226:227], off offset:64 nt
	global_load_dwordx4 v[10:13], v[226:227], off offset:128 nt
	s_nop 0
	global_load_dwordx4 v[6:9], v[226:227], off offset:192 nt
	s_lshl_b32 s34, s34, 2
	s_ashr_i32 s35, s34, 31
	s_or_b64 s[34:35], s[34:35], s[12:13]
	s_waitcnt vmcnt(0)
	v_pk_mul_f32 v[4:5], v[4:5], s[24:25] op_sel_hi:[1,0]
	v_pk_mul_f32 v[2:3], v[2:3], s[24:25] op_sel_hi:[1,0]
	v_pk_mul_f32 v[56:57], v[56:57], s[24:25] op_sel_hi:[1,0]
	v_pk_mul_f32 v[54:55], v[54:55], s[24:25] op_sel_hi:[1,0]
	v_pk_mul_f32 v[60:61], v[60:61], s[24:25] op_sel_hi:[1,0]
	v_pk_fma_f32 v[4:5], v[192:193], s[26:27], v[4:5] op_sel_hi:[1,0,1]
	v_pk_fma_f32 v[2:3], v[190:191], s[26:27], v[2:3] op_sel_hi:[1,0,1]
	v_pk_fma_f32 v[188:189], v[188:189], s[26:27], v[56:57] op_sel_hi:[1,0,1]
	v_pk_fma_f32 v[186:187], v[186:187], s[26:27], v[54:55] op_sel_hi:[1,0,1]
	v_pk_mul_f32 v[58:59], v[58:59], s[24:25] op_sel_hi:[1,0]
	v_pk_fma_f32 v[184:185], v[184:185], s[26:27], v[60:61] op_sel_hi:[1,0,1]
	v_add_f32_e32 v54, v2, v3
	v_add_f32_e32 v55, v4, v5
	v_mul_f32_e32 v56, v3, v3
	v_mul_f32_e32 v57, v5, v5
	v_mul_f32_e32 v60, v187, v187
	v_mul_f32_e32 v61, v189, v189
	v_pk_mul_f32 v[64:65], v[64:65], s[24:25] op_sel_hi:[1,0]
	v_pk_mul_f32 v[62:63], v[62:63], s[24:25] op_sel_hi:[1,0]
	v_pk_fma_f32 v[182:183], v[182:183], s[26:27], v[58:59] op_sel_hi:[1,0,1]
	v_add_f32_e32 v58, v186, v187
	v_add_f32_e32 v59, v188, v189
	v_add_f32_e32 v54, v54, v55
	v_fmac_f32_e32 v56, v2, v2
	v_fmac_f32_e32 v57, v4, v4
	v_fmac_f32_e32 v60, v186, v186
	v_fmac_f32_e32 v61, v188, v188
	v_pk_fma_f32 v[180:181], v[180:181], s[26:27], v[64:65] op_sel_hi:[1,0,1]
	v_pk_fma_f32 v[178:179], v[178:179], s[26:27], v[62:63] op_sel_hi:[1,0,1]
	v_mul_f32_e32 v64, v183, v183
	v_mul_f32_e32 v65, v185, v185
	v_add_f32_e32 v55, v58, v59
	v_add_f32_e32 v54, 0, v54
	v_add_f32_e32 v56, v56, v57
	v_add_f32_e32 v57, v60, v61
	v_add_f32_e32 v62, v182, v183
	v_add_f32_e32 v63, v184, v185
	v_mul_f32_e32 v192, v179, v179
	v_fmac_f32_e32 v64, v182, v182
	v_fmac_f32_e32 v65, v184, v184
	v_add_f32_e32 v54, v54, v55
	v_add_f32_e32 v55, v56, v57
	v_mul_f32_e32 v56, v181, v181
	v_add_f32_e32 v190, v178, v179
	v_add_f32_e32 v191, v180, v181
	v_add_f32_e32 v58, v62, v63
	v_fmac_f32_e32 v192, v178, v178
	v_add_f32_e32 v60, v64, v65
	v_fmac_f32_e32 v56, v180, v180
	v_add_f32_e32 v59, v190, v191
	v_add_f32_e32 v54, v54, v58
	v_add_f32_e32 v55, v55, v60
	v_add_f32_e32 v56, v192, v56
	v_add_f32_e32 v54, v54, v59
	v_add_f32_e32 v55, v55, v56
	v_mov_b32_e32 v56, v54
	v_mov_b32_e32 v57, v55
	s_nop 0
	v_permlane16_swap_b32_e32 v54, v56
	v_permlane16_swap_b32_e32 v55, v57
	v_add_f32_e32 v54, v54, v56
	v_add_f32_e32 v55, v55, v57
	v_mov_b32_e32 v56, v54
	v_mov_b32_e32 v57, v55
	s_nop 0
	v_permlane32_swap_b32_e32 v54, v56
	v_permlane32_swap_b32_e32 v55, v57
	s_and_saveexec_b64 s[38:39], s[4:5]
	s_cbranch_execz .LBB0_581
	v_pk_add_f32 v[54:55], v[54:55], v[56:57]
	v_lshlrev_b64 v[56:57], 7, v[212:213]
	v_lshl_add_u64 v[56:57], s[16:17], 0, v[56:57]
	v_lshl_add_u64 v[56:57], s[34:35], 3, v[56:57]
	global_store_dwordx2 v[56:57], v[54:55], off sc1
.LBB0_581:
	s_or_b64 exec, exec, s[38:39]
	v_pk_mul_f32 v[24:25], v[24:25], s[24:25] op_sel_hi:[1,0]
	v_pk_mul_f32 v[22:23], v[22:23], s[24:25] op_sel_hi:[1,0]
	v_pk_fma_f32 v[24:25], v[176:177], s[26:27], v[24:25] op_sel_hi:[1,0,1]
	v_pk_fma_f32 v[22:23], v[174:175], s[26:27], v[22:23] op_sel_hi:[1,0,1]
	v_pk_mul_f32 v[42:43], v[42:43], s[24:25] op_sel_hi:[1,0]
	v_pk_mul_f32 v[44:45], v[44:45], s[24:25] op_sel_hi:[1,0]
	v_pk_fma_f32 v[162:163], v[162:163], s[26:27], v[42:43] op_sel_hi:[1,0,1]
	v_add_f32_e32 v42, v22, v23
	v_add_f32_e32 v43, v24, v25
	v_pk_mul_f32 v[52:53], v[52:53], s[24:25] op_sel_hi:[1,0]
	v_pk_mul_f32 v[50:51], v[50:51], s[24:25] op_sel_hi:[1,0]
	v_pk_fma_f32 v[164:165], v[164:165], s[26:27], v[44:45] op_sel_hi:[1,0,1]
	v_add_f32_e32 v42, v42, v43
	v_mul_f32_e32 v43, v23, v23
	v_mul_f32_e32 v44, v25, v25
	v_pk_fma_f32 v[172:173], v[172:173], s[26:27], v[52:53] op_sel_hi:[1,0,1]
	v_pk_fma_f32 v[170:171], v[170:171], s[26:27], v[50:51] op_sel_hi:[1,0,1]
	v_fmac_f32_e32 v43, v22, v22
	v_fmac_f32_e32 v44, v24, v24
	v_add_f32_e32 v43, v43, v44
	v_add_f32_e32 v44, v170, v171
	v_add_f32_e32 v45, v172, v173
	v_add_f32_e32 v42, 0, v42
	v_add_f32_e32 v44, v44, v45
	v_add_f32_e32 v42, v42, v44
	v_mul_f32_e32 v44, v171, v171
	v_mul_f32_e32 v45, v173, v173
	v_pk_mul_f32 v[48:49], v[48:49], s[24:25] op_sel_hi:[1,0]
	v_pk_mul_f32 v[46:47], v[46:47], s[24:25] op_sel_hi:[1,0]
	v_fmac_f32_e32 v44, v170, v170
	v_fmac_f32_e32 v45, v172, v172
	v_pk_fma_f32 v[168:169], v[168:169], s[26:27], v[48:49] op_sel_hi:[1,0,1]
	v_pk_fma_f32 v[166:167], v[166:167], s[26:27], v[46:47] op_sel_hi:[1,0,1]
	v_add_f32_e32 v44, v44, v45
	v_add_f32_e32 v43, v43, v44
	v_add_f32_e32 v44, v166, v167
	v_add_f32_e32 v45, v168, v169
	v_add_f32_e32 v44, v44, v45
	v_add_f32_e32 v42, v42, v44
	v_mul_f32_e32 v44, v167, v167
	v_mul_f32_e32 v45, v169, v169
	v_fmac_f32_e32 v44, v166, v166
	v_fmac_f32_e32 v45, v168, v168
	v_add_f32_e32 v44, v44, v45
	v_add_f32_e32 v43, v43, v44
	v_add_f32_e32 v44, v162, v163
	v_add_f32_e32 v45, v164, v165
	v_add_f32_e32 v44, v44, v45
	v_add_f32_e32 v42, v42, v44
	v_mul_f32_e32 v44, v163, v163
	v_mul_f32_e32 v45, v165, v165
	v_fmac_f32_e32 v44, v162, v162
	v_fmac_f32_e32 v45, v164, v164
	v_add_f32_e32 v44, v44, v45
	v_add_f32_e32 v43, v43, v44
	v_mov_b32_e32 v44, v42
	v_mov_b32_e32 v45, v43
	s_nop 0
	v_permlane16_swap_b32_e32 v42, v44
	v_permlane16_swap_b32_e32 v43, v45
	v_add_f32_e32 v42, v42, v44
	v_add_f32_e32 v43, v43, v45
	v_mov_b32_e32 v44, v42
	v_mov_b32_e32 v45, v43
	s_nop 0
	v_permlane32_swap_b32_e32 v42, v44
	v_permlane32_swap_b32_e32 v43, v45
	s_and_saveexec_b64 s[38:39], s[4:5]
	s_cbranch_execz .LBB0_583
	v_pk_add_f32 v[42:43], v[42:43], v[44:45]
	v_lshlrev_b64 v[44:45], 7, v[210:211]
	v_lshl_add_u64 v[44:45], s[16:17], 0, v[44:45]
	v_lshl_add_u64 v[44:45], s[34:35], 3, v[44:45]
	global_store_dwordx2 v[44:45], v[42:43], off sc1
.LBB0_583:
	s_or_b64 exec, exec, s[38:39]
	v_pk_mul_f32 v[40:41], v[40:41], s[24:25] op_sel_hi:[1,0]
	v_pk_mul_f32 v[38:39], v[38:39], s[24:25] op_sel_hi:[1,0]
	v_pk_fma_f32 v[44:45], v[160:161], s[26:27], v[40:41] op_sel_hi:[1,0,1]
	v_pk_fma_f32 v[42:43], v[158:159], s[26:27], v[38:39] op_sel_hi:[1,0,1]
	v_pk_mul_f32 v[26:27], v[26:27], s[24:25] op_sel_hi:[1,0]
	v_pk_mul_f32 v[28:29], v[28:29], s[24:25] op_sel_hi:[1,0]
	v_pk_fma_f32 v[146:147], v[146:147], s[26:27], v[26:27] op_sel_hi:[1,0,1]
	v_add_f32_e32 v26, v42, v43
	v_add_f32_e32 v27, v44, v45
	v_pk_mul_f32 v[36:37], v[36:37], s[24:25] op_sel_hi:[1,0]
	v_pk_mul_f32 v[34:35], v[34:35], s[24:25] op_sel_hi:[1,0]
	v_pk_fma_f32 v[148:149], v[148:149], s[26:27], v[28:29] op_sel_hi:[1,0,1]
	v_add_f32_e32 v26, v26, v27
	v_mul_f32_e32 v27, v43, v43
	v_mul_f32_e32 v28, v45, v45
	v_pk_fma_f32 v[156:157], v[156:157], s[26:27], v[36:37] op_sel_hi:[1,0,1]
	v_pk_fma_f32 v[154:155], v[154:155], s[26:27], v[34:35] op_sel_hi:[1,0,1]
	v_fmac_f32_e32 v27, v42, v42
	v_fmac_f32_e32 v28, v44, v44
	v_add_f32_e32 v27, v27, v28
	v_add_f32_e32 v28, v154, v155
	v_add_f32_e32 v29, v156, v157
	v_add_f32_e32 v26, 0, v26
	v_add_f32_e32 v28, v28, v29
	v_add_f32_e32 v26, v26, v28
	v_mul_f32_e32 v28, v155, v155
	v_mul_f32_e32 v29, v157, v157
	v_pk_mul_f32 v[32:33], v[32:33], s[24:25] op_sel_hi:[1,0]
	v_pk_mul_f32 v[30:31], v[30:31], s[24:25] op_sel_hi:[1,0]
	v_fmac_f32_e32 v28, v154, v154
	v_fmac_f32_e32 v29, v156, v156
	v_pk_fma_f32 v[152:153], v[152:153], s[26:27], v[32:33] op_sel_hi:[1,0,1]
	v_pk_fma_f32 v[150:151], v[150:151], s[26:27], v[30:31] op_sel_hi:[1,0,1]
	v_add_f32_e32 v28, v28, v29
	v_add_f32_e32 v27, v27, v28
	v_add_f32_e32 v28, v150, v151
	v_add_f32_e32 v29, v152, v153
	v_add_f32_e32 v28, v28, v29
	v_add_f32_e32 v26, v26, v28
	v_mul_f32_e32 v28, v151, v151
	v_mul_f32_e32 v29, v153, v153
	v_fmac_f32_e32 v28, v150, v150
	v_fmac_f32_e32 v29, v152, v152
	v_add_f32_e32 v28, v28, v29
	v_add_f32_e32 v27, v27, v28
	v_add_f32_e32 v28, v146, v147
	v_add_f32_e32 v29, v148, v149
	v_add_f32_e32 v28, v28, v29
	v_add_f32_e32 v26, v26, v28
	v_mul_f32_e32 v28, v147, v147
	v_mul_f32_e32 v29, v149, v149
	v_fmac_f32_e32 v28, v146, v146
	v_fmac_f32_e32 v29, v148, v148
	v_add_f32_e32 v28, v28, v29
	v_add_f32_e32 v27, v27, v28
	v_mov_b32_e32 v28, v26
	v_mov_b32_e32 v29, v27
	s_nop 0
	v_permlane16_swap_b32_e32 v26, v28
	v_permlane16_swap_b32_e32 v27, v29
	v_add_f32_e32 v26, v26, v28
	v_add_f32_e32 v27, v27, v29
	v_mov_b32_e32 v28, v26
	v_mov_b32_e32 v29, v27
	s_nop 0
	v_permlane32_swap_b32_e32 v26, v28
	v_permlane32_swap_b32_e32 v27, v29
	s_and_saveexec_b64 s[38:39], s[4:5]
	s_cbranch_execz .LBB0_585
	v_pk_add_f32 v[26:27], v[26:27], v[28:29]
	v_lshlrev_b64 v[28:29], 7, v[208:209]
	v_lshl_add_u64 v[28:29], s[16:17], 0, v[28:29]
	v_lshl_add_u64 v[28:29], s[34:35], 3, v[28:29]
	global_store_dwordx2 v[28:29], v[26:27], off sc1
.LBB0_585:
	s_or_b64 exec, exec, s[38:39]
	v_pk_mul_f32 v[20:21], v[20:21], s[24:25] op_sel_hi:[1,0]
	v_pk_mul_f32 v[18:19], v[18:19], s[24:25] op_sel_hi:[1,0]
	v_pk_fma_f32 v[60:61], v[144:145], s[26:27], v[20:21] op_sel_hi:[1,0,1]
	v_pk_fma_f32 v[58:59], v[142:143], s[26:27], v[18:19] op_sel_hi:[1,0,1]
	v_pk_mul_f32 v[6:7], v[6:7], s[24:25] op_sel_hi:[1,0]
	v_pk_mul_f32 v[8:9], v[8:9], s[24:25] op_sel_hi:[1,0]
	v_pk_fma_f32 v[174:175], v[130:131], s[26:27], v[6:7] op_sel_hi:[1,0,1]
	v_add_f32_e32 v6, v58, v59
	v_add_f32_e32 v7, v60, v61
	v_pk_mul_f32 v[16:17], v[16:17], s[24:25] op_sel_hi:[1,0]
	v_pk_mul_f32 v[14:15], v[14:15], s[24:25] op_sel_hi:[1,0]
	v_pk_fma_f32 v[158:159], v[132:133], s[26:27], v[8:9] op_sel_hi:[1,0,1]
	v_add_f32_e32 v6, v6, v7
	v_mul_f32_e32 v7, v59, v59
	v_mul_f32_e32 v8, v61, v61
	v_pk_fma_f32 v[142:143], v[140:141], s[26:27], v[16:17] op_sel_hi:[1,0,1]
	v_pk_fma_f32 v[160:161], v[138:139], s[26:27], v[14:15] op_sel_hi:[1,0,1]
	v_fmac_f32_e32 v7, v58, v58
	v_fmac_f32_e32 v8, v60, v60
	v_add_f32_e32 v7, v7, v8
	v_add_f32_e32 v8, v160, v161
	v_add_f32_e32 v9, v142, v143
	v_add_f32_e32 v6, 0, v6
	v_add_f32_e32 v8, v8, v9
	v_add_f32_e32 v6, v6, v8
	v_mul_f32_e32 v8, v161, v161
	v_mul_f32_e32 v9, v143, v143
	v_pk_mul_f32 v[12:13], v[12:13], s[24:25] op_sel_hi:[1,0]
	v_pk_mul_f32 v[10:11], v[10:11], s[24:25] op_sel_hi:[1,0]
	v_fmac_f32_e32 v8, v160, v160
	v_fmac_f32_e32 v9, v142, v142
	v_pk_fma_f32 v[140:141], v[136:137], s[26:27], v[12:13] op_sel_hi:[1,0,1]
	v_pk_fma_f32 v[144:145], v[134:135], s[26:27], v[10:11] op_sel_hi:[1,0,1]
	v_add_f32_e32 v8, v8, v9
	v_add_f32_e32 v7, v7, v8
	v_add_f32_e32 v8, v144, v145
	v_add_f32_e32 v9, v140, v141
	v_add_f32_e32 v8, v8, v9
	v_add_f32_e32 v6, v6, v8
	v_mul_f32_e32 v8, v145, v145
	v_mul_f32_e32 v9, v141, v141
	v_fmac_f32_e32 v8, v144, v144
	v_fmac_f32_e32 v9, v140, v140
	v_add_f32_e32 v8, v8, v9
	v_add_f32_e32 v7, v7, v8
	v_add_f32_e32 v8, v174, v175
	v_add_f32_e32 v9, v158, v159
	v_add_f32_e32 v8, v8, v9
	v_add_f32_e32 v6, v6, v8
	v_mul_f32_e32 v8, v175, v175
	v_mul_f32_e32 v9, v159, v159
	v_fmac_f32_e32 v8, v174, v174
	v_fmac_f32_e32 v9, v158, v158
	v_add_f32_e32 v8, v8, v9
	v_add_f32_e32 v7, v7, v8
	v_mov_b32_e32 v8, v6
	v_mov_b32_e32 v9, v7
	s_nop 0
	v_permlane16_swap_b32_e32 v6, v8
	v_permlane16_swap_b32_e32 v7, v9
	v_add_f32_e32 v6, v6, v8
	v_add_f32_e32 v7, v7, v9
	v_mov_b32_e32 v8, v6
	v_mov_b32_e32 v9, v7
	s_nop 0
	v_permlane32_swap_b32_e32 v6, v8
	v_permlane32_swap_b32_e32 v7, v9
	s_and_saveexec_b64 s[38:39], s[4:5]
	s_cbranch_execz .LBB0_587
	v_pk_add_f32 v[6:7], v[6:7], v[8:9]
	v_lshlrev_b64 v[8:9], 7, v[206:207]
	v_lshl_add_u64 v[8:9], s[16:17], 0, v[8:9]
	v_lshl_add_u64 v[8:9], s[34:35], 3, v[8:9]
	global_store_dwordx2 v[8:9], v[6:7], off sc1
.LBB0_587:
	s_or_b64 exec, exec, s[38:39]
	v_add_u32_e32 v138, s2, v221
	v_ashrrev_i32_e32 v139, 31, v138
	v_lshlrev_b64 v[6:7], 12, v[138:139]
	v_lshl_add_u64 v[6:7], v[214:215], 0, v[6:7]
	global_load_dwordx4 v[190:193], v[6:7], off nt
	global_load_dwordx4 v[226:229], v[6:7], off offset:64 nt
	global_load_dwordx4 v[230:233], v[6:7], off offset:128 nt
	global_load_dwordx4 v[234:237], v[6:7], off offset:192 nt
	v_or_b32_e32 v136, 16, v138
	v_ashrrev_i32_e32 v137, 31, v136
	v_lshlrev_b64 v[6:7], 12, v[136:137]
	v_or_b32_e32 v134, 32, v138
	v_lshl_add_u64 v[6:7], v[214:215], 0, v[6:7]
	v_ashrrev_i32_e32 v135, 31, v134
	global_load_dwordx4 v[62:65], v[6:7], off nt
	global_load_dwordx4 v[54:57], v[6:7], off offset:64 nt
	global_load_dwordx4 v[50:53], v[6:7], off offset:128 nt
	global_load_dwordx4 v[46:49], v[6:7], off offset:192 nt
	v_lshlrev_b64 v[6:7], 12, v[134:135]
	v_or_b32_e32 v130, 48, v138
	v_lshl_add_u64 v[6:7], v[214:215], 0, v[6:7]
	v_ashrrev_i32_e32 v131, 31, v130
	global_load_dwordx4 v[38:41], v[6:7], off nt
	global_load_dwordx4 v[34:37], v[6:7], off offset:64 nt
	global_load_dwordx4 v[30:33], v[6:7], off offset:128 nt
	global_load_dwordx4 v[26:29], v[6:7], off offset:192 nt
	v_lshlrev_b64 v[6:7], 12, v[130:131]
	v_lshl_add_u64 v[6:7], v[214:215], 0, v[6:7]
	global_load_dwordx4 v[18:21], v[6:7], off nt
	global_load_dwordx4 v[14:17], v[6:7], off offset:64 nt
	global_load_dwordx4 v[10:13], v[6:7], off offset:128 nt
	s_nop 0
	global_load_dwordx4 v[6:9], v[6:7], off offset:192 nt
	s_ashr_i32 s37, s36, 31
	v_lshl_add_u64 v[132:133], s[36:37], 1, v[202:203]
	v_lshlrev_b64 v[176:177], 11, v[212:213]
	v_cvt_pk_bf16_f32 v212, v2, v3
	v_cvt_pk_bf16_f32 v213, v4, v5
	v_cvt_pk_bf16_f32 v2, v182, v183
	v_cvt_pk_bf16_f32 v4, v178, v179
	v_cvt_pk_bf16_f32 v3, v184, v185
	v_cvt_pk_bf16_f32 v5, v180, v181
	v_lshl_add_u64 v[176:177], v[132:133], 0, v[176:177]
	v_cvt_pk_bf16_f32 v214, v186, v187
	v_cvt_pk_bf16_f32 v215, v188, v189
	v_permlane16_swap_b32_e32 v2, v4
	v_permlane16_swap_b32_e32 v3, v5
	v_permlane16_swap_b32_e32 v212, v214
	v_permlane16_swap_b32_e32 v213, v215
	global_store_dwordx4 v[176:177], v[2:5], off offset:64 sc1
	global_store_dwordx4 v[176:177], v[212:215], off sc1
	s_nop 0
	v_lshlrev_b64 v[2:3], 11, v[210:211]
	v_lshl_add_u64 v[176:177], v[132:133], 0, v[2:3]
	v_cvt_pk_bf16_f32 v2, v22, v23
	v_cvt_pk_bf16_f32 v4, v170, v171
	v_cvt_pk_bf16_f32 v3, v24, v25
	v_cvt_pk_bf16_f32 v5, v172, v173
	v_permlane16_swap_b32_e32 v2, v4
	s_nop 0
	v_permlane16_swap_b32_e32 v3, v5
	global_store_dwordx4 v[176:177], v[2:5], off sc1
	s_nop 1
	v_cvt_pk_bf16_f32 v2, v166, v167
	v_cvt_pk_bf16_f32 v4, v162, v163
	v_cvt_pk_bf16_f32 v3, v168, v169
	v_cvt_pk_bf16_f32 v5, v164, v165
	v_permlane16_swap_b32_e32 v2, v4
	s_nop 0
	v_permlane16_swap_b32_e32 v3, v5
	global_store_dwordx4 v[176:177], v[2:5], off offset:64 sc1
	s_nop 1
	v_lshlrev_b64 v[2:3], 11, v[208:209]
	v_lshl_add_u64 v[22:23], v[132:133], 0, v[2:3]
	v_cvt_pk_bf16_f32 v2, v42, v43
	v_cvt_pk_bf16_f32 v4, v154, v155
	v_cvt_pk_bf16_f32 v3, v44, v45
	v_cvt_pk_bf16_f32 v5, v156, v157
	v_permlane16_swap_b32_e32 v2, v4
	s_nop 0
	v_permlane16_swap_b32_e32 v3, v5
	global_store_dwordx4 v[22:23], v[2:5], off sc1
	s_waitcnt vmcnt(19)
	v_pk_mul_f32 v[42:43], v[226:227], s[24:25] op_sel_hi:[1,0]
	v_cvt_pk_bf16_f32 v2, v150, v151
	v_cvt_pk_bf16_f32 v4, v146, v147
	v_cvt_pk_bf16_f32 v3, v152, v153
	v_cvt_pk_bf16_f32 v5, v148, v149
	v_permlane16_swap_b32_e32 v2, v4
	s_nop 0
	v_permlane16_swap_b32_e32 v3, v5
	global_store_dwordx4 v[22:23], v[2:5], off offset:64 sc1
	s_waitcnt vmcnt(18)
	v_pk_mul_f32 v[44:45], v[236:237], s[24:25] op_sel_hi:[1,0]
	v_lshlrev_b64 v[2:3], 11, v[206:207]
	v_lshl_add_u64 v[22:23], v[132:133], 0, v[2:3]
	v_cvt_pk_bf16_f32 v2, v58, v59
	v_cvt_pk_bf16_f32 v4, v160, v161
	v_cvt_pk_bf16_f32 v3, v60, v61
	v_cvt_pk_bf16_f32 v5, v142, v143
	v_permlane16_swap_b32_e32 v2, v4
	s_nop 0
	v_permlane16_swap_b32_e32 v3, v5
	global_store_dwordx4 v[22:23], v[2:5], off sc1
	v_pk_mul_f32 v[60:61], v[234:235], s[24:25] op_sel_hi:[1,0]
	v_pk_fma_f32 v[44:45], v[116:117], s[26:27], v[44:45] op_sel_hi:[1,0,1]
	v_cvt_pk_bf16_f32 v2, v144, v145
	v_cvt_pk_bf16_f32 v4, v174, v175
	v_cvt_pk_bf16_f32 v3, v140, v141
	v_cvt_pk_bf16_f32 v5, v158, v159
	v_permlane16_swap_b32_e32 v2, v4
	s_nop 0
	v_permlane16_swap_b32_e32 v3, v5
	global_store_dwordx4 v[22:23], v[2:5], off offset:64 sc1
	v_pk_fma_f32 v[60:61], v[114:115], s[26:27], v[60:61] op_sel_hi:[1,0,1]
	v_pk_fma_f32 v[58:59], v[122:123], s[26:27], v[42:43] op_sel_hi:[1,0,1]
	v_pk_mul_f32 v[2:3], v[192:193], s[24:25] op_sel_hi:[1,0]
	v_pk_mul_f32 v[4:5], v[190:191], s[24:25] op_sel_hi:[1,0]
	v_pk_fma_f32 v[2:3], v[128:129], s[26:27], v[2:3] op_sel_hi:[1,0,1]
	v_pk_fma_f32 v[22:23], v[126:127], s[26:27], v[4:5] op_sel_hi:[1,0,1]
	v_add_f32_e32 v115, v2, v3
	v_add_f32_e32 v114, v22, v23
	v_pk_mul_f32 v[4:5], v[228:229], s[24:25] op_sel_hi:[1,0]
	v_add_f32_e32 v114, v114, v115
	v_mul_f32_e32 v115, v23, v23
	v_mul_f32_e32 v116, v3, v3
	v_pk_fma_f32 v[24:25], v[124:125], s[26:27], v[4:5] op_sel_hi:[1,0,1]
	v_fmac_f32_e32 v115, v22, v22
	v_fmac_f32_e32 v116, v2, v2
	v_add_f32_e32 v115, v115, v116
	v_add_f32_e32 v116, v58, v59
	v_add_f32_e32 v117, v24, v25
	v_add_f32_e32 v114, 0, v114
	v_add_f32_e32 v116, v116, v117
	v_add_f32_e32 v114, v114, v116
	v_mul_f32_e32 v116, v59, v59
	v_mul_f32_e32 v117, v25, v25
	v_pk_mul_f32 v[4:5], v[232:233], s[24:25] op_sel_hi:[1,0]
	v_pk_mul_f32 v[42:43], v[230:231], s[24:25] op_sel_hi:[1,0]
	v_fmac_f32_e32 v116, v58, v58
	v_fmac_f32_e32 v117, v24, v24
	v_pk_fma_f32 v[4:5], v[120:121], s[26:27], v[4:5] op_sel_hi:[1,0,1]
	v_pk_fma_f32 v[42:43], v[118:119], s[26:27], v[42:43] op_sel_hi:[1,0,1]
	v_add_f32_e32 v116, v116, v117
	v_add_f32_e32 v115, v115, v116
	v_add_f32_e32 v116, v42, v43
	v_add_f32_e32 v117, v4, v5
	v_add_f32_e32 v116, v116, v117
	v_add_f32_e32 v114, v114, v116
	v_mul_f32_e32 v116, v43, v43
	v_mul_f32_e32 v117, v5, v5
	v_fmac_f32_e32 v116, v42, v42
	v_fmac_f32_e32 v117, v4, v4
	v_add_f32_e32 v116, v116, v117
	v_add_f32_e32 v115, v115, v116
	v_add_f32_e32 v116, v60, v61
	v_add_f32_e32 v117, v44, v45
	v_add_f32_e32 v116, v116, v117
	v_add_f32_e32 v114, v114, v116
	v_mul_f32_e32 v116, v61, v61
	v_mul_f32_e32 v117, v45, v45
	v_fmac_f32_e32 v116, v60, v60
	v_fmac_f32_e32 v117, v44, v44
	v_add_f32_e32 v116, v116, v117
	v_add_f32_e32 v115, v115, v116
	v_mov_b32_e32 v116, v114
	v_mov_b32_e32 v117, v115
	s_nop 0
	v_permlane16_swap_b32_e32 v114, v116
	v_permlane16_swap_b32_e32 v115, v117
	v_add_f32_e32 v114, v114, v116
	v_add_f32_e32 v115, v115, v117
	v_mov_b32_e32 v116, v114
	v_mov_b32_e32 v117, v115
	s_nop 0
	v_permlane32_swap_b32_e32 v114, v116
	v_permlane32_swap_b32_e32 v115, v117
	s_and_saveexec_b64 s[36:37], s[4:5]
	s_cbranch_execz .LBB0_589
	v_pk_add_f32 v[114:115], v[114:115], v[116:117]
	v_lshlrev_b64 v[116:117], 7, v[138:139]
	v_lshl_add_u64 v[116:117], s[16:17], 0, v[116:117]
	v_lshl_add_u64 v[116:117], s[34:35], 3, v[116:117]
	global_store_dwordx2 v[116:117], v[114:115], off sc1
.LBB0_589:
	s_or_b64 exec, exec, s[36:37]
	s_waitcnt vmcnt(19)
	v_pk_mul_f32 v[64:65], v[64:65], s[24:25] op_sel_hi:[1,0]
	v_pk_mul_f32 v[114:115], v[62:63], s[24:25] op_sel_hi:[1,0]
	v_pk_fma_f32 v[62:63], v[112:113], s[26:27], v[64:65] op_sel_hi:[1,0,1]
	v_pk_fma_f32 v[64:65], v[110:111], s[26:27], v[114:115] op_sel_hi:[1,0,1]
	s_waitcnt vmcnt(18)
	v_pk_mul_f32 v[56:57], v[56:57], s[24:25] op_sel_hi:[1,0]
	v_pk_mul_f32 v[110:111], v[54:55], s[24:25] op_sel_hi:[1,0]
	v_pk_fma_f32 v[54:55], v[108:109], s[26:27], v[56:57] op_sel_hi:[1,0,1]
	v_pk_fma_f32 v[56:57], v[106:107], s[26:27], v[110:111] op_sel_hi:[1,0,1]
	s_waitcnt vmcnt(17)
	v_pk_mul_f32 v[52:53], v[52:53], s[24:25] op_sel_hi:[1,0]
	v_pk_mul_f32 v[106:107], v[50:51], s[24:25] op_sel_hi:[1,0]
	v_pk_fma_f32 v[50:51], v[104:105], s[26:27], v[52:53] op_sel_hi:[1,0,1]
	v_pk_fma_f32 v[52:53], v[102:103], s[26:27], v[106:107] op_sel_hi:[1,0,1]
	s_waitcnt vmcnt(16)
	v_pk_mul_f32 v[48:49], v[48:49], s[24:25] op_sel_hi:[1,0]
	v_pk_mul_f32 v[102:103], v[46:47], s[24:25] op_sel_hi:[1,0]
	v_pk_fma_f32 v[46:47], v[92:93], s[26:27], v[48:49] op_sel_hi:[1,0,1]
	v_pk_fma_f32 v[48:49], v[90:91], s[26:27], v[102:103] op_sel_hi:[1,0,1]
	v_add_f32_e32 v90, v64, v65
	v_add_f32_e32 v91, v62, v63
	v_add_f32_e32 v90, v90, v91
	v_mul_f32_e32 v91, v65, v65
	v_mul_f32_e32 v92, v63, v63
	v_fmac_f32_e32 v91, v64, v64
	v_fmac_f32_e32 v92, v62, v62
	v_add_f32_e32 v91, v91, v92
	v_add_f32_e32 v92, v56, v57
	v_add_f32_e32 v93, v54, v55
	v_add_f32_e32 v90, 0, v90
	v_add_f32_e32 v92, v92, v93
	v_add_f32_e32 v90, v90, v92
	v_mul_f32_e32 v92, v57, v57
	v_mul_f32_e32 v93, v55, v55
	v_fmac_f32_e32 v92, v56, v56
	v_fmac_f32_e32 v93, v54, v54
	v_add_f32_e32 v92, v92, v93
	v_add_f32_e32 v91, v91, v92
	v_add_f32_e32 v92, v52, v53
	v_add_f32_e32 v93, v50, v51
	v_add_f32_e32 v92, v92, v93
	v_add_f32_e32 v90, v90, v92
	v_mul_f32_e32 v92, v53, v53
	v_mul_f32_e32 v93, v51, v51
	v_fmac_f32_e32 v92, v52, v52
	v_fmac_f32_e32 v93, v50, v50
	v_add_f32_e32 v92, v92, v93
	v_add_f32_e32 v91, v91, v92
	v_add_f32_e32 v92, v48, v49
	v_add_f32_e32 v93, v46, v47
	v_add_f32_e32 v92, v92, v93
	v_add_f32_e32 v90, v90, v92
	v_mul_f32_e32 v92, v49, v49
	v_mul_f32_e32 v93, v47, v47
	v_fmac_f32_e32 v92, v48, v48
	v_fmac_f32_e32 v93, v46, v46
	v_add_f32_e32 v92, v92, v93
	v_add_f32_e32 v91, v91, v92
	v_mov_b32_e32 v92, v90
	v_mov_b32_e32 v93, v91
	s_nop 0
	v_permlane16_swap_b32_e32 v90, v92
	v_permlane16_swap_b32_e32 v91, v93
	v_add_f32_e32 v90, v90, v92
	v_add_f32_e32 v91, v91, v93
	v_mov_b32_e32 v92, v90
	v_mov_b32_e32 v93, v91
	s_nop 0
	v_permlane32_swap_b32_e32 v90, v92
	v_permlane32_swap_b32_e32 v91, v93
	s_and_saveexec_b64 s[36:37], s[4:5]
	s_cbranch_execz .LBB0_591
	v_pk_add_f32 v[90:91], v[90:91], v[92:93]
	v_lshlrev_b64 v[92:93], 7, v[136:137]
	v_lshl_add_u64 v[92:93], s[16:17], 0, v[92:93]
	v_lshl_add_u64 v[92:93], s[34:35], 3, v[92:93]
	global_store_dwordx2 v[92:93], v[90:91], off sc1
.LBB0_591:
	s_or_b64 exec, exec, s[36:37]
	s_waitcnt vmcnt(15)
	v_pk_mul_f32 v[40:41], v[40:41], s[24:25] op_sel_hi:[1,0]
	v_pk_mul_f32 v[90:91], v[38:39], s[24:25] op_sel_hi:[1,0]
	v_pk_fma_f32 v[38:39], v[88:89], s[26:27], v[40:41] op_sel_hi:[1,0,1]
	v_pk_fma_f32 v[40:41], v[86:87], s[26:27], v[90:91] op_sel_hi:[1,0,1]
	s_waitcnt vmcnt(14)
	v_pk_mul_f32 v[36:37], v[36:37], s[24:25] op_sel_hi:[1,0]
	v_pk_mul_f32 v[86:87], v[34:35], s[24:25] op_sel_hi:[1,0]
	v_pk_fma_f32 v[34:35], v[84:85], s[26:27], v[36:37] op_sel_hi:[1,0,1]
	v_pk_fma_f32 v[36:37], v[82:83], s[26:27], v[86:87] op_sel_hi:[1,0,1]
	s_waitcnt vmcnt(13)
	v_pk_mul_f32 v[32:33], v[32:33], s[24:25] op_sel_hi:[1,0]
	v_pk_mul_f32 v[82:83], v[30:31], s[24:25] op_sel_hi:[1,0]
	v_pk_fma_f32 v[30:31], v[100:101], s[26:27], v[32:33] op_sel_hi:[1,0,1]
	v_pk_fma_f32 v[32:33], v[98:99], s[26:27], v[82:83] op_sel_hi:[1,0,1]
	s_waitcnt vmcnt(12)
	v_pk_mul_f32 v[28:29], v[28:29], s[24:25] op_sel_hi:[1,0]
	v_pk_mul_f32 v[82:83], v[26:27], s[24:25] op_sel_hi:[1,0]
	v_pk_fma_f32 v[26:27], v[96:97], s[26:27], v[28:29] op_sel_hi:[1,0,1]
	v_pk_fma_f32 v[28:29], v[94:95], s[26:27], v[82:83] op_sel_hi:[1,0,1]
	v_add_f32_e32 v82, v40, v41
	v_add_f32_e32 v83, v38, v39
	v_add_f32_e32 v82, v82, v83
	v_mul_f32_e32 v83, v41, v41
	v_mul_f32_e32 v84, v39, v39
	v_fmac_f32_e32 v83, v40, v40
	v_fmac_f32_e32 v84, v38, v38
	v_add_f32_e32 v83, v83, v84
	v_add_f32_e32 v84, v36, v37
	v_add_f32_e32 v85, v34, v35
	v_add_f32_e32 v82, 0, v82
	v_add_f32_e32 v84, v84, v85
	v_add_f32_e32 v82, v82, v84
	v_mul_f32_e32 v84, v37, v37
	v_mul_f32_e32 v85, v35, v35
	v_fmac_f32_e32 v84, v36, v36
	v_fmac_f32_e32 v85, v34, v34
	v_add_f32_e32 v84, v84, v85
	v_add_f32_e32 v83, v83, v84
	v_add_f32_e32 v84, v32, v33
	v_add_f32_e32 v85, v30, v31
	v_add_f32_e32 v84, v84, v85
	v_add_f32_e32 v82, v82, v84
	v_mul_f32_e32 v84, v33, v33
	v_mul_f32_e32 v85, v31, v31
	v_fmac_f32_e32 v84, v32, v32
	v_fmac_f32_e32 v85, v30, v30
	v_add_f32_e32 v84, v84, v85
	v_add_f32_e32 v83, v83, v84
	v_add_f32_e32 v84, v28, v29
	v_add_f32_e32 v85, v26, v27
	v_add_f32_e32 v84, v84, v85
	v_add_f32_e32 v82, v82, v84
	v_mul_f32_e32 v84, v29, v29
	v_mul_f32_e32 v85, v27, v27
	v_fmac_f32_e32 v84, v28, v28
	v_fmac_f32_e32 v85, v26, v26
	v_add_f32_e32 v84, v84, v85
	v_add_f32_e32 v83, v83, v84
	v_mov_b32_e32 v84, v82
	v_mov_b32_e32 v85, v83
	s_nop 0
	v_permlane16_swap_b32_e32 v82, v84
	v_permlane16_swap_b32_e32 v83, v85
	v_add_f32_e32 v82, v82, v84
	v_add_f32_e32 v83, v83, v85
	v_mov_b32_e32 v84, v82
	v_mov_b32_e32 v85, v83
	s_nop 0
	v_permlane32_swap_b32_e32 v82, v84
	v_permlane32_swap_b32_e32 v83, v85
	s_and_saveexec_b64 s[36:37], s[4:5]
	s_cbranch_execz .LBB0_593
	v_pk_add_f32 v[82:83], v[82:83], v[84:85]
	v_lshlrev_b64 v[84:85], 7, v[134:135]
	v_lshl_add_u64 v[84:85], s[16:17], 0, v[84:85]
	v_lshl_add_u64 v[84:85], s[34:35], 3, v[84:85]
	global_store_dwordx2 v[84:85], v[82:83], off sc1
.LBB0_593:
	s_or_b64 exec, exec, s[36:37]
	s_waitcnt vmcnt(11)
	v_pk_mul_f32 v[20:21], v[20:21], s[24:25] op_sel_hi:[1,0]
	v_pk_mul_f32 v[82:83], v[18:19], s[24:25] op_sel_hi:[1,0]
	v_pk_fma_f32 v[18:19], v[72:73], s[26:27], v[20:21] op_sel_hi:[1,0,1]
	v_pk_fma_f32 v[20:21], v[70:71], s[26:27], v[82:83] op_sel_hi:[1,0,1]
	s_waitcnt vmcnt(10)
	v_pk_mul_f32 v[16:17], v[16:17], s[24:25] op_sel_hi:[1,0]
	v_pk_mul_f32 v[70:71], v[14:15], s[24:25] op_sel_hi:[1,0]
	v_pk_fma_f32 v[14:15], v[68:69], s[26:27], v[16:17] op_sel_hi:[1,0,1]
	v_pk_fma_f32 v[16:17], v[66:67], s[26:27], v[70:71] op_sel_hi:[1,0,1]
	s_waitcnt vmcnt(9)
	v_pk_mul_f32 v[12:13], v[12:13], s[24:25] op_sel_hi:[1,0]
	v_pk_mul_f32 v[66:67], v[10:11], s[24:25] op_sel_hi:[1,0]
	v_pk_fma_f32 v[10:11], v[80:81], s[26:27], v[12:13] op_sel_hi:[1,0,1]
	v_pk_fma_f32 v[12:13], v[78:79], s[26:27], v[66:67] op_sel_hi:[1,0,1]
	s_waitcnt vmcnt(8)
	v_pk_mul_f32 v[8:9], v[8:9], s[24:25] op_sel_hi:[1,0]
	v_pk_mul_f32 v[66:67], v[6:7], s[24:25] op_sel_hi:[1,0]
	v_pk_fma_f32 v[6:7], v[76:77], s[26:27], v[8:9] op_sel_hi:[1,0,1]
	v_pk_fma_f32 v[8:9], v[74:75], s[26:27], v[66:67] op_sel_hi:[1,0,1]
	v_add_f32_e32 v66, v20, v21
	v_add_f32_e32 v67, v18, v19
	v_add_f32_e32 v66, v66, v67
	v_mul_f32_e32 v67, v21, v21
	v_mul_f32_e32 v68, v19, v19
	v_fmac_f32_e32 v67, v20, v20
	v_fmac_f32_e32 v68, v18, v18
	v_add_f32_e32 v67, v67, v68
	v_add_f32_e32 v68, v16, v17
	v_add_f32_e32 v69, v14, v15
	v_add_f32_e32 v66, 0, v66
	v_add_f32_e32 v68, v68, v69
	v_add_f32_e32 v66, v66, v68
	v_mul_f32_e32 v68, v17, v17
	v_mul_f32_e32 v69, v15, v15
	v_fmac_f32_e32 v68, v16, v16
	v_fmac_f32_e32 v69, v14, v14
	v_add_f32_e32 v68, v68, v69
	v_add_f32_e32 v67, v67, v68
	v_add_f32_e32 v68, v12, v13
	v_add_f32_e32 v69, v10, v11
	v_add_f32_e32 v68, v68, v69
	v_add_f32_e32 v66, v66, v68
	v_mul_f32_e32 v68, v13, v13
	v_mul_f32_e32 v69, v11, v11
	v_fmac_f32_e32 v68, v12, v12
	v_fmac_f32_e32 v69, v10, v10
	v_add_f32_e32 v68, v68, v69
	v_add_f32_e32 v67, v67, v68
	v_add_f32_e32 v68, v8, v9
	v_add_f32_e32 v69, v6, v7
	v_add_f32_e32 v68, v68, v69
	v_add_f32_e32 v66, v66, v68
	v_mul_f32_e32 v68, v9, v9
	v_mul_f32_e32 v69, v7, v7
	v_fmac_f32_e32 v68, v8, v8
	v_fmac_f32_e32 v69, v6, v6
	v_add_f32_e32 v68, v68, v69
	v_add_f32_e32 v67, v67, v68
	v_mov_b32_e32 v68, v66
	v_mov_b32_e32 v69, v67
	s_nop 0
	v_permlane16_swap_b32_e32 v66, v68
	v_permlane16_swap_b32_e32 v67, v69
	v_add_f32_e32 v66, v66, v68
	v_add_f32_e32 v67, v67, v69
	v_mov_b32_e32 v68, v66
	v_mov_b32_e32 v69, v67
	s_nop 0
	v_permlane32_swap_b32_e32 v66, v68
	v_permlane32_swap_b32_e32 v67, v69
	s_and_saveexec_b64 s[36:37], s[4:5]
	s_cbranch_execz .LBB0_595
	v_pk_add_f32 v[66:67], v[66:67], v[68:69]
	v_lshlrev_b64 v[68:69], 7, v[130:131]
	v_lshl_add_u64 v[68:69], s[16:17], 0, v[68:69]
	v_lshl_add_u64 v[68:69], s[34:35], 3, v[68:69]
	global_store_dwordx2 v[68:69], v[66:67], off sc1
.LBB0_595:
	s_or_b64 exec, exec, s[36:37]
	v_lshlrev_b64 v[66:67], 11, v[138:139]
	v_lshl_add_u64 v[70:71], v[132:133], 0, v[66:67]
	v_cvt_pk_bf16_f32 v66, v22, v23
	v_cvt_pk_bf16_f32 v69, v24, v25
	v_cvt_pk_bf16_f32 v22, v42, v43
	v_cvt_pk_bf16_f32 v24, v60, v61
	v_cvt_pk_bf16_f32 v23, v4, v5
	v_cvt_pk_bf16_f32 v25, v44, v45
	v_cvt_pk_bf16_f32 v67, v2, v3
	v_permlane16_swap_b32_e32 v22, v24
	v_permlane16_swap_b32_e32 v23, v25
	v_lshlrev_b64 v[2:3], 11, v[136:137]
	global_store_dwordx4 v[70:71], v[22:25], off offset:64 sc1
	v_cvt_pk_bf16_f32 v4, v56, v57
	v_cvt_pk_bf16_f32 v5, v54, v55
	v_lshl_add_u64 v[22:23], v[132:133], 0, v[2:3]
	v_cvt_pk_bf16_f32 v2, v64, v65
	v_cvt_pk_bf16_f32 v3, v62, v63
	s_nop 0
	v_permlane16_swap_b32_e32 v2, v4
	v_permlane16_swap_b32_e32 v3, v5
	global_store_dwordx4 v[22:23], v[2:5], off sc1
	v_cvt_pk_bf16_f32 v68, v58, v59
	s_nop 1
	v_permlane16_swap_b32_e32 v66, v68
	v_cvt_pk_bf16_f32 v2, v52, v53
	v_cvt_pk_bf16_f32 v4, v48, v49
	v_cvt_pk_bf16_f32 v3, v50, v51
	v_cvt_pk_bf16_f32 v5, v46, v47
	v_permlane16_swap_b32_e32 v2, v4
	s_nop 0
	v_permlane16_swap_b32_e32 v3, v5
	global_store_dwordx4 v[22:23], v[2:5], off offset:64 sc1
	v_permlane16_swap_b32_e32 v67, v69
	s_nop 0
	v_lshlrev_b64 v[2:3], 11, v[134:135]
	v_lshl_add_u64 v[22:23], v[132:133], 0, v[2:3]
	v_cvt_pk_bf16_f32 v2, v40, v41
	v_cvt_pk_bf16_f32 v4, v36, v37
	v_cvt_pk_bf16_f32 v3, v38, v39
	v_cvt_pk_bf16_f32 v5, v34, v35
	v_permlane16_swap_b32_e32 v2, v4
	s_nop 0
	v_permlane16_swap_b32_e32 v3, v5
	global_store_dwordx4 v[22:23], v[2:5], off sc1
	s_and_b64 vcc, exec, s[6:7]
	s_mov_b64 s[6:7], -1
	v_cvt_pk_bf16_f32 v2, v32, v33
	v_cvt_pk_bf16_f32 v4, v28, v29
	v_cvt_pk_bf16_f32 v3, v30, v31
	v_cvt_pk_bf16_f32 v5, v26, v27
	v_permlane16_swap_b32_e32 v2, v4
	s_nop 0
	v_permlane16_swap_b32_e32 v3, v5
	global_store_dwordx4 v[22:23], v[2:5], off offset:64 sc1
	global_store_dwordx4 v[70:71], v[66:69], off sc1
	s_nop 0
	v_lshlrev_b64 v[2:3], 11, v[130:131]
	v_lshl_add_u64 v[22:23], v[132:133], 0, v[2:3]
	v_cvt_pk_bf16_f32 v2, v20, v21
	v_cvt_pk_bf16_f32 v4, v16, v17
	v_cvt_pk_bf16_f32 v3, v18, v19
	v_cvt_pk_bf16_f32 v5, v14, v15
	v_permlane16_swap_b32_e32 v2, v4
	s_nop 0
	v_permlane16_swap_b32_e32 v3, v5
	global_store_dwordx4 v[22:23], v[2:5], off sc1
	s_nop 1
	v_cvt_pk_bf16_f32 v2, v12, v13
	v_cvt_pk_bf16_f32 v4, v8, v9
	v_cvt_pk_bf16_f32 v3, v10, v11
	v_cvt_pk_bf16_f32 v5, v6, v7
	v_permlane16_swap_b32_e32 v2, v4
	s_nop 0
	v_permlane16_swap_b32_e32 v3, v5
	global_store_dwordx4 v[22:23], v[2:5], off offset:64 sc1
	s_cbranch_vccnz .LBB0_561
	s_andn2_b64 vcc, exec, s[14:15]
	s_cbranch_vccnz .LBB0_560
	s_barrier
	s_branch .LBB0_560

.LBB0_994:
	s_ashr_i32 s36, s34, 3
	s_lshl_b32 s2, s34, 7
	s_ashr_i32 s37, s36, 31
	v_readlane_b32 s80, v239, 7
	s_and_b32 s2, s2, 0x380
	s_lshl_b64 s[36:37], s[36:37], 13
	v_readlane_b32 s86, v239, 13
	v_or_b32_e32 v2, s2, v219
	v_readlane_b32 s87, v239, 14
	s_add_u32 s36, s86, s36
	s_waitcnt vmcnt(0)
	s_addc_u32 s37, s87, s37
	v_lshlrev_b32_e32 v4, 2, v2
	v_mov_b32_e32 v5, v199
	global_load_dwordx4 v[26:29], v4, s[36:37]
	global_load_dwordx4 v[30:33], v4, s[36:37] offset:16
	v_lshl_add_u64 v[4:5], s[36:37], 0, v[4:5]
	s_mov_b64 s[36:37], 0x1000
	s_movk_i32 s2, 0x1000
	v_lshl_add_u64 v[6:7], v[4:5], 0, s[36:37]
	v_add_co_u32_e32 v4, vcc, s2, v4
	v_mov_b32_e32 v8, v186
	s_nop 0
	v_addc_co_u32_e32 v5, vcc, 0, v5, vcc
	global_load_dwordx4 v[34:37], v[4:5], off
	global_load_dwordx4 v[38:41], v[6:7], off offset:16
	v_mov_b32_e32 v6, v190
	v_mov_b32_e32 v14, v178
	v_mov_b32_e32 v24, v183
	v_mov_b32_e32 v20, v192
	v_lshl_add_u32 v4, s96, 8, v218
	v_ashrrev_i32_e32 v5, 31, v4
	v_lshlrev_b64 v[4:5], 10, v[4:5]
	v_mov_b32_e32 v3, v199
	v_mov_b32_e32 v12, v182
	v_mov_b32_e32 v42, v179
	v_mov_b32_e32 v22, v188
	v_lshl_add_u64 v[4:5], s[58:59], 0, v[4:5]
	v_lshl_add_u64 v[2:3], v[4:5], 0, v[2:3]
	v_lshl_add_u64 v[2:3], v[2:3], 0, v[204:205]
	s_mov_b32 s2, 0x8000
	v_readlane_b32 s81, v239, 8
	v_readlane_b32 s82, v239, 9
	v_readlane_b32 s83, v239, 10
	v_readlane_b32 s84, v239, 11
	v_readlane_b32 s85, v239, 12
	v_readlane_b32 s88, v239, 15
	v_readlane_b32 s89, v239, 16
	v_readlane_b32 s90, v239, 17
	v_readlane_b32 s91, v239, 18
	v_readlane_b32 s92, v239, 19
	v_readlane_b32 s93, v239, 20
	v_readlane_b32 s94, v239, 21
	v_readlane_b32 s95, v239, 22
	s_waitcnt vmcnt(0)
	v_mov_b32_e32 v7, v26
	v_mov_b32_e32 v9, v30
	v_pk_mul_f32 v[16:17], v[8:9], s[24:25]
	v_mov_b32_e32 v26, v191
	v_sub_f32_e32 v16, v16, v17
	v_mov_b32_e32 v21, v28
	v_pk_mul_f32 v[10:11], v[26:27], s[24:25]
	v_max_f32_e32 v16, 0xc1898193, v16
	v_pk_mul_f32 v[18:19], v[6:7], s[24:25]
	v_pk_mul_f32 v[6:7], v[20:21], s[24:25]
	v_add_f32_e32 v25, 1.0, v35
	v_add_f32_e32 v15, 1.0, v38
	v_sub_f32_e32 v10, v10, v11
	v_pk_mul_f32 v[20:21], v[14:15], s[26:27]
	v_pk_mul_f32 v[14:15], v[24:25], s[26:27]
	v_exp_f32_e32 v25, v16
	v_max_f32_e32 v10, 0xc1898193, v10
	v_sub_f32_e32 v18, v18, v19
	v_sub_f32_e32 v6, v6, v7
	v_exp_f32_e32 v26, v10
	v_sub_f32_e32 v14, v14, v15
	v_max_f32_e32 v18, 0xc1898193, v18
	v_max_f32_e32 v6, 0xc1898193, v6
	v_med3_f32 v14, v14, s71, v223
	v_mov_b32_e32 v30, v187
	v_mov_b32_e32 v23, v32
	v_add_f32_e32 v13, 1.0, v34
	v_add_f32_e32 v43, 1.0, v39
	v_exp_f32_e32 v24, v18
	v_sub_f32_e32 v20, v20, v21
	v_exp_f32_e32 v28, v6
	v_mul_f32_e32 v10, v10, v14
	v_add_f32_e32 v14, 1.0, v25
	v_pk_mul_f32 v[8:9], v[30:31], s[24:25]
	v_pk_mul_f32 v[4:5], v[22:23], s[24:25]
	v_pk_mul_f32 v[22:23], v[12:13], s[26:27]
	v_pk_mul_f32 v[12:13], v[42:43], s[26:27]
	v_med3_f32 v20, v20, s71, v223
	v_rcp_f32_e32 v14, v14
	v_sub_f32_e32 v8, v8, v9
	v_sub_f32_e32 v12, v12, v13
	v_mul_f32_e32 v16, v16, v20
	v_add_f32_e32 v20, 1.0, v26
	v_max_f32_e32 v8, 0xc1898193, v8
	v_med3_f32 v12, v12, s71, v223
	v_rcp_f32_e32 v20, v20
	v_exp_f32_e32 v27, v8
	v_mul_f32_e32 v8, v8, v12
	v_add_f32_e32 v12, 1.0, v24
	v_add_f32_e32 v24, 1.0, v28
	v_mul_f32_e32 v14, v14, v16
	v_rcp_f32_e32 v16, v24
	v_add_f32_e32 v25, 1.0, v36
	v_mov_b32_e32 v24, v184
	v_sub_f32_e32 v22, v22, v23
	v_pk_mul_f32 v[24:25], v[24:25], s[26:27]
	v_sub_f32_e32 v4, v4, v5
	v_med3_f32 v22, v22, s71, v223
	v_mul_f32_e32 v10, v20, v10
	v_sub_f32_e32 v20, v24, v25
	v_max_f32_e32 v4, 0xc1898193, v4
	v_mul_f32_e32 v18, v18, v22
	v_add_f32_e32 v22, 1.0, v27
	v_med3_f32 v20, v20, s71, v223
	v_add_f32_e32 v27, 1.0, v40
	v_mov_b32_e32 v26, v180
	v_exp_f32_e32 v30, v4
	v_rcp_f32_e32 v12, v12
	v_mul_f32_e32 v6, v6, v20
	v_pk_mul_f32 v[26:27], v[26:27], s[26:27]
	v_rcp_f32_e32 v22, v22
	v_mul_f32_e32 v6, v16, v6
	v_sub_f32_e32 v16, v26, v27
	v_mov_b32_e32 v28, v193
	v_med3_f32 v16, v16, s71, v223
	v_pk_mul_f32 v[28:29], v[28:29], s[24:25]
	v_mul_f32_e32 v4, v4, v16
	v_sub_f32_e32 v16, v28, v29
	v_mov_b32_e32 v32, v189
	v_mul_f32_e32 v12, v12, v18
	v_add_f32_e32 v18, 1.0, v30
	v_max_f32_e32 v16, 0xc1898193, v16
	v_pk_mul_f32 v[30:31], v[32:33], s[24:25]
	v_mul_f32_e32 v8, v22, v8
	v_rcp_f32_e32 v18, v18
	v_sub_f32_e32 v20, v30, v31
	v_exp_f32_e32 v22, v16
	v_max_f32_e32 v20, 0xc1898193, v20
	v_exp_f32_e32 v24, v20
	v_mul_f32_e32 v4, v18, v4
	v_add_f32_e32 v18, 1.0, v22
	v_add_f32_e32 v33, 1.0, v37
	v_mov_b32_e32 v32, v185
	v_rcp_f32_e32 v18, v18
	v_pk_mul_f32 v[32:33], v[32:33], s[26:27]
	v_mov_b32_e32 v36, v199
	v_add_f32_e32 v22, 1.0, v24
	v_sub_f32_e32 v24, v32, v33
	v_cvt_pk_fp8_f32 v36, v12, v10
	v_med3_f32 v24, v24, s71, v223
	v_mul_f32_e32 v16, v16, v24
	v_mul_f32_e32 v16, v18, v16
	v_add_f32_e32 v35, 1.0, v41
	v_mov_b32_e32 v34, v181
	v_cvt_pk_fp8_f32 v36, v6, v16 op_sel:[0,0,1]
	v_fma_f32 v6, v174, s24, -v19
	v_rcp_f32_e32 v22, v22
	v_pk_mul_f32 v[34:35], v[34:35], s[26:27]
	v_mov_b32_e32 v37, v199
	v_max_f32_e32 v6, 0xc1898193, v6
	v_sub_f32_e32 v18, v34, v35
	v_cvt_pk_fp8_f32 v37, v14, v8
	v_exp_f32_e32 v12, v6
	v_med3_f32 v10, v18, s71, v223
	v_mul_f32_e32 v10, v20, v10
	v_mul_f32_e32 v10, v22, v10
	v_cvt_pk_fp8_f32 v37, v4, v10 op_sel:[0,0,1]
	v_add_f32_e32 v4, 1.0, v12
	v_rcp_f32_e32 v4, v4
	v_fma_f32 v8, v170, s24, -v17
	v_fma_f32 v12, v166, s26, -v23
	v_max_f32_e32 v8, 0xc1898193, v8
	v_med3_f32 v12, v12, s71, v223
	v_exp_f32_e32 v14, v8
	v_mul_f32_e32 v6, v6, v12
	v_mul_f32_e32 v4, v4, v6
	v_fma_f32 v6, v162, s26, -v21
	v_med3_f32 v6, v6, s71, v223
	v_mul_f32_e32 v6, v8, v6
	v_fma_f32 v8, v175, s24, -v11
	v_add_f32_e32 v10, 1.0, v14
	v_max_f32_e32 v8, 0xc1898193, v8
	v_rcp_f32_e32 v10, v10
	v_fma_f32 v12, v171, s24, -v9
	v_exp_f32_e32 v14, v8
	v_max_f32_e32 v12, 0xc1898193, v12
	v_exp_f32_e32 v16, v12
	v_mul_f32_e32 v6, v10, v6
	v_add_f32_e32 v10, 1.0, v14
	v_rcp_f32_e32 v10, v10
	v_add_f32_e32 v14, 1.0, v16
	v_fma_f32 v16, v167, s26, -v15
	v_med3_f32 v16, v16, s71, v223
	v_mul_f32_e32 v8, v8, v16
	v_mul_f32_e32 v8, v10, v8
	v_fma_f32 v10, v163, s26, -v13
	v_med3_f32 v10, v10, s71, v223
	v_mul_f32_e32 v10, v12, v10
	v_fma_f32 v12, v176, s24, -v7
	v_max_f32_e32 v12, 0xc1898193, v12
	v_rcp_f32_e32 v14, v14
	v_fma_f32 v16, v172, s24, -v5
	v_exp_f32_e32 v18, v12
	v_max_f32_e32 v16, 0xc1898193, v16
	v_exp_f32_e32 v20, v16
	v_mul_f32_e32 v10, v14, v10
	v_add_f32_e32 v14, 1.0, v18
	v_rcp_f32_e32 v14, v14
	v_add_f32_e32 v18, 1.0, v20
	v_fma_f32 v20, v168, s26, -v25
	v_med3_f32 v20, v20, s71, v223
	v_mul_f32_e32 v12, v12, v20
	v_mul_f32_e32 v12, v14, v12
	v_fma_f32 v14, v164, s26, -v27
	v_med3_f32 v14, v14, s71, v223
	v_mul_f32_e32 v14, v16, v14
	v_fma_f32 v16, v177, s24, -v29
	v_max_f32_e32 v16, 0xc1898193, v16
	v_rcp_f32_e32 v18, v18
	v_fma_f32 v20, v173, s24, -v31
	v_exp_f32_e32 v22, v16
	v_max_f32_e32 v20, 0xc1898193, v20
	v_exp_f32_e32 v24, v20
	v_mul_f32_e32 v14, v18, v14
	v_add_f32_e32 v18, 1.0, v22
	v_rcp_f32_e32 v18, v18
	v_add_f32_e32 v22, 1.0, v24
	v_fma_f32 v24, v169, s26, -v33
	v_med3_f32 v24, v24, s71, v223
	v_rcp_f32_e32 v22, v22
	v_mul_f32_e32 v16, v16, v24
	v_mov_b32_e32 v39, v199
	v_mul_f32_e32 v16, v18, v16
	v_fma_f32 v18, v165, s26, -v35
	v_cvt_pk_fp8_f32 v39, v6, v10
	v_med3_f32 v18, v18, s71, v223
	v_mov_b32_e32 v38, v199
	v_cvt_pk_fp8_f32 v38, v4, v8
	v_mul_f32_e32 v4, v20, v18
	v_mul_f32_e32 v4, v22, v4
	v_cvt_pk_fp8_f32 v39, v14, v4 op_sel:[0,0,1]
	v_fma_f32 v4, v158, s24, -v19
	v_max_f32_e32 v4, 0xc1898193, v4
	v_exp_f32_e32 v8, v4
	v_cvt_pk_fp8_f32 v38, v12, v16 op_sel:[0,0,1]
	v_fma_f32 v6, v154, s24, -v17
	v_fma_f32 v12, v150, s26, -v23
	v_add_f32_e32 v8, 1.0, v8
	v_rcp_f32_e32 v8, v8
	v_max_f32_e32 v6, 0xc1898193, v6
	v_med3_f32 v12, v12, s71, v223
	v_exp_f32_e32 v10, v6
	v_mul_f32_e32 v4, v4, v12
	v_mul_f32_e32 v4, v8, v4
	v_fma_f32 v8, v146, s26, -v21
	v_med3_f32 v8, v8, s71, v223
	v_mul_f32_e32 v6, v6, v8
	v_fma_f32 v8, v159, s24, -v11
	v_add_f32_e32 v10, 1.0, v10
	v_max_f32_e32 v8, 0xc1898193, v8
	v_rcp_f32_e32 v10, v10
	v_fma_f32 v12, v155, s24, -v9
	v_exp_f32_e32 v14, v8
	v_max_f32_e32 v12, 0xc1898193, v12
	v_exp_f32_e32 v16, v12
	v_mul_f32_e32 v6, v10, v6
	v_add_f32_e32 v10, 1.0, v14
	v_rcp_f32_e32 v10, v10
	v_add_f32_e32 v14, 1.0, v16
	v_fma_f32 v16, v151, s26, -v15
	v_med3_f32 v16, v16, s71, v223
	v_mul_f32_e32 v8, v8, v16
	v_mul_f32_e32 v8, v10, v8
	v_fma_f32 v10, v147, s26, -v13
	v_med3_f32 v10, v10, s71, v223
	v_mul_f32_e32 v10, v12, v10
	v_fma_f32 v12, v160, s24, -v7
	v_max_f32_e32 v12, 0xc1898193, v12
	v_rcp_f32_e32 v14, v14
	v_fma_f32 v16, v156, s24, -v5
	v_exp_f32_e32 v18, v12
	v_max_f32_e32 v16, 0xc1898193, v16
	v_exp_f32_e32 v20, v16
	v_mul_f32_e32 v10, v14, v10
	v_add_f32_e32 v14, 1.0, v18
	v_rcp_f32_e32 v14, v14
	v_add_f32_e32 v18, 1.0, v20
	v_fma_f32 v20, v152, s26, -v25
	v_med3_f32 v20, v20, s71, v223
	v_mul_f32_e32 v12, v12, v20
	v_mul_f32_e32 v12, v14, v12
	v_fma_f32 v14, v148, s26, -v27
	v_med3_f32 v14, v14, s71, v223
	v_mul_f32_e32 v14, v16, v14
	v_fma_f32 v16, v161, s24, -v29
	v_max_f32_e32 v16, 0xc1898193, v16
	v_rcp_f32_e32 v18, v18
	v_fma_f32 v20, v157, s24, -v31
	v_exp_f32_e32 v22, v16
	v_max_f32_e32 v20, 0xc1898193, v20
	v_exp_f32_e32 v24, v20
	v_mul_f32_e32 v14, v18, v14
	v_add_f32_e32 v18, 1.0, v22
	v_permlane16_swap_b32_e32 v36, v38
	v_permlane16_swap_b32_e32 v37, v39
	v_rcp_f32_e32 v18, v18
	global_store_dwordx4 v[2:3], v[36:39], off sc1
	v_add_f32_e32 v22, 1.0, v24
	v_fma_f32 v24, v153, s26, -v33
	v_mov_b32_e32 v36, v199
	v_mov_b32_e32 v37, v199
	v_med3_f32 v24, v24, s71, v223
	v_cvt_pk_fp8_f32 v36, v4, v8
	v_cvt_pk_fp8_f32 v37, v6, v10
	v_fma_f32 v6, v142, s24, -v19
	v_rcp_f32_e32 v22, v22
	v_mul_f32_e32 v16, v16, v24
	v_max_f32_e32 v6, 0xc1898193, v6
	v_mul_f32_e32 v16, v18, v16
	v_fma_f32 v18, v149, s26, -v35
	v_fma_f32 v8, v138, s24, -v17
	v_exp_f32_e32 v10, v6
	v_med3_f32 v4, v18, s71, v223
	v_max_f32_e32 v8, 0xc1898193, v8
	v_mul_f32_e32 v4, v20, v4
	v_cvt_pk_fp8_f32 v36, v12, v16 op_sel:[0,0,1]
	v_exp_f32_e32 v12, v8
	v_mul_f32_e32 v4, v22, v4
	v_cvt_pk_fp8_f32 v37, v14, v4 op_sel:[0,0,1]
	v_add_f32_e32 v4, 1.0, v10
	v_rcp_f32_e32 v4, v4
	v_add_f32_e32 v10, 1.0, v12
	v_fma_f32 v12, v134, s26, -v23
	v_med3_f32 v12, v12, s71, v223
	v_mul_f32_e32 v6, v6, v12
	v_mul_f32_e32 v4, v4, v6
	v_fma_f32 v6, v130, s26, -v21
	v_med3_f32 v6, v6, s71, v223
	v_mul_f32_e32 v6, v8, v6
	v_fma_f32 v8, v143, s24, -v11
	v_max_f32_e32 v8, 0xc1898193, v8
	v_rcp_f32_e32 v10, v10
	v_fma_f32 v12, v139, s24, -v9
	v_exp_f32_e32 v14, v8
	v_max_f32_e32 v12, 0xc1898193, v12
	v_exp_f32_e32 v16, v12
	v_mul_f32_e32 v6, v10, v6
	v_add_f32_e32 v10, 1.0, v14
	v_rcp_f32_e32 v10, v10
	v_add_f32_e32 v14, 1.0, v16
	v_fma_f32 v16, v135, s26, -v15
	v_med3_f32 v16, v16, s71, v223
	v_mul_f32_e32 v8, v8, v16
	v_mul_f32_e32 v8, v10, v8
	v_fma_f32 v10, v131, s26, -v13
	v_med3_f32 v10, v10, s71, v223
	v_mul_f32_e32 v10, v12, v10
	v_fma_f32 v12, v144, s24, -v7
	v_max_f32_e32 v12, 0xc1898193, v12
	v_rcp_f32_e32 v14, v14
	v_fma_f32 v16, v140, s24, -v5
	v_exp_f32_e32 v18, v12
	v_max_f32_e32 v16, 0xc1898193, v16
	v_exp_f32_e32 v20, v16
	v_mul_f32_e32 v10, v14, v10
	v_add_f32_e32 v14, 1.0, v18
	v_rcp_f32_e32 v14, v14
	v_add_f32_e32 v18, 1.0, v20
	v_fma_f32 v20, v136, s26, -v25
	v_med3_f32 v20, v20, s71, v223
	v_mul_f32_e32 v12, v12, v20
	v_mul_f32_e32 v12, v14, v12
	v_fma_f32 v14, v132, s26, -v27
	v_med3_f32 v14, v14, s71, v223
	v_mul_f32_e32 v14, v16, v14
	v_fma_f32 v16, v145, s24, -v29
	v_max_f32_e32 v16, 0xc1898193, v16
	v_rcp_f32_e32 v18, v18
	v_fma_f32 v20, v141, s24, -v31
	v_exp_f32_e32 v22, v16
	v_max_f32_e32 v20, 0xc1898193, v20
	v_exp_f32_e32 v24, v20
	v_mul_f32_e32 v14, v18, v14
	v_add_f32_e32 v18, 1.0, v22
	v_rcp_f32_e32 v18, v18
	v_add_f32_e32 v22, 1.0, v24
	v_fma_f32 v24, v137, s26, -v33
	v_med3_f32 v24, v24, s71, v223
	v_rcp_f32_e32 v22, v22
	v_mul_f32_e32 v16, v16, v24
	v_mov_b32_e32 v39, v199
	v_mul_f32_e32 v16, v18, v16
	v_fma_f32 v18, v133, s26, -v35
	v_cvt_pk_fp8_f32 v39, v6, v10
	v_med3_f32 v18, v18, s71, v223
	v_mov_b32_e32 v38, v199
	v_cvt_pk_fp8_f32 v38, v4, v8
	v_mul_f32_e32 v4, v20, v18
	v_mul_f32_e32 v4, v22, v4
	v_cvt_pk_fp8_f32 v39, v14, v4 op_sel:[0,0,1]
	v_fma_f32 v4, v126, s24, -v19
	v_max_f32_e32 v4, 0xc1898193, v4
	v_exp_f32_e32 v8, v4
	v_cvt_pk_fp8_f32 v38, v12, v16 op_sel:[0,0,1]
	v_fma_f32 v6, v122, s24, -v17
	v_fma_f32 v12, v118, s26, -v23
	v_add_f32_e32 v8, 1.0, v8
	v_rcp_f32_e32 v8, v8
	v_max_f32_e32 v6, 0xc1898193, v6
	v_med3_f32 v12, v12, s71, v223
	v_exp_f32_e32 v10, v6
	v_mul_f32_e32 v4, v4, v12
	v_mul_f32_e32 v4, v8, v4
	v_fma_f32 v8, v114, s26, -v21
	v_med3_f32 v8, v8, s71, v223
	v_mul_f32_e32 v6, v6, v8
	v_fma_f32 v8, v127, s24, -v11
	v_add_f32_e32 v10, 1.0, v10
	v_max_f32_e32 v8, 0xc1898193, v8
	v_rcp_f32_e32 v10, v10
	v_fma_f32 v12, v123, s24, -v9
	v_exp_f32_e32 v14, v8
	v_max_f32_e32 v12, 0xc1898193, v12
	v_exp_f32_e32 v16, v12
	v_mul_f32_e32 v6, v10, v6
	v_add_f32_e32 v10, 1.0, v14
	v_rcp_f32_e32 v10, v10
	v_add_f32_e32 v14, 1.0, v16
	v_fma_f32 v16, v119, s26, -v15
	v_med3_f32 v16, v16, s71, v223
	v_mul_f32_e32 v8, v8, v16
	v_mul_f32_e32 v8, v10, v8
	v_fma_f32 v10, v115, s26, -v13
	v_med3_f32 v10, v10, s71, v223
	v_mul_f32_e32 v10, v12, v10
	v_fma_f32 v12, v128, s24, -v7
	v_max_f32_e32 v12, 0xc1898193, v12
	v_rcp_f32_e32 v14, v14
	v_fma_f32 v16, v124, s24, -v5
	v_exp_f32_e32 v18, v12
	v_max_f32_e32 v16, 0xc1898193, v16
	v_exp_f32_e32 v20, v16
	v_mul_f32_e32 v10, v14, v10
	v_add_f32_e32 v14, 1.0, v18
	v_rcp_f32_e32 v14, v14
	v_add_f32_e32 v18, 1.0, v20
	v_fma_f32 v20, v120, s26, -v25
	v_med3_f32 v20, v20, s71, v223
	v_mul_f32_e32 v12, v12, v20
	v_mul_f32_e32 v12, v14, v12
	v_fma_f32 v14, v116, s26, -v27
	v_med3_f32 v14, v14, s71, v223
	v_mul_f32_e32 v14, v16, v14
	v_fma_f32 v16, v129, s24, -v29
	v_max_f32_e32 v16, 0xc1898193, v16
	v_rcp_f32_e32 v18, v18
	v_fma_f32 v20, v125, s24, -v31
	v_exp_f32_e32 v22, v16
	v_max_f32_e32 v20, 0xc1898193, v20
	v_exp_f32_e32 v24, v20
	v_add_co_u32_e32 v40, vcc, s2, v2
	v_mul_f32_e32 v14, v18, v14
	v_add_f32_e32 v18, 1.0, v22
	v_permlane16_swap_b32_e32 v36, v38
	v_permlane16_swap_b32_e32 v37, v39
	v_addc_co_u32_e32 v41, vcc, 0, v3, vcc
	v_rcp_f32_e32 v18, v18
	global_store_dwordx4 v[40:41], v[36:39], off sc1
	v_add_f32_e32 v22, 1.0, v24
	v_fma_f32 v24, v121, s26, -v33
	v_mov_b32_e32 v36, v199
	v_mov_b32_e32 v37, v199
	v_med3_f32 v24, v24, s71, v223
	v_cvt_pk_fp8_f32 v36, v4, v8
	v_cvt_pk_fp8_f32 v37, v6, v10
	v_fma_f32 v6, v110, s24, -v19
	v_rcp_f32_e32 v22, v22
	v_mul_f32_e32 v16, v16, v24
	v_max_f32_e32 v6, 0xc1898193, v6
	v_mul_f32_e32 v16, v18, v16
	v_fma_f32 v18, v117, s26, -v35
	v_fma_f32 v8, v106, s24, -v17
	v_exp_f32_e32 v10, v6
	v_med3_f32 v4, v18, s71, v223
	v_max_f32_e32 v8, 0xc1898193, v8
	v_mul_f32_e32 v4, v20, v4
	v_cvt_pk_fp8_f32 v36, v12, v16 op_sel:[0,0,1]
	v_exp_f32_e32 v12, v8
	v_mul_f32_e32 v4, v22, v4
	v_cvt_pk_fp8_f32 v37, v14, v4 op_sel:[0,0,1]
	v_add_f32_e32 v4, 1.0, v10
	v_rcp_f32_e32 v4, v4
	v_add_f32_e32 v10, 1.0, v12
	v_fma_f32 v12, v102, s26, -v23
	v_med3_f32 v12, v12, s71, v223
	v_mul_f32_e32 v6, v6, v12
	v_mul_f32_e32 v4, v4, v6
	v_fma_f32 v6, v90, s26, -v21
	v_med3_f32 v6, v6, s71, v223
	v_mul_f32_e32 v6, v8, v6
	v_fma_f32 v8, v111, s24, -v11
	v_max_f32_e32 v8, 0xc1898193, v8
	v_rcp_f32_e32 v10, v10
	v_fma_f32 v12, v107, s24, -v9
	v_exp_f32_e32 v14, v8
	v_max_f32_e32 v12, 0xc1898193, v12
	v_exp_f32_e32 v16, v12
	v_mul_f32_e32 v6, v10, v6
	v_add_f32_e32 v10, 1.0, v14
	v_rcp_f32_e32 v10, v10
	v_add_f32_e32 v14, 1.0, v16
	v_fma_f32 v16, v103, s26, -v15
	v_med3_f32 v16, v16, s71, v223
	v_mul_f32_e32 v8, v8, v16
	v_mul_f32_e32 v8, v10, v8
	v_fma_f32 v10, v91, s26, -v13
	v_med3_f32 v10, v10, s71, v223
	v_mul_f32_e32 v10, v12, v10
	v_fma_f32 v12, v112, s24, -v7
	v_max_f32_e32 v12, 0xc1898193, v12
	v_rcp_f32_e32 v14, v14
	v_fma_f32 v16, v108, s24, -v5
	v_exp_f32_e32 v18, v12
	v_max_f32_e32 v16, 0xc1898193, v16
	v_exp_f32_e32 v20, v16
	v_mul_f32_e32 v10, v14, v10
	v_add_f32_e32 v14, 1.0, v18
	v_rcp_f32_e32 v14, v14
	v_add_f32_e32 v18, 1.0, v20
	v_fma_f32 v20, v104, s26, -v25
	v_med3_f32 v20, v20, s71, v223
	v_mul_f32_e32 v12, v12, v20
	v_mul_f32_e32 v12, v14, v12
	v_fma_f32 v14, v92, s26, -v27
	v_med3_f32 v14, v14, s71, v223
	v_mul_f32_e32 v14, v16, v14
	v_fma_f32 v16, v113, s24, -v29
	v_max_f32_e32 v16, 0xc1898193, v16
	v_rcp_f32_e32 v18, v18
	v_fma_f32 v20, v109, s24, -v31
	v_exp_f32_e32 v22, v16
	v_max_f32_e32 v20, 0xc1898193, v20
	v_exp_f32_e32 v24, v20
	v_mul_f32_e32 v14, v18, v14
	v_add_f32_e32 v18, 1.0, v22
	v_rcp_f32_e32 v18, v18
	v_add_f32_e32 v22, 1.0, v24
	v_fma_f32 v24, v105, s26, -v33
	v_med3_f32 v24, v24, s71, v223
	v_rcp_f32_e32 v22, v22
	v_mul_f32_e32 v16, v16, v24
	v_mov_b32_e32 v39, v199
	v_mul_f32_e32 v16, v18, v16
	v_fma_f32 v18, v93, s26, -v35
	v_cvt_pk_fp8_f32 v39, v6, v10
	v_med3_f32 v18, v18, s71, v223
	v_mov_b32_e32 v38, v199
	v_cvt_pk_fp8_f32 v38, v4, v8
	v_mul_f32_e32 v4, v20, v18
	v_mul_f32_e32 v4, v22, v4
	v_cvt_pk_fp8_f32 v39, v14, v4 op_sel:[0,0,1]
	v_fma_f32 v4, v86, s24, -v19
	v_max_f32_e32 v4, 0xc1898193, v4
	v_exp_f32_e32 v8, v4
	v_cvt_pk_fp8_f32 v38, v12, v16 op_sel:[0,0,1]
	v_fma_f32 v6, v82, s24, -v17
	v_fma_f32 v12, v94, s26, -v23
	v_add_f32_e32 v8, 1.0, v8
	v_rcp_f32_e32 v8, v8
	v_max_f32_e32 v6, 0xc1898193, v6
	v_med3_f32 v12, v12, s71, v223
	v_exp_f32_e32 v10, v6
	v_mul_f32_e32 v4, v4, v12
	v_mul_f32_e32 v4, v8, v4
	v_fma_f32 v8, v98, s26, -v21
	v_med3_f32 v8, v8, s71, v223
	v_mul_f32_e32 v6, v6, v8
	v_fma_f32 v8, v87, s24, -v11
	v_add_f32_e32 v10, 1.0, v10
	v_max_f32_e32 v8, 0xc1898193, v8
	v_rcp_f32_e32 v10, v10
	v_fma_f32 v12, v83, s24, -v9
	v_exp_f32_e32 v14, v8
	v_max_f32_e32 v12, 0xc1898193, v12
	v_exp_f32_e32 v16, v12
	v_mul_f32_e32 v6, v10, v6
	v_add_f32_e32 v10, 1.0, v14
	v_rcp_f32_e32 v10, v10
	v_add_f32_e32 v14, 1.0, v16
	v_fma_f32 v16, v95, s26, -v15
	v_med3_f32 v16, v16, s71, v223
	v_mul_f32_e32 v8, v8, v16
	v_mul_f32_e32 v8, v10, v8
	v_fma_f32 v10, v99, s26, -v13
	v_med3_f32 v10, v10, s71, v223
	v_mul_f32_e32 v10, v12, v10
	v_fma_f32 v12, v88, s24, -v7
	v_max_f32_e32 v12, 0xc1898193, v12
	v_rcp_f32_e32 v14, v14
	v_fma_f32 v16, v84, s24, -v5
	v_exp_f32_e32 v18, v12
	v_max_f32_e32 v16, 0xc1898193, v16
	v_exp_f32_e32 v20, v16
	v_mul_f32_e32 v10, v14, v10
	v_add_f32_e32 v14, 1.0, v18
	v_rcp_f32_e32 v14, v14
	v_add_f32_e32 v18, 1.0, v20
	v_fma_f32 v20, v96, s26, -v25
	v_med3_f32 v20, v20, s71, v223
	v_mul_f32_e32 v12, v12, v20
	v_mul_f32_e32 v12, v14, v12
	v_fma_f32 v14, v100, s26, -v27
	v_med3_f32 v14, v14, s71, v223
	v_mul_f32_e32 v14, v16, v14
	v_fma_f32 v16, v89, s24, -v29
	v_max_f32_e32 v16, 0xc1898193, v16
	v_rcp_f32_e32 v18, v18
	v_fma_f32 v20, v85, s24, -v31
	v_exp_f32_e32 v22, v16
	v_max_f32_e32 v20, 0xc1898193, v20
	v_exp_f32_e32 v24, v20
	s_mov_b32 s2, 0x20000
	v_add_co_u32_e32 v40, vcc, s2, v2
	v_mul_f32_e32 v14, v18, v14
	v_add_f32_e32 v18, 1.0, v22
	v_permlane16_swap_b32_e32 v36, v38
	v_permlane16_swap_b32_e32 v37, v39
	v_addc_co_u32_e32 v41, vcc, 0, v3, vcc
	v_rcp_f32_e32 v18, v18
	global_store_dwordx4 v[40:41], v[36:39], off sc1
	v_add_f32_e32 v22, 1.0, v24
	v_fma_f32 v24, v97, s26, -v33
	v_mov_b32_e32 v36, v199
	v_mov_b32_e32 v37, v199
	v_med3_f32 v24, v24, s71, v223
	v_cvt_pk_fp8_f32 v36, v4, v8
	v_cvt_pk_fp8_f32 v37, v6, v10
	v_fma_f32 v6, v70, s24, -v19
	v_rcp_f32_e32 v22, v22
	v_mul_f32_e32 v16, v16, v24
	v_max_f32_e32 v6, 0xc1898193, v6
	v_mul_f32_e32 v16, v18, v16
	v_fma_f32 v18, v101, s26, -v35
	v_fma_f32 v8, v66, s24, -v17
	v_exp_f32_e32 v10, v6
	v_med3_f32 v4, v18, s71, v223
	v_max_f32_e32 v8, 0xc1898193, v8
	v_mul_f32_e32 v4, v20, v4
	v_cvt_pk_fp8_f32 v36, v12, v16 op_sel:[0,0,1]
	v_exp_f32_e32 v12, v8
	v_mul_f32_e32 v4, v22, v4
	v_cvt_pk_fp8_f32 v37, v14, v4 op_sel:[0,0,1]
	v_add_f32_e32 v4, 1.0, v10
	v_rcp_f32_e32 v4, v4
	v_add_f32_e32 v10, 1.0, v12
	v_fma_f32 v12, v74, s26, -v23
	v_med3_f32 v12, v12, s71, v223
	v_mul_f32_e32 v6, v6, v12
	v_mul_f32_e32 v4, v4, v6
	v_fma_f32 v6, v78, s26, -v21
	v_med3_f32 v6, v6, s71, v223
	v_mul_f32_e32 v6, v8, v6
	v_fma_f32 v8, v71, s24, -v11
	v_max_f32_e32 v8, 0xc1898193, v8
	v_rcp_f32_e32 v10, v10
	v_fma_f32 v9, v67, s24, -v9
	v_exp_f32_e32 v11, v8
	v_max_f32_e32 v9, 0xc1898193, v9
	v_exp_f32_e32 v12, v9
	v_mul_f32_e32 v6, v10, v6
	v_add_f32_e32 v10, 1.0, v11
	v_rcp_f32_e32 v10, v10
	v_add_f32_e32 v11, 1.0, v12
	v_fma_f32 v12, v75, s26, -v15
	v_med3_f32 v12, v12, s71, v223
	v_mul_f32_e32 v8, v8, v12
	v_mul_f32_e32 v8, v10, v8
	v_fma_f32 v10, v79, s26, -v13
	v_fma_f32 v7, v72, s24, -v7
	v_med3_f32 v10, v10, s71, v223
	v_max_f32_e32 v7, 0xc1898193, v7
	v_mul_f32_e32 v9, v9, v10
	v_fma_f32 v5, v68, s24, -v5
	v_exp_f32_e32 v10, v7
	v_max_f32_e32 v5, 0xc1898193, v5
	v_rcp_f32_e32 v11, v11
	v_exp_f32_e32 v12, v5
	v_add_f32_e32 v10, 1.0, v10
	v_rcp_f32_e32 v10, v10
	v_mul_f32_e32 v9, v11, v9
	v_add_f32_e32 v11, 1.0, v12
	v_fma_f32 v12, v76, s26, -v25
	v_med3_f32 v12, v12, s71, v223
	v_mul_f32_e32 v7, v7, v12
	v_mul_f32_e32 v7, v10, v7
	v_fma_f32 v10, v80, s26, -v27
	v_med3_f32 v10, v10, s71, v223
	v_mul_f32_e32 v5, v5, v10
	v_fma_f32 v10, v73, s24, -v29
	v_max_f32_e32 v10, 0xc1898193, v10
	v_rcp_f32_e32 v11, v11
	v_fma_f32 v12, v69, s24, -v31
	v_exp_f32_e32 v13, v10
	v_max_f32_e32 v12, 0xc1898193, v12
	v_exp_f32_e32 v14, v12
	v_mul_f32_e32 v5, v11, v5
	v_add_f32_e32 v11, 1.0, v13
	v_rcp_f32_e32 v11, v11
	v_add_f32_e32 v13, 1.0, v14
	v_fma_f32 v14, v77, s26, -v33
	v_med3_f32 v14, v14, s71, v223
	v_rcp_f32_e32 v13, v13
	v_mul_f32_e32 v10, v10, v14
	v_mov_b32_e32 v38, v199
	v_mov_b32_e32 v39, v199
	v_mul_f32_e32 v10, v11, v10
	v_fma_f32 v11, v81, s26, -v35
	v_cvt_pk_fp8_f32 v38, v4, v8
	v_cvt_pk_fp8_f32 v39, v6, v9
	v_med3_f32 v11, v11, s71, v223
	v_mul_f32_e32 v4, v12, v11
	v_mul_f32_e32 v4, v13, v4
	v_cvt_pk_fp8_f32 v38, v7, v10 op_sel:[0,0,1]
	v_cvt_pk_fp8_f32 v39, v5, v4 op_sel:[0,0,1]
	v_add_co_u32_e32 v2, vcc, 0x28000, v2
	v_permlane16_swap_b32_e32 v36, v38
	s_nop 0
	v_addc_co_u32_e32 v3, vcc, 0, v3, vcc
	v_permlane16_swap_b32_e32 v37, v39
	s_and_b64 vcc, exec, s[4:5]
	s_mov_b64 s[4:5], -1
	global_store_dwordx4 v[2:3], v[36:39], off sc1
	s_cbranch_vccnz .LBB0_975
	s_andn2_b64 vcc, exec, s[16:17]
	s_cbranch_vccnz .LBB0_974
	s_barrier
	s_branch .LBB0_974

.LBB0_1090:
	v_lshl_add_u32 v2, s27, 8, v215
	v_ashrrev_i32_e32 v3, 31, v2
	s_ashr_i32 s0, s84, 2
	s_lshl_b32 s1, s84, 8
	v_lshl_add_u64 v[4:5], v[2:3], 2, s[92:93]
	v_add_u32_e32 v6, 0x80, v2
	v_add_u32_e32 v8, 0x90, v2
	v_add_u32_e32 v10, 0xa0, v2
	v_add_u32_e32 v2, 0xb0, v2
	s_and_b32 s84, s1, 0x300
	v_ashrrev_i32_e32 v3, 31, v2
	s_ashr_i32 s1, s0, 31
	v_readlane_b32 s40, v239, 7
	s_waitcnt vmcnt(0)
	v_ashrrev_i32_e32 v7, 31, v6
	v_ashrrev_i32_e32 v9, 31, v8
	v_ashrrev_i32_e32 v11, 31, v10
	v_lshl_add_u64 v[2:3], v[2:3], 2, s[92:93]
	s_lshl_b64 s[0:1], s[0:1], 12
	v_readlane_b32 s50, v239, 17
	v_lshl_add_u64 v[6:7], v[6:7], 2, s[92:93]
	v_lshl_add_u64 v[8:9], v[8:9], 2, s[92:93]
	v_lshl_add_u64 v[10:11], v[10:11], 2, s[92:93]
	global_load_dword v34, v[4:5], off
	global_load_dword v36, v[4:5], off offset:64
	global_load_dword v38, v[4:5], off offset:128
	global_load_dword v26, v[4:5], off offset:192
	global_load_dword v24, v[6:7], off
	global_load_dword v22, v[8:9], off
	global_load_dword v20, v[10:11], off
	global_load_dword v18, v[2:3], off
	v_or_b32_e32 v2, s84, v217
	v_readlane_b32 s51, v239, 18
	s_add_u32 s0, s50, s0
	s_addc_u32 s1, s51, s1
	v_lshlrev_b32_e32 v2, 2, v2
	global_load_dwordx4 v[14:17], v2, s[0:1]
	global_load_dwordx4 v[10:13], v2, s[0:1] offset:16
	global_load_dwordx4 v[6:9], v2, s[0:1] offset:128
	s_nop 0
	global_load_dwordx4 v[2:5], v2, s[0:1] offset:144
	v_mov_b32_e32 v28, v199
	v_mov_b32_e32 v29, v199
	v_mov_b32_e32 v30, v199
	v_mov_b32_e32 v31, v199
	v_mov_b32_e32 v32, v199
	v_mov_b32_e32 v33, v199
	v_readlane_b32 s41, v239, 8
	v_readlane_b32 s42, v239, 9
	v_readlane_b32 s43, v239, 10
	v_readlane_b32 s44, v239, 11
	v_readlane_b32 s45, v239, 12
	v_readlane_b32 s46, v239, 13
	v_readlane_b32 s47, v239, 14
	v_readlane_b32 s48, v239, 15
	v_readlane_b32 s49, v239, 16
	v_readlane_b32 s52, v239, 19
	v_readlane_b32 s53, v239, 20
	v_readlane_b32 s54, v239, 21
	v_readlane_b32 s55, v239, 22
	s_waitcnt vmcnt(0)
	v_ashrrev_i32_e32 v35, 31, v34
	v_lshlrev_b64 v[40:41], 10, v[34:35]
	v_cmp_lt_i64_e32 vcc, -1, v[34:35]
	v_ashrrev_i32_e32 v37, 31, v36
	v_lshlrev_b64 v[42:43], 10, v[36:37]
	v_cndmask_b32_e32 v35, 0, v41, vcc
	v_cndmask_b32_e32 v34, v221, v40, vcc
	v_cmp_lt_i64_e64 s[0:1], -1, v[36:37]
	v_lshl_add_u64 v[34:35], s[94:95], 0, v[34:35]
	v_lshl_add_u64 v[34:35], v[34:35], 0, s[84:85]
	v_pk_fma_f32 v[40:41], v[190:191], s[8:9], v[14:15] op_sel_hi:[1,0,1]
	v_pk_fma_f32 v[46:47], v[186:187], s[8:9], v[10:11] op_sel_hi:[1,0,1]
	v_pk_fma_f32 v[50:51], v[174:175], s[8:9], v[6:7] op_sel_hi:[1,0,1]
	v_pk_fma_f32 v[54:55], v[170:171], s[8:9], v[2:3] op_sel_hi:[1,0,1]
	v_cvt_pk_fp8_f32 v28, v40, v41
	v_cvt_pk_fp8_f32 v29, v46, v47
	v_cvt_pk_fp8_f32 v30, v50, v51
	v_cvt_pk_fp8_f32 v31, v54, v55
	v_pk_fma_f32 v[36:37], v[192:193], s[8:9], v[16:17] op_sel_hi:[1,0,1]
	v_pk_fma_f32 v[44:45], v[188:189], s[8:9], v[12:13] op_sel_hi:[1,0,1]
	v_pk_fma_f32 v[48:49], v[176:177], s[8:9], v[8:9] op_sel_hi:[1,0,1]
	v_pk_fma_f32 v[52:53], v[172:173], s[8:9], v[4:5] op_sel_hi:[1,0,1]
	v_cvt_pk_fp8_f32 v28, v36, v37 op_sel:[0,0,1]
	v_cvt_pk_fp8_f32 v29, v44, v45 op_sel:[0,0,1]
	v_cvt_pk_fp8_f32 v30, v48, v49 op_sel:[0,0,1]
	v_cvt_pk_fp8_f32 v31, v52, v53 op_sel:[0,0,1]
	v_lshl_add_u64 v[34:35], v[34:35], 0, s[6:7]
	v_lshl_add_u64 v[34:35], v[34:35], 0, v[202:203]
	v_permlane16_swap_b32_e32 v28, v30
	v_permlane16_swap_b32_e32 v29, v31
	v_pk_fma_f32 v[58:59], v[182:183], s[8:9], v[14:15] op_sel_hi:[1,0,1]
	v_pk_fma_f32 v[62:63], v[178:179], s[8:9], v[10:11] op_sel_hi:[1,0,1]
	global_store_dwordx4 v[34:35], v[28:31], off sc1
	v_mov_b32_e32 v34, v199
	v_mov_b32_e32 v35, v199
	v_pk_fma_f32 v[28:29], v[166:167], s[8:9], v[6:7] op_sel_hi:[1,0,1]
	v_pk_fma_f32 v[30:31], v[162:163], s[8:9], v[2:3] op_sel_hi:[1,0,1]
	v_cvt_pk_fp8_f32 v32, v58, v59
	v_cvt_pk_fp8_f32 v33, v62, v63
	v_cvt_pk_fp8_f32 v34, v28, v29
	v_cvt_pk_fp8_f32 v35, v30, v31
	v_pk_fma_f32 v[56:57], v[184:185], s[8:9], v[16:17] op_sel_hi:[1,0,1]
	v_pk_fma_f32 v[60:61], v[180:181], s[8:9], v[12:13] op_sel_hi:[1,0,1]
	v_pk_fma_f32 v[28:29], v[168:169], s[8:9], v[8:9] op_sel_hi:[1,0,1]
	v_pk_fma_f32 v[30:31], v[164:165], s[8:9], v[4:5] op_sel_hi:[1,0,1]
	v_cndmask_b32_e64 v43, 0, v43, s[0:1]
	v_cndmask_b32_e64 v42, v221, v42, s[0:1]
	v_cvt_pk_fp8_f32 v32, v56, v57 op_sel:[0,0,1]
	v_cvt_pk_fp8_f32 v33, v60, v61 op_sel:[0,0,1]
	v_cvt_pk_fp8_f32 v34, v28, v29 op_sel:[0,0,1]
	v_cvt_pk_fp8_f32 v35, v30, v31 op_sel:[0,0,1]
	v_lshl_add_u64 v[40:41], s[94:95], 0, v[42:43]
	v_lshl_add_u64 v[40:41], v[40:41], 0, s[84:85]
	v_lshl_add_u64 v[40:41], v[40:41], 0, s[6:7]
	v_ashrrev_i32_e32 v39, 31, v38
	v_lshl_add_u64 v[28:29], v[40:41], 0, v[202:203]
	v_permlane16_swap_b32_e32 v32, v34
	v_permlane16_swap_b32_e32 v33, v35
	global_store_dwordx4 v[28:29], v[32:35], off sc1
	v_lshlrev_b64 v[28:29], 10, v[38:39]
	v_cmp_lt_i64_e32 vcc, -1, v[38:39]
	v_pk_fma_f32 v[30:31], v[158:159], s[8:9], v[14:15] op_sel_hi:[1,0,1]
	v_pk_fma_f32 v[34:35], v[154:155], s[8:9], v[10:11] op_sel_hi:[1,0,1]
	v_cndmask_b32_e32 v29, 0, v29, vcc
	v_cndmask_b32_e32 v28, v221, v28, vcc
	v_lshl_add_u64 v[28:29], s[94:95], 0, v[28:29]
	v_lshl_add_u64 v[28:29], v[28:29], 0, s[84:85]
	v_lshl_add_u64 v[32:33], v[28:29], 0, s[6:7]
	v_mov_b32_e32 v28, v199
	v_mov_b32_e32 v29, v199
	v_cvt_pk_fp8_f32 v28, v30, v31
	v_cvt_pk_fp8_f32 v29, v34, v35
	v_pk_fma_f32 v[30:31], v[160:161], s[8:9], v[16:17] op_sel_hi:[1,0,1]
	v_pk_fma_f32 v[34:35], v[156:157], s[8:9], v[12:13] op_sel_hi:[1,0,1]
	v_cvt_pk_fp8_f32 v28, v30, v31 op_sel:[0,0,1]
	v_cvt_pk_fp8_f32 v29, v34, v35 op_sel:[0,0,1]
	v_pk_fma_f32 v[34:35], v[150:151], s[8:9], v[6:7] op_sel_hi:[1,0,1]
	v_pk_fma_f32 v[36:37], v[146:147], s[8:9], v[2:3] op_sel_hi:[1,0,1]
	v_mov_b32_e32 v30, v199
	v_mov_b32_e32 v31, v199
	v_cvt_pk_fp8_f32 v30, v34, v35
	v_cvt_pk_fp8_f32 v31, v36, v37
	v_pk_fma_f32 v[34:35], v[152:153], s[8:9], v[8:9] op_sel_hi:[1,0,1]
	v_pk_fma_f32 v[36:37], v[148:149], s[8:9], v[4:5] op_sel_hi:[1,0,1]
	v_cvt_pk_fp8_f32 v30, v34, v35 op_sel:[0,0,1]
	v_cvt_pk_fp8_f32 v31, v36, v37 op_sel:[0,0,1]
	v_ashrrev_i32_e32 v27, 31, v26
	v_lshl_add_u64 v[32:33], v[32:33], 0, v[202:203]
	v_permlane16_swap_b32_e32 v28, v30
	v_permlane16_swap_b32_e32 v29, v31
	global_store_dwordx4 v[32:33], v[28:31], off sc1
	v_cmp_lt_i64_e32 vcc, -1, v[26:27]
	v_pk_fma_f32 v[32:33], v[138:139], s[8:9], v[10:11] op_sel_hi:[1,0,1]
	v_lshlrev_b64 v[28:29], 10, v[26:27]
	v_cndmask_b32_e32 v27, 0, v29, vcc
	v_cndmask_b32_e32 v26, v221, v28, vcc
	v_lshl_add_u64 v[26:27], s[94:95], 0, v[26:27]
	v_lshl_add_u64 v[26:27], v[26:27], 0, s[84:85]
	v_lshl_add_u64 v[30:31], v[26:27], 0, s[6:7]
	v_pk_fma_f32 v[28:29], v[142:143], s[8:9], v[14:15] op_sel_hi:[1,0,1]
	v_mov_b32_e32 v26, v199
	v_mov_b32_e32 v27, v199
	v_cvt_pk_fp8_f32 v26, v28, v29
	v_cvt_pk_fp8_f32 v27, v32, v33
	v_pk_fma_f32 v[28:29], v[144:145], s[8:9], v[16:17] op_sel_hi:[1,0,1]
	v_pk_fma_f32 v[32:33], v[140:141], s[8:9], v[12:13] op_sel_hi:[1,0,1]
	v_cvt_pk_fp8_f32 v26, v28, v29 op_sel:[0,0,1]
	v_cvt_pk_fp8_f32 v27, v32, v33 op_sel:[0,0,1]
	v_pk_fma_f32 v[32:33], v[134:135], s[8:9], v[6:7] op_sel_hi:[1,0,1]
	v_pk_fma_f32 v[34:35], v[130:131], s[8:9], v[2:3] op_sel_hi:[1,0,1]
	v_mov_b32_e32 v28, v199
	v_mov_b32_e32 v29, v199
	v_cvt_pk_fp8_f32 v28, v32, v33
	v_cvt_pk_fp8_f32 v29, v34, v35
	v_pk_fma_f32 v[32:33], v[136:137], s[8:9], v[8:9] op_sel_hi:[1,0,1]
	v_pk_fma_f32 v[34:35], v[132:133], s[8:9], v[4:5] op_sel_hi:[1,0,1]
	v_cvt_pk_fp8_f32 v28, v32, v33 op_sel:[0,0,1]
	v_cvt_pk_fp8_f32 v29, v34, v35 op_sel:[0,0,1]
	v_ashrrev_i32_e32 v25, 31, v24
	v_lshl_add_u64 v[30:31], v[30:31], 0, v[202:203]
	v_permlane16_swap_b32_e32 v26, v28
	v_permlane16_swap_b32_e32 v27, v29
	global_store_dwordx4 v[30:31], v[26:29], off sc1
	v_cmp_lt_i64_e32 vcc, -1, v[24:25]
	v_pk_fma_f32 v[30:31], v[122:123], s[8:9], v[10:11] op_sel_hi:[1,0,1]
	v_lshlrev_b64 v[26:27], 10, v[24:25]
	v_cndmask_b32_e32 v25, 0, v27, vcc
	v_cndmask_b32_e32 v24, v221, v26, vcc
	v_lshl_add_u64 v[24:25], s[94:95], 0, v[24:25]
	v_lshl_add_u64 v[24:25], v[24:25], 0, s[84:85]
	v_lshl_add_u64 v[28:29], v[24:25], 0, s[6:7]
	v_pk_fma_f32 v[26:27], v[126:127], s[8:9], v[14:15] op_sel_hi:[1,0,1]
	v_mov_b32_e32 v24, v199
	v_mov_b32_e32 v25, v199
	v_cvt_pk_fp8_f32 v24, v26, v27
	v_cvt_pk_fp8_f32 v25, v30, v31
	v_pk_fma_f32 v[26:27], v[128:129], s[8:9], v[16:17] op_sel_hi:[1,0,1]
	v_pk_fma_f32 v[30:31], v[124:125], s[8:9], v[12:13] op_sel_hi:[1,0,1]
	v_cvt_pk_fp8_f32 v24, v26, v27 op_sel:[0,0,1]
	v_cvt_pk_fp8_f32 v25, v30, v31 op_sel:[0,0,1]
	v_pk_fma_f32 v[30:31], v[118:119], s[8:9], v[6:7] op_sel_hi:[1,0,1]
	v_pk_fma_f32 v[32:33], v[114:115], s[8:9], v[2:3] op_sel_hi:[1,0,1]
	v_mov_b32_e32 v26, v199
	v_mov_b32_e32 v27, v199
	v_cvt_pk_fp8_f32 v26, v30, v31
	v_cvt_pk_fp8_f32 v27, v32, v33
	v_pk_fma_f32 v[30:31], v[120:121], s[8:9], v[8:9] op_sel_hi:[1,0,1]
	v_pk_fma_f32 v[32:33], v[116:117], s[8:9], v[4:5] op_sel_hi:[1,0,1]
	v_cvt_pk_fp8_f32 v26, v30, v31 op_sel:[0,0,1]
	v_cvt_pk_fp8_f32 v27, v32, v33 op_sel:[0,0,1]
	v_ashrrev_i32_e32 v23, 31, v22
	v_lshl_add_u64 v[28:29], v[28:29], 0, v[202:203]
	v_permlane16_swap_b32_e32 v24, v26
	v_permlane16_swap_b32_e32 v25, v27
	global_store_dwordx4 v[28:29], v[24:27], off sc1
	v_cmp_lt_i64_e32 vcc, -1, v[22:23]
	v_pk_fma_f32 v[28:29], v[98:99], s[8:9], v[10:11] op_sel_hi:[1,0,1]
	v_lshlrev_b64 v[24:25], 10, v[22:23]
	v_cndmask_b32_e32 v23, 0, v25, vcc
	v_cndmask_b32_e32 v22, v221, v24, vcc
	v_lshl_add_u64 v[22:23], s[94:95], 0, v[22:23]
	v_lshl_add_u64 v[22:23], v[22:23], 0, s[84:85]
	v_lshl_add_u64 v[26:27], v[22:23], 0, s[6:7]
	v_pk_fma_f32 v[24:25], v[106:107], s[8:9], v[14:15] op_sel_hi:[1,0,1]
	v_mov_b32_e32 v22, v199
	v_mov_b32_e32 v23, v199
	v_cvt_pk_fp8_f32 v22, v24, v25
	v_cvt_pk_fp8_f32 v23, v28, v29
	v_pk_fma_f32 v[24:25], v[108:109], s[8:9], v[16:17] op_sel_hi:[1,0,1]
	v_pk_fma_f32 v[28:29], v[100:101], s[8:9], v[12:13] op_sel_hi:[1,0,1]
	v_cvt_pk_fp8_f32 v22, v24, v25 op_sel:[0,0,1]
	v_cvt_pk_fp8_f32 v23, v28, v29 op_sel:[0,0,1]
	v_pk_fma_f32 v[28:29], v[90:91], s[8:9], v[6:7] op_sel_hi:[1,0,1]
	v_pk_fma_f32 v[30:31], v[82:83], s[8:9], v[2:3] op_sel_hi:[1,0,1]
	v_mov_b32_e32 v24, v199
	v_mov_b32_e32 v25, v199
	v_cvt_pk_fp8_f32 v24, v28, v29
	v_cvt_pk_fp8_f32 v25, v30, v31
	v_pk_fma_f32 v[28:29], v[92:93], s[8:9], v[8:9] op_sel_hi:[1,0,1]
	v_pk_fma_f32 v[30:31], v[84:85], s[8:9], v[4:5] op_sel_hi:[1,0,1]
	v_cvt_pk_fp8_f32 v24, v28, v29 op_sel:[0,0,1]
	v_cvt_pk_fp8_f32 v25, v30, v31 op_sel:[0,0,1]
	v_ashrrev_i32_e32 v21, 31, v20
	v_lshl_add_u64 v[26:27], v[26:27], 0, v[202:203]
	v_permlane16_swap_b32_e32 v22, v24
	v_permlane16_swap_b32_e32 v23, v25
	global_store_dwordx4 v[26:27], v[22:25], off sc1
	v_cmp_lt_i64_e32 vcc, -1, v[20:21]
	v_pk_fma_f32 v[26:27], v[74:75], s[8:9], v[10:11] op_sel_hi:[1,0,1]
	v_lshlrev_b64 v[22:23], 10, v[20:21]
	v_cndmask_b32_e32 v21, 0, v23, vcc
	v_cndmask_b32_e32 v20, v221, v22, vcc
	v_lshl_add_u64 v[20:21], s[94:95], 0, v[20:21]
	v_lshl_add_u64 v[20:21], v[20:21], 0, s[84:85]
	v_lshl_add_u64 v[24:25], v[20:21], 0, s[6:7]
	v_pk_fma_f32 v[22:23], v[78:79], s[8:9], v[14:15] op_sel_hi:[1,0,1]
	v_mov_b32_e32 v20, v199
	v_mov_b32_e32 v21, v199
	v_cvt_pk_fp8_f32 v20, v22, v23
	v_cvt_pk_fp8_f32 v21, v26, v27
	v_pk_fma_f32 v[22:23], v[80:81], s[8:9], v[16:17] op_sel_hi:[1,0,1]
	v_pk_fma_f32 v[26:27], v[76:77], s[8:9], v[12:13] op_sel_hi:[1,0,1]
	v_cvt_pk_fp8_f32 v20, v22, v23 op_sel:[0,0,1]
	v_cvt_pk_fp8_f32 v21, v26, v27 op_sel:[0,0,1]
	v_pk_fma_f32 v[26:27], v[102:103], s[8:9], v[6:7] op_sel_hi:[1,0,1]
	v_pk_fma_f32 v[28:29], v[110:111], s[8:9], v[2:3] op_sel_hi:[1,0,1]
	v_mov_b32_e32 v22, v199
	v_mov_b32_e32 v23, v199
	v_cvt_pk_fp8_f32 v22, v26, v27
	v_cvt_pk_fp8_f32 v23, v28, v29
	v_pk_fma_f32 v[26:27], v[104:105], s[8:9], v[8:9] op_sel_hi:[1,0,1]
	v_pk_fma_f32 v[28:29], v[112:113], s[8:9], v[4:5] op_sel_hi:[1,0,1]
	v_cvt_pk_fp8_f32 v22, v26, v27 op_sel:[0,0,1]
	v_cvt_pk_fp8_f32 v23, v28, v29 op_sel:[0,0,1]
	v_ashrrev_i32_e32 v19, 31, v18
	v_lshl_add_u64 v[24:25], v[24:25], 0, v[202:203]
	v_permlane16_swap_b32_e32 v20, v22
	v_permlane16_swap_b32_e32 v21, v23
	global_store_dwordx4 v[24:25], v[20:23], off sc1
	v_cmp_lt_i64_e32 vcc, -1, v[18:19]
	v_pk_fma_f32 v[12:13], v[68:69], s[8:9], v[12:13] op_sel_hi:[1,0,1]
	v_lshlrev_b64 v[20:21], 10, v[18:19]
	v_cndmask_b32_e32 v19, 0, v21, vcc
	v_cndmask_b32_e32 v18, v221, v20, vcc
	v_pk_fma_f32 v[20:21], v[66:67], s[8:9], v[10:11] op_sel_hi:[1,0,1]
	v_mov_b32_e32 v11, v199
	v_cvt_pk_fp8_f32 v11, v20, v21
	v_pk_fma_f32 v[14:15], v[70:71], s[8:9], v[14:15] op_sel_hi:[1,0,1]
	v_mov_b32_e32 v10, v199
	v_pk_fma_f32 v[6:7], v[86:87], s[8:9], v[6:7] op_sel_hi:[1,0,1]
	v_cvt_pk_fp8_f32 v11, v12, v13 op_sel:[0,0,1]
	v_pk_fma_f32 v[2:3], v[94:95], s[8:9], v[2:3] op_sel_hi:[1,0,1]
	v_mov_b32_e32 v12, v199
	v_mov_b32_e32 v13, v199
	v_cvt_pk_fp8_f32 v10, v14, v15
	v_cvt_pk_fp8_f32 v12, v6, v7
	v_cvt_pk_fp8_f32 v13, v2, v3
	v_pk_fma_f32 v[14:15], v[72:73], s[8:9], v[16:17] op_sel_hi:[1,0,1]
	v_pk_fma_f32 v[2:3], v[88:89], s[8:9], v[8:9] op_sel_hi:[1,0,1]
	v_pk_fma_f32 v[4:5], v[96:97], s[8:9], v[4:5] op_sel_hi:[1,0,1]
	v_cvt_pk_fp8_f32 v10, v14, v15 op_sel:[0,0,1]
	v_cvt_pk_fp8_f32 v12, v2, v3 op_sel:[0,0,1]
	v_cvt_pk_fp8_f32 v13, v4, v5 op_sel:[0,0,1]
	v_lshl_add_u64 v[18:19], s[94:95], 0, v[18:19]
	v_lshl_add_u64 v[18:19], v[18:19], 0, s[84:85]
	v_lshl_add_u64 v[18:19], v[18:19], 0, s[6:7]
	v_lshl_add_u64 v[2:3], v[18:19], 0, v[202:203]
	v_permlane16_swap_b32_e32 v10, v12
	v_permlane16_swap_b32_e32 v11, v13
	s_and_b64 vcc, exec, s[2:3]
	s_mov_b64 s[0:1], -1
	global_store_dwordx4 v[2:3], v[10:13], off sc1
	s_cbranch_vccnz .LBB0_1076
	s_andn2_b64 vcc, exec, s[90:91]
	s_cbranch_vccnz .LBB0_1075
	s_barrier
	s_branch .LBB0_1075
